# adds: gdn triangular solve readlanes software-pipelined through 4 SGPRs (no s_nop)
# speedup vs baseline: 1.0163x; 1.0163x over previous
; #define LAS __attribute__((address_space(3)))
; __device__ __forceinline__ int otid() { int t = threadIdx.x; asm volatile("" : "+v"(t)); return t; }
; __device__ __forceinline__ void ph_gdn_prep(const Params& p, LAS unsigned char* lds) {
;     ...
;         { const int lane = otid() & 63; const int h = wid; float g = gg[(t0 + lane) * 8 + h]; const float bt = gb[(t0 + lane) * 8 + h];
;             g = wave_scan(g);
;             Gs[h * 64 + lane] = g; Bs[h * 64 + lane] = bt;
;             ((float*)(gd + GD_GOFF))[((size_t)(b * 8 + h) * 256 + n) * 64 + lane] = g; }
;         for (int kh = 0; kh < 4; ++kh) {
;             const int tidA = otid(), jrow = tidA >> 3, part = tidA & 7, m16 = tidA & 15, q4 = (tidA >> 4) & 3;
;             { const bf16_t* src = qkvc + (t0 + jrow) * DM + 512 + kh * 128 + part * 16;
;                 const u32x4 a = *(const u32x4*)src, c = *(const u32x4*)(src + 8);
;                 *(LAS u32x4*)(KS + img256(jrow, part * 16)) = a; *(LAS u32x4*)(KS + img256(jrow, part * 16 + 8)) = c; }
;             __syncthreads();
;             { const int it = wid >> 1;
; #pragma unroll
;                 for (int jj = 0; jj < 2; ++jj) { const int jt = (wid & 1) * 2 + jj; f32x4 acc = (f32x4){0.f, 0.f, 0.f, 0.f};
; #pragma unroll
;                     for (int s = 0; s < 4; ++s) acc = __builtin_amdgcn_mfma_f32_16x16x32_bf16(frag256(KS, 16 * it + m16, 4 * s + q4), frag256(KS, 16 * jt + m16, 4 * s + q4), acc, 0, 0, 0);
; #pragma unroll
;                     for (int r = 0; r < 4; ++r) KK[kh * 64 * 68 + (16 * it + 4 * q4 + r) * 68 + 16 * jt + m16] = acc[r]; } }
;             __syncthreads();
;         }
.LBB0_222:
	s_ashr_i32 s56, s52, 8
	s_and_b32 s70, s52, 0xff
	s_ashr_i32 s57, s56, 31
	s_lshl_b64 s[58:59], s[56:57], 14
	s_lshl_b32 s0, s70, 6
	v_mov_b32_e32 v2, v0
	s_or_b32 s58, s58, s0
	v_mov_b32_e32 v3, s59
	v_and_b32_e32 v6, 63, v2
	v_or_b32_e32 v2, s58, v6
	v_lshl_add_u64 v[2:3], v[2:3], 3, s[28:29]
	v_lshlrev_b64 v[2:3], 2, v[2:3]
	v_lshl_add_u64 v[4:5], s[30:31], 0, v[2:3]
	global_load_dword v4, v[4:5], off
	v_lshl_add_u64 v[2:3], s[34:35], 0, v[2:3]
	global_load_dword v2, v[2:3], off
	s_lshl_b64 s[0:1], s[58:59], 12
	s_sub_u32 s0, 0, s0
	s_subb_u32 s1, 0, s1
	s_add_u32 s60, s50, s0
	s_addc_u32 s61, s51, s1
	s_lshl_b32 s71, s56, 3
	s_add_i32 s0, s71, s28
	s_ashr_i32 s1, s0, 31
	s_lshl_b64 s[0:1], s[0:1], 16
	v_readlane_b32 s2, v240, 8
	s_add_u32 s0, s2, s0
	v_readlane_b32 s2, v240, 10
	s_addc_u32 s1, s2, s1
	s_lshl_b32 s2, s70, 8
	s_add_u32 s0, s0, s2
	s_addc_u32 s1, s1, 0
	s_add_i32 s53, 0, 0x12000
	v_mov_b32_e32 v29, s75
	v_readlane_b32 s2, v240, 12
	s_mul_i32 s10, s70, 0xa000
	s_mov_b64 s[54:55], 0
	v_readlane_b32 s76, v240, 20
	v_readlane_b32 s78, v240, 19
	s_mov_b32 s79, 0
	s_mov_b32 s42, 0
	s_waitcnt vmcnt(1)
	v_add_f32_dpp v3, v4, v4 row_shr:1 row_mask:0xf bank_mask:0xf bound_ctrl:1
	s_nop 1
	v_add_f32_dpp v3, v3, v3 row_shr:2 row_mask:0xf bank_mask:0xf bound_ctrl:1
	v_mov_b32_e32 v4, v123
	s_nop 0
	v_add_f32_dpp v3, v3, v3 row_shr:4 row_mask:0xf bank_mask:0xf bound_ctrl:1
	s_nop 1
	v_add_f32_dpp v3, v3, v3 row_shr:8 row_mask:0xf bank_mask:0xf bound_ctrl:1
	s_nop 1
	v_mov_b32_dpp v4, v3 row_bcast:15 row_mask:0xa bank_mask:0xf
	v_add_f32_e32 v3, v3, v4
	v_mov_b32_e32 v4, v123
	s_nop 1
	v_mov_b32_dpp v4, v3 row_bcast:31 row_mask:0xc bank_mask:0xf
	v_add_f32_e32 v3, v3, v4
	v_or_b32_e32 v4, s69, v6
	v_lshl_add_u32 v4, v4, 2, 0
	s_waitcnt vmcnt(0)
	ds_write2st64_b32 v4, v3, v2 offset1:8
	v_lshlrev_b32_e32 v2, 2, v6
	v_mov_b32_e32 v4, v0
	global_store_dword v2, v3, s[0:1]
	v_readlane_b32 s0, v240, 11
	v_ashrrev_i32_e32 v10, 3, v4
	v_ashrrev_i32_e32 v11, 31, v10
	v_and_b32_e32 v14, 15, v4
	v_lshrrev_b32_e32 v12, 4, v4
	v_bfe_u32 v15, v4, 4, 2
	v_lshl_add_u64 v[2:3], s[58:59], 0, v[10:11]
	v_lshlrev_b32_e32 v4, 4, v4
	v_lshlrev_b64 v[2:3], 12, v[2:3]
	v_and_b32_e32 v11, 0x70, v4
	v_lshl_add_u64 v[2:3], s[60:61], 0, v[2:3]
	v_lshlrev_b32_e32 v122, 1, v11
	v_lshl_add_u64 v[6:7], v[2:3], 0, v[122:123]
	global_load_dwordx4 v[2:5], v[6:7], off offset:1040
	s_nop 0
	global_load_dwordx4 v[6:9], v[6:7], off offset:1024
	v_lshrrev_b32_e32 v11, 3, v11
	v_lshlrev_b32_e32 v13, 8, v10
	v_and_b32_e32 v16, 15, v10
	v_bitop3_b32 v10, v11, v10, 15 bitop3:0x78
	v_lshlrev_b32_e32 v10, 4, v10
	v_add3_u32 v10, s53, v10, v13
	v_lshl_add_u32 v19, v14, 2, 0
	v_lshl_or_b32 v18, v15, 2, s74
	s_waitcnt vmcnt(0)
	ds_write_b128 v10, v[6:9]
	v_bitop3_b32 v6, v11, v16, 1 bitop3:0x36
	v_lshlrev_b32_e32 v6, 4, v6
	v_add3_u32 v6, s53, v6, v13
	ds_write_b128 v6, v[2:5]
	v_lshlrev_b32_e32 v2, 8, v14
	v_add_u32_e32 v16, s73, v2
	v_add_u32_e32 v17, s53, v2
	v_bitop3_b32 v2, v12, v14, 3 bitop3:0x6c
	v_lshlrev_b32_e32 v21, 4, v2
	v_add_u32_e32 v22, v16, v21
	s_waitcnt lgkmcnt(0)
	s_barrier
	ds_read_b128 v[2:5], v22
	v_add_u32_e32 v20, s87, v17
	v_add_u32_e32 v6, v20, v21
	ds_read_b128 v[6:9], v6
	v_add_u32_e32 v17, s89, v17
	s_waitcnt lgkmcnt(0)
	v_mfma_f32_16x16x32_bf16 v[2:5], v[2:5], v[6:9], 0
	v_bitop3_b32 v6, v15, v14, 4 bitop3:0x36
	v_lshlrev_b32_e32 v23, 4, v6
	v_add_u32_e32 v24, v16, v23
	ds_read_b128 v[6:9], v24
	v_add_u32_e32 v10, v20, v23
	ds_read_b128 v[10:13], v10
	s_waitcnt lgkmcnt(0)
	v_mfma_f32_16x16x32_bf16 v[2:5], v[6:9], v[10:13], v[2:5]
	v_bitop3_b32 v6, v15, v14, 8 bitop3:0x36
	v_lshlrev_b32_e32 v25, 4, v6
	v_add_u32_e32 v26, v16, v25
	ds_read_b128 v[6:9], v26
	v_add_u32_e32 v10, v20, v25
	ds_read_b128 v[10:13], v10
	s_waitcnt lgkmcnt(0)
	v_mfma_f32_16x16x32_bf16 v[2:5], v[6:9], v[10:13], v[2:5]
	v_bitop3_b32 v6, v15, v14, 12 bitop3:0x36
	v_lshlrev_b32_e32 v14, 4, v6
	v_add_u32_e32 v15, v16, v14
	ds_read_b128 v[6:9], v15
	v_add_u32_e32 v10, v20, v14
	ds_read_b128 v[10:13], v10
	v_mul_lo_u32 v16, v18, s7
	s_waitcnt lgkmcnt(0)
	v_mfma_f32_16x16x32_bf16 v[2:5], v[6:9], v[10:13], v[2:5]
	v_add3_u32 v6, v19, s88, v16
	v_add_u32_e32 v6, 0x1000, v6
	s_nop 5
	ds_write2_b32 v6, v2, v3 offset1:68
	ds_write2_b32 v6, v4, v5 offset0:136 offset1:204
	ds_read_b128 v[2:5], v22
	v_add_u32_e32 v6, v17, v21
	ds_read_b128 v[6:9], v6
	v_add_u32_e32 v10, v17, v23
	ds_read_b128 v[10:13], v10
	s_waitcnt lgkmcnt(1)
	v_mfma_f32_16x16x32_bf16 v[2:5], v[2:5], v[6:9], 0
	ds_read_b128 v[6:9], v24
	s_waitcnt lgkmcnt(0)
	v_mfma_f32_16x16x32_bf16 v[2:5], v[6:9], v[10:13], v[2:5]
	ds_read_b128 v[6:9], v26
	v_add_u32_e32 v10, v17, v25
	ds_read_b128 v[10:13], v10
	s_waitcnt lgkmcnt(0)
	v_mfma_f32_16x16x32_bf16 v[2:5], v[6:9], v[10:13], v[2:5]
	ds_read_b128 v[6:9], v15
	v_add_u32_e32 v10, v17, v14
	ds_read_b128 v[10:13], v10
	s_waitcnt lgkmcnt(0)
	v_mfma_f32_16x16x32_bf16 v[2:5], v[6:9], v[10:13], v[2:5]
	v_add3_u32 v6, v19, s90, v16
	v_add_u32_e32 v6, 0x1000, v6
	s_nop 5
	ds_write2_b32 v6, v2, v3 offset1:68
	ds_write2_b32 v6, v4, v5 offset0:136 offset1:204
	v_mov_b32_e32 v4, v0
	s_waitcnt lgkmcnt(0)
	s_barrier
; #define LAS __attribute__((address_space(3)))
; __device__ __forceinline__ int otid() { int t = threadIdx.x; asm volatile("" : "+v"(t)); return t; }
; __device__ __forceinline__ void ph_gdn_prep(const Params& p, LAS unsigned char* lds) {
;     ...
;             const int tidA = otid(), jrow = tidA >> 3, part = tidA & 7, m16 = tidA & 15, q4 = (tidA >> 4) & 3;
;             { const bf16_t* src = qkvc + (t0 + jrow) * DM + 512 + kh * 128 + part * 16;
;                 const u32x4 a = *(const u32x4*)src, c = *(const u32x4*)(src + 8);
;                 *(LAS u32x4*)(KS + img256(jrow, part * 16)) = a; *(LAS u32x4*)(KS + img256(jrow, part * 16 + 8)) = c; }
;             __syncthreads();
;             { const int it = wid >> 1;
; #pragma unroll
;                 for (int jj = 0; jj < 2; ++jj) { const int jt = (wid & 1) * 2 + jj; f32x4 acc = (f32x4){0.f, 0.f, 0.f, 0.f};
; #pragma unroll
;                     for (int s = 0; s < 4; ++s) acc = __builtin_amdgcn_mfma_f32_16x16x32_bf16(frag256(KS, 16 * it + m16, 4 * s + q4), frag256(KS, 16 * jt + m16, 4 * s + q4), acc, 0, 0, 0);
; #pragma unroll
;                     for (int r = 0; r < 4; ++r) KK[kh * 64 * 68 + (16 * it + 4 * q4 + r) * 68 + 16 * jt + m16] = acc[r]; } }
;             __syncthreads();
	s_nop 0
	v_ashrrev_i32_e32 v10, 3, v4
	v_ashrrev_i32_e32 v11, 31, v10
	v_and_b32_e32 v14, 15, v4
	v_lshrrev_b32_e32 v12, 4, v4
	v_bfe_u32 v15, v4, 4, 2
	v_lshl_add_u64 v[2:3], s[58:59], 0, v[10:11]
	v_lshlrev_b32_e32 v4, 4, v4
	v_lshlrev_b64 v[2:3], 12, v[2:3]
	v_and_b32_e32 v11, 0x70, v4
	v_lshl_add_u64 v[2:3], s[60:61], 0, v[2:3]
	v_lshlrev_b32_e32 v122, 1, v11
	v_lshl_add_u64 v[6:7], v[2:3], 0, v[122:123]
	global_load_dwordx4 v[2:5], v[6:7], off offset:1296
	s_nop 0
	global_load_dwordx4 v[6:9], v[6:7], off offset:1280
	v_lshrrev_b32_e32 v11, 3, v11
	v_lshlrev_b32_e32 v13, 8, v10
	v_and_b32_e32 v16, 15, v10
	v_bitop3_b32 v10, v11, v10, 15 bitop3:0x78
	v_lshlrev_b32_e32 v10, 4, v10
	v_add3_u32 v10, s53, v10, v13
	v_lshl_add_u32 v19, v14, 2, 0
	v_lshl_or_b32 v18, v15, 2, s74
	s_waitcnt vmcnt(0)
	ds_write_b128 v10, v[6:9]
	v_bitop3_b32 v6, v11, v16, 1 bitop3:0x36
	v_lshlrev_b32_e32 v6, 4, v6
	v_add3_u32 v6, s53, v6, v13
	ds_write_b128 v6, v[2:5]
	v_lshlrev_b32_e32 v2, 8, v14
	v_add_u32_e32 v16, s73, v2
	v_add_u32_e32 v17, s53, v2
	v_bitop3_b32 v2, v12, v14, 3 bitop3:0x6c
	v_lshlrev_b32_e32 v21, 4, v2
	v_add_u32_e32 v22, v16, v21
	s_waitcnt lgkmcnt(0)
	s_barrier
	ds_read_b128 v[2:5], v22
	v_add_u32_e32 v20, s87, v17
	v_add_u32_e32 v6, v20, v21
	ds_read_b128 v[6:9], v6
	v_add_u32_e32 v17, s89, v17
	s_waitcnt lgkmcnt(0)
	v_mfma_f32_16x16x32_bf16 v[2:5], v[2:5], v[6:9], 0
	v_bitop3_b32 v6, v15, v14, 4 bitop3:0x36
	v_lshlrev_b32_e32 v23, 4, v6
	v_add_u32_e32 v24, v16, v23
	ds_read_b128 v[6:9], v24
	v_add_u32_e32 v10, v20, v23
	ds_read_b128 v[10:13], v10
	s_waitcnt lgkmcnt(0)
	v_mfma_f32_16x16x32_bf16 v[2:5], v[6:9], v[10:13], v[2:5]
	v_bitop3_b32 v6, v15, v14, 8 bitop3:0x36
	v_lshlrev_b32_e32 v25, 4, v6
	v_add_u32_e32 v26, v16, v25
	ds_read_b128 v[6:9], v26
	v_add_u32_e32 v10, v20, v25
	ds_read_b128 v[10:13], v10
	s_waitcnt lgkmcnt(0)
	v_mfma_f32_16x16x32_bf16 v[2:5], v[6:9], v[10:13], v[2:5]
	v_bitop3_b32 v6, v15, v14, 12 bitop3:0x36
	v_lshlrev_b32_e32 v14, 4, v6
	v_add_u32_e32 v15, v16, v14
	ds_read_b128 v[6:9], v15
	v_add_u32_e32 v10, v20, v14
	ds_read_b128 v[10:13], v10
	v_mul_lo_u32 v16, v18, s7
	s_waitcnt lgkmcnt(0)
	v_mfma_f32_16x16x32_bf16 v[2:5], v[6:9], v[10:13], v[2:5]
	v_add3_u32 v6, v19, s88, v16
	v_add_u32_e32 v6, 0x5400, v6
	s_nop 5
	ds_write2_b32 v6, v2, v3 offset1:68
	ds_write2_b32 v6, v4, v5 offset0:136 offset1:204
	ds_read_b128 v[2:5], v22
	v_add_u32_e32 v6, v17, v21
	ds_read_b128 v[6:9], v6
	v_add_u32_e32 v10, v17, v23
	ds_read_b128 v[10:13], v10
	s_waitcnt lgkmcnt(1)
	v_mfma_f32_16x16x32_bf16 v[2:5], v[2:5], v[6:9], 0
	ds_read_b128 v[6:9], v24
	s_waitcnt lgkmcnt(0)
	v_mfma_f32_16x16x32_bf16 v[2:5], v[6:9], v[10:13], v[2:5]
	ds_read_b128 v[6:9], v26
	v_add_u32_e32 v10, v17, v25
	ds_read_b128 v[10:13], v10
	s_waitcnt lgkmcnt(0)
	v_mfma_f32_16x16x32_bf16 v[2:5], v[6:9], v[10:13], v[2:5]
	ds_read_b128 v[6:9], v15
	v_add_u32_e32 v10, v17, v14
	ds_read_b128 v[10:13], v10
	s_waitcnt lgkmcnt(0)
	v_mfma_f32_16x16x32_bf16 v[2:5], v[6:9], v[10:13], v[2:5]
	v_add3_u32 v6, v19, s90, v16
	v_add_u32_e32 v6, 0x5400, v6
	s_nop 5
	ds_write2_b32 v6, v2, v3 offset1:68
	ds_write2_b32 v6, v4, v5 offset0:136 offset1:204
	v_mov_b32_e32 v4, v0
	s_waitcnt lgkmcnt(0)
	s_barrier
	s_nop 0
	v_ashrrev_i32_e32 v10, 3, v4
	v_ashrrev_i32_e32 v11, 31, v10
	v_and_b32_e32 v14, 15, v4
	v_lshrrev_b32_e32 v12, 4, v4
	v_bfe_u32 v15, v4, 4, 2
	v_lshl_add_u64 v[2:3], s[58:59], 0, v[10:11]
	v_lshlrev_b32_e32 v4, 4, v4
	v_lshlrev_b64 v[2:3], 12, v[2:3]
	v_and_b32_e32 v11, 0x70, v4
	v_lshl_add_u64 v[2:3], s[60:61], 0, v[2:3]
	v_lshlrev_b32_e32 v122, 1, v11
	v_lshl_add_u64 v[6:7], v[2:3], 0, v[122:123]
	global_load_dwordx4 v[2:5], v[6:7], off offset:1552
	s_nop 0
	global_load_dwordx4 v[6:9], v[6:7], off offset:1536
	v_lshrrev_b32_e32 v11, 3, v11
	v_lshlrev_b32_e32 v13, 8, v10
	v_and_b32_e32 v16, 15, v10
	v_bitop3_b32 v10, v11, v10, 15 bitop3:0x78
	v_lshlrev_b32_e32 v10, 4, v10
	v_add3_u32 v10, s53, v10, v13
	v_lshl_add_u32 v19, v14, 2, 0
	v_lshl_or_b32 v18, v15, 2, s74
	s_waitcnt vmcnt(0)
	ds_write_b128 v10, v[6:9]
	v_bitop3_b32 v6, v11, v16, 1 bitop3:0x36
	v_lshlrev_b32_e32 v6, 4, v6
	v_add3_u32 v6, s53, v6, v13
	ds_write_b128 v6, v[2:5]
	v_lshlrev_b32_e32 v2, 8, v14
	v_add_u32_e32 v16, s73, v2
	v_add_u32_e32 v17, s53, v2
	v_bitop3_b32 v2, v12, v14, 3 bitop3:0x6c
	v_lshlrev_b32_e32 v21, 4, v2
	v_add_u32_e32 v22, v16, v21
	s_waitcnt lgkmcnt(0)
	s_barrier
	ds_read_b128 v[2:5], v22
	v_add_u32_e32 v20, s87, v17
	v_add_u32_e32 v6, v20, v21
	ds_read_b128 v[6:9], v6
	v_add_u32_e32 v17, s89, v17
	s_waitcnt lgkmcnt(0)
	v_mfma_f32_16x16x32_bf16 v[2:5], v[2:5], v[6:9], 0
	v_bitop3_b32 v6, v15, v14, 4 bitop3:0x36
	v_lshlrev_b32_e32 v23, 4, v6
	v_add_u32_e32 v24, v16, v23
	ds_read_b128 v[6:9], v24
	v_add_u32_e32 v10, v20, v23
	ds_read_b128 v[10:13], v10
	s_waitcnt lgkmcnt(0)
	v_mfma_f32_16x16x32_bf16 v[2:5], v[6:9], v[10:13], v[2:5]
	v_bitop3_b32 v6, v15, v14, 8 bitop3:0x36
	v_lshlrev_b32_e32 v25, 4, v6
	v_add_u32_e32 v26, v16, v25
	ds_read_b128 v[6:9], v26
	v_add_u32_e32 v10, v20, v25
	ds_read_b128 v[10:13], v10
	s_waitcnt lgkmcnt(0)
	v_mfma_f32_16x16x32_bf16 v[2:5], v[6:9], v[10:13], v[2:5]
	v_bitop3_b32 v6, v15, v14, 12 bitop3:0x36
	v_lshlrev_b32_e32 v14, 4, v6
	v_add_u32_e32 v15, v16, v14
	ds_read_b128 v[6:9], v15
	v_add_u32_e32 v10, v20, v14
	ds_read_b128 v[10:13], v10
	v_mul_lo_u32 v16, v18, s7
	s_waitcnt lgkmcnt(0)
	v_mfma_f32_16x16x32_bf16 v[2:5], v[6:9], v[10:13], v[2:5]
	v_add3_u32 v6, v19, s88, v16
	v_add_u32_e32 v6, 0x9800, v6
	s_nop 5
	ds_write2_b32 v6, v2, v3 offset1:68
	ds_write2_b32 v6, v4, v5 offset0:136 offset1:204
	ds_read_b128 v[2:5], v22
	v_add_u32_e32 v6, v17, v21
	ds_read_b128 v[6:9], v6
	v_add_u32_e32 v10, v17, v23
	ds_read_b128 v[10:13], v10
	s_waitcnt lgkmcnt(1)
	v_mfma_f32_16x16x32_bf16 v[2:5], v[2:5], v[6:9], 0
	ds_read_b128 v[6:9], v24
	s_waitcnt lgkmcnt(0)
	v_mfma_f32_16x16x32_bf16 v[2:5], v[6:9], v[10:13], v[2:5]
	ds_read_b128 v[6:9], v26
	v_add_u32_e32 v10, v17, v25
	ds_read_b128 v[10:13], v10
	s_waitcnt lgkmcnt(0)
	v_mfma_f32_16x16x32_bf16 v[2:5], v[6:9], v[10:13], v[2:5]
	ds_read_b128 v[6:9], v15
	v_add_u32_e32 v10, v17, v14
	ds_read_b128 v[10:13], v10
	s_waitcnt lgkmcnt(0)
	v_mfma_f32_16x16x32_bf16 v[2:5], v[6:9], v[10:13], v[2:5]
	v_add3_u32 v6, v19, s90, v16
	v_add_u32_e32 v6, 0x9800, v6
	s_nop 5
	ds_write2_b32 v6, v2, v3 offset1:68
	ds_write2_b32 v6, v4, v5 offset0:136 offset1:204
	v_mov_b32_e32 v4, v0
	s_waitcnt lgkmcnt(0)
	s_barrier
; #define LAS __attribute__((address_space(3)))
; __device__ __forceinline__ int otid() { int t = threadIdx.x; asm volatile("" : "+v"(t)); return t; }
; __device__ __forceinline__ void ph_gdn_prep(const Params& p, LAS unsigned char* lds) {
;     ...
;         for (int kh = 0; kh < 4; ++kh) {
;             const int tidA = otid(), jrow = tidA >> 3, part = tidA & 7, m16 = tidA & 15, q4 = (tidA >> 4) & 3;
;             { const bf16_t* src = qkvc + (t0 + jrow) * DM + 512 + kh * 128 + part * 16;
;                 const u32x4 a = *(const u32x4*)src, c = *(const u32x4*)(src + 8);
;                 *(LAS u32x4*)(KS + img256(jrow, part * 16)) = a; *(LAS u32x4*)(KS + img256(jrow, part * 16 + 8)) = c; }
;             __syncthreads();
;             { const int it = wid >> 1;
; #pragma unroll
;                 for (int jj = 0; jj < 2; ++jj) { const int jt = (wid & 1) * 2 + jj; f32x4 acc = (f32x4){0.f, 0.f, 0.f, 0.f};
; #pragma unroll
;                     for (int s = 0; s < 4; ++s) acc = __builtin_amdgcn_mfma_f32_16x16x32_bf16(frag256(KS, 16 * it + m16, 4 * s + q4), frag256(KS, 16 * jt + m16, 4 * s + q4), acc, 0, 0, 0);
; #pragma unroll
;                     for (int r = 0; r < 4; ++r) KK[kh * 64 * 68 + (16 * it + 4 * q4 + r) * 68 + 16 * jt + m16] = acc[r]; } }
;             __syncthreads();
;         }
;         float mcol[64];
;         { const int h = wid, kh = h >> 1, c = otid() & 63; const float Gc_ = Gs[h * 64 + c];
; #pragma unroll
;             for (int j = 0; j < 64; ++j) { const float kkv = KK[kh * 64 * 68 + j * 68 + c]; const float v = -Bs[h * 64 + j] * kkv * __expf(Gs[h * 64 + j] - Gc_); mcol[j] = (j > c) ? v : 0.f; } }
	s_nop 0
	v_ashrrev_i32_e32 v10, 3, v4
	v_ashrrev_i32_e32 v11, 31, v10
	v_and_b32_e32 v14, 15, v4
	v_lshrrev_b32_e32 v12, 4, v4
	v_bfe_u32 v15, v4, 4, 2
	v_lshl_add_u64 v[2:3], s[58:59], 0, v[10:11]
	v_lshlrev_b32_e32 v4, 4, v4
	v_lshlrev_b64 v[2:3], 12, v[2:3]
	v_and_b32_e32 v11, 0x70, v4
	v_lshl_add_u64 v[2:3], s[60:61], 0, v[2:3]
	v_lshlrev_b32_e32 v122, 1, v11
	v_lshl_add_u64 v[6:7], v[2:3], 0, v[122:123]
	global_load_dwordx4 v[2:5], v[6:7], off offset:1808
	s_nop 0
	global_load_dwordx4 v[6:9], v[6:7], off offset:1792
	v_lshrrev_b32_e32 v11, 3, v11
	v_lshlrev_b32_e32 v13, 8, v10
	v_and_b32_e32 v16, 15, v10
	v_bitop3_b32 v10, v11, v10, 15 bitop3:0x78
	v_lshlrev_b32_e32 v10, 4, v10
	v_add3_u32 v10, s53, v10, v13
	v_lshl_add_u32 v19, v14, 2, 0
	v_lshl_or_b32 v18, v15, 2, s74
	s_waitcnt vmcnt(0)
	ds_write_b128 v10, v[6:9]
	v_bitop3_b32 v6, v11, v16, 1 bitop3:0x36
	v_lshlrev_b32_e32 v6, 4, v6
	v_add3_u32 v6, s53, v6, v13
	ds_write_b128 v6, v[2:5]
	v_lshlrev_b32_e32 v2, 8, v14
	v_add_u32_e32 v16, s73, v2
	v_add_u32_e32 v17, s53, v2
	v_bitop3_b32 v2, v12, v14, 3 bitop3:0x6c
	v_lshlrev_b32_e32 v21, 4, v2
	v_add_u32_e32 v22, v16, v21
	s_waitcnt lgkmcnt(0)
	s_barrier
	ds_read_b128 v[2:5], v22
	v_add_u32_e32 v20, s87, v17
	v_add_u32_e32 v6, v20, v21
	ds_read_b128 v[6:9], v6
	v_add_u32_e32 v17, s89, v17
	s_waitcnt lgkmcnt(0)
	v_mfma_f32_16x16x32_bf16 v[2:5], v[2:5], v[6:9], 0
	v_bitop3_b32 v6, v15, v14, 4 bitop3:0x36
	v_lshlrev_b32_e32 v23, 4, v6
	v_add_u32_e32 v24, v16, v23
	ds_read_b128 v[6:9], v24
	v_add_u32_e32 v10, v20, v23
	ds_read_b128 v[10:13], v10
	s_waitcnt lgkmcnt(0)
	v_mfma_f32_16x16x32_bf16 v[2:5], v[6:9], v[10:13], v[2:5]
	v_bitop3_b32 v6, v15, v14, 8 bitop3:0x36
	v_lshlrev_b32_e32 v25, 4, v6
	v_add_u32_e32 v26, v16, v25
	ds_read_b128 v[6:9], v26
	v_add_u32_e32 v10, v20, v25
	ds_read_b128 v[10:13], v10
	s_waitcnt lgkmcnt(0)
	v_mfma_f32_16x16x32_bf16 v[2:5], v[6:9], v[10:13], v[2:5]
	v_bitop3_b32 v6, v15, v14, 12 bitop3:0x36
	v_lshlrev_b32_e32 v14, 4, v6
	v_add_u32_e32 v15, v16, v14
	ds_read_b128 v[6:9], v15
	v_add_u32_e32 v10, v20, v14
	ds_read_b128 v[10:13], v10
	v_mul_lo_u32 v16, v18, s7
	s_waitcnt lgkmcnt(0)
	v_mfma_f32_16x16x32_bf16 v[2:5], v[6:9], v[10:13], v[2:5]
	v_add3_u32 v6, v19, s88, v16
	v_add_u32_e32 v6, 0xdc00, v6
	s_nop 5
	ds_write2_b32 v6, v2, v3 offset1:68
	ds_write2_b32 v6, v4, v5 offset0:136 offset1:204
	ds_read_b128 v[2:5], v22
	v_add_u32_e32 v6, v17, v21
	ds_read_b128 v[6:9], v6
	v_add_u32_e32 v10, v17, v23
	ds_read_b128 v[10:13], v10
	s_waitcnt lgkmcnt(1)
	v_mfma_f32_16x16x32_bf16 v[2:5], v[2:5], v[6:9], 0
	ds_read_b128 v[6:9], v24
	s_waitcnt lgkmcnt(0)
	v_mfma_f32_16x16x32_bf16 v[2:5], v[6:9], v[10:13], v[2:5]
	ds_read_b128 v[6:9], v26
	v_add_u32_e32 v10, v17, v25
	ds_read_b128 v[10:13], v10
	s_waitcnt lgkmcnt(0)
	v_mfma_f32_16x16x32_bf16 v[2:5], v[6:9], v[10:13], v[2:5]
	ds_read_b128 v[6:9], v15
	v_add_u32_e32 v10, v17, v14
	ds_read_b128 v[10:13], v10
	s_waitcnt lgkmcnt(0)
	v_mfma_f32_16x16x32_bf16 v[2:5], v[6:9], v[10:13], v[2:5]
	v_add3_u32 v6, v19, s90, v16
	v_add_u32_e32 v6, 0xdc00, v6
	s_nop 5
	ds_write2_b32 v6, v2, v3 offset1:68
	ds_write2_b32 v6, v4, v5 offset0:136 offset1:204
	v_mov_b32_e32 v2, v0
	s_waitcnt lgkmcnt(0)
	s_barrier
	ds_read2_b32 v[6:7], v29 offset0:1 offset1:2
	v_and_b32_e32 v22, 63, v2
	v_lshlrev_b32_e32 v2, 2, v22
	v_add_u32_e32 v27, s0, v2
	v_readlane_b32 s0, v240, 21
	v_add_u32_e32 v3, s75, v2
	v_add_u32_e32 v2, 0x1000, v27
	v_mov_b32_e32 v4, s0
	ds_read_b32 v23, v3
	ds_read2_b32 v[4:5], v4 offset1:1
	ds_read2_b32 v[2:3], v2 offset0:68 offset1:136
	v_cmp_eq_u32_e32 vcc, 0, v22
	v_readlane_b32 s0, v240, 22
	v_add_u32_e32 v8, 0x2400, v27
	v_add_u32_e32 v13, 0x4c00, v27
	s_waitcnt lgkmcnt(0)
	v_mul_f32_e64 v2, v2, -v4
	v_sub_f32_e32 v4, v6, v23
	v_mul_f32_e32 v4, 0x3fb8aa3b, v4
	v_exp_f32_e32 v4, v4
	ds_read2_b32 v[70:71], v29 offset0:57 offset1:58
	ds_read2_b32 v[74:75], v29 offset0:61 offset1:62
	v_mul_f32_e32 v2, v2, v4
	v_cndmask_b32_e32 v24, 0, v2, vcc
	v_mul_f32_e64 v2, v3, -v5
	v_sub_f32_e32 v3, v7, v23
	v_mul_f32_e32 v3, 0x3fb8aa3b, v3
	v_exp_f32_e32 v3, v3
	v_cmp_gt_u32_e32 vcc, 2, v22
	v_mov_b32_e32 v4, s0
	ds_read2_b32 v[4:5], v4 offset1:1
	ds_read2_b32 v[6:7], v29 offset0:3 offset1:4
	v_mul_f32_e32 v2, v2, v3
	v_cndmask_b32_e32 v25, 0, v2, vcc
	v_add_u32_e32 v2, 0x1200, v27
	ds_read2_b32 v[2:3], v2 offset0:76 offset1:144
	v_cmp_gt_u32_e32 vcc, 3, v22
	v_readlane_b32 s0, v240, 23
	v_readlane_b32 s1, v25, 1
	s_waitcnt lgkmcnt(0)
	v_mul_f32_e64 v2, v2, -v4
	v_sub_f32_e32 v4, v6, v23
	v_mul_f32_e32 v4, 0x3fb8aa3b, v4
	v_exp_f32_e32 v4, v4
	s_nop 0
	v_mul_f32_e32 v2, v2, v4
	v_cndmask_b32_e32 v28, 0, v2, vcc
	v_mul_f32_e64 v2, v3, -v5
	v_sub_f32_e32 v3, v7, v23
	v_mul_f32_e32 v3, 0x3fb8aa3b, v3
	v_exp_f32_e32 v3, v3
	v_cmp_gt_u32_e32 vcc, 4, v22
	v_mov_b32_e32 v4, s0
	ds_read2_b32 v[4:5], v4 offset1:1
	ds_read2_b32 v[6:7], v29 offset0:5 offset1:6
	v_mul_f32_e32 v2, v2, v3
	v_cndmask_b32_e32 v26, 0, v2, vcc
	v_add_u32_e32 v2, 0x1400, v27
	ds_read2_b32 v[2:3], v2 offset0:84 offset1:152
	v_cmp_gt_u32_e32 vcc, 5, v22
	v_readlane_b32 s0, v240, 24
	s_waitcnt lgkmcnt(0)
	v_mul_f32_e64 v2, v2, -v4
	v_sub_f32_e32 v4, v6, v23
	v_mul_f32_e32 v4, 0x3fb8aa3b, v4
	v_exp_f32_e32 v4, v4
	s_nop 0
	v_mul_f32_e32 v2, v2, v4
	v_cndmask_b32_e32 v32, 0, v2, vcc
	v_mul_f32_e64 v2, v3, -v5
	v_sub_f32_e32 v3, v7, v23
	v_mul_f32_e32 v3, 0x3fb8aa3b, v3
	v_exp_f32_e32 v3, v3
	v_cmp_gt_u32_e32 vcc, 6, v22
	v_mov_b32_e32 v4, s0
	ds_read2_b32 v[4:5], v4 offset1:1
	ds_read2_b32 v[6:7], v29 offset0:7 offset1:8
	v_mul_f32_e32 v2, v2, v3
	v_cndmask_b32_e32 v31, 0, v2, vcc
	v_add_u32_e32 v2, 0x1600, v27
	ds_read2_b32 v[2:3], v2 offset0:92 offset1:160
	v_cmp_gt_u32_e32 vcc, 7, v22
	v_readlane_b32 s0, v240, 25
	s_waitcnt lgkmcnt(0)
; __device__ __forceinline__ int otid() { int t = threadIdx.x; asm volatile("" : "+v"(t)); return t; }
; __device__ __forceinline__ void ph_gdn_prep(const Params& p, LAS unsigned char* lds) {
;     ...
;         { const int h = wid, kh = h >> 1, c = otid() & 63; const float Gc_ = Gs[h * 64 + c];
; #pragma unroll
;             for (int j = 0; j < 64; ++j) { const float kkv = KK[kh * 64 * 68 + j * 68 + c]; const float v = -Bs[h * 64 + j] * kkv * __expf(Gs[h * 64 + j] - Gc_); mcol[j] = (j > c) ? v : 0.f; } }
	v_mul_f32_e64 v2, v2, -v4
	v_sub_f32_e32 v4, v6, v23
	v_mul_f32_e32 v4, 0x3fb8aa3b, v4
	v_exp_f32_e32 v4, v4
	s_nop 0
	v_mul_f32_e32 v2, v2, v4
	v_cndmask_b32_e32 v34, 0, v2, vcc
	v_mul_f32_e64 v2, v3, -v5
	v_sub_f32_e32 v3, v7, v23
	v_mul_f32_e32 v3, 0x3fb8aa3b, v3
	v_exp_f32_e32 v3, v3
	v_cmp_gt_u32_e32 vcc, 8, v22
	v_mov_b32_e32 v4, s0
	ds_read2_b32 v[4:5], v4 offset1:1
	ds_read2_b32 v[6:7], v29 offset0:9 offset1:10
	v_mul_f32_e32 v2, v2, v3
	v_cndmask_b32_e32 v33, 0, v2, vcc
	v_add_u32_e32 v2, 0x1800, v27
	ds_read2_b32 v[2:3], v2 offset0:100 offset1:168
	v_cmp_gt_u32_e32 vcc, 9, v22
	v_readlane_b32 s0, v240, 26
	s_waitcnt lgkmcnt(0)
	v_mul_f32_e64 v2, v2, -v4
	v_sub_f32_e32 v4, v6, v23
	v_mul_f32_e32 v4, 0x3fb8aa3b, v4
	v_exp_f32_e32 v4, v4
	s_nop 0
	v_mul_f32_e32 v2, v2, v4
	v_cndmask_b32_e32 v36, 0, v2, vcc
	v_mul_f32_e64 v2, v3, -v5
	v_sub_f32_e32 v3, v7, v23
	v_mul_f32_e32 v3, 0x3fb8aa3b, v3
	v_exp_f32_e32 v3, v3
	v_cmp_gt_u32_e32 vcc, 10, v22
	v_mov_b32_e32 v4, s0
	ds_read2_b32 v[4:5], v4 offset1:1
	ds_read2_b32 v[6:7], v29 offset0:11 offset1:12
	v_mul_f32_e32 v2, v2, v3
	v_cndmask_b32_e32 v35, 0, v2, vcc
	v_add_u32_e32 v2, 0x1a00, v27
	ds_read2_b32 v[2:3], v2 offset0:108 offset1:176
	v_cmp_gt_u32_e32 vcc, 11, v22
	v_readlane_b32 s0, v240, 27
	s_waitcnt lgkmcnt(0)
	v_mul_f32_e64 v2, v2, -v4
	v_sub_f32_e32 v4, v6, v23
	v_mul_f32_e32 v4, 0x3fb8aa3b, v4
	v_exp_f32_e32 v4, v4
	s_nop 0
	v_mul_f32_e32 v2, v2, v4
	v_cndmask_b32_e32 v43, 0, v2, vcc
	v_mul_f32_e64 v2, v3, -v5
	v_sub_f32_e32 v3, v7, v23
	v_mul_f32_e32 v3, 0x3fb8aa3b, v3
	v_exp_f32_e32 v3, v3
	v_cmp_gt_u32_e32 vcc, 12, v22
	v_mov_b32_e32 v4, s0
	ds_read2_b32 v[4:5], v4 offset1:1
	ds_read2_b32 v[6:7], v29 offset0:13 offset1:14
	v_mul_f32_e32 v2, v2, v3
	v_cndmask_b32_e32 v38, 0, v2, vcc
	v_add_u32_e32 v2, 0x1c00, v27
	ds_read2_b32 v[2:3], v2 offset0:116 offset1:184
	v_cmp_gt_u32_e32 vcc, 13, v22
	v_readlane_b32 s0, v240, 28
	s_waitcnt lgkmcnt(0)
	v_mul_f32_e64 v2, v2, -v4
	v_sub_f32_e32 v4, v6, v23
	v_mul_f32_e32 v4, 0x3fb8aa3b, v4
	v_exp_f32_e32 v4, v4
	s_nop 0
	v_mul_f32_e32 v2, v2, v4
	v_cndmask_b32_e32 v52, 0, v2, vcc
	v_mul_f32_e64 v2, v3, -v5
	v_sub_f32_e32 v3, v7, v23
	v_mul_f32_e32 v3, 0x3fb8aa3b, v3
	v_exp_f32_e32 v3, v3
	v_cmp_gt_u32_e32 vcc, 14, v22
	v_mov_b32_e32 v4, s0
	ds_read2_b32 v[4:5], v4 offset1:1
	ds_read2_b32 v[6:7], v29 offset0:15 offset1:16
	v_mul_f32_e32 v2, v2, v3
	v_cndmask_b32_e32 v39, 0, v2, vcc
	v_add_u32_e32 v2, 0x1e00, v27
	ds_read2_b32 v[2:3], v2 offset0:124 offset1:192
	v_cmp_gt_u32_e32 vcc, 15, v22
	v_readlane_b32 s0, v240, 29
	s_waitcnt lgkmcnt(0)
	v_mul_f32_e64 v2, v2, -v4
	v_sub_f32_e32 v4, v6, v23
	v_mul_f32_e32 v4, 0x3fb8aa3b, v4
	v_exp_f32_e32 v4, v4
	s_nop 0
	v_mul_f32_e32 v2, v2, v4
	v_cndmask_b32_e32 v56, 0, v2, vcc
	v_mul_f32_e64 v2, v3, -v5
	v_sub_f32_e32 v3, v7, v23
	v_mul_f32_e32 v3, 0x3fb8aa3b, v3
	v_exp_f32_e32 v3, v3
	v_cmp_gt_u32_e32 vcc, 16, v22
	v_mov_b32_e32 v4, s0
	ds_read2_b32 v[4:5], v4 offset1:1
	ds_read2_b32 v[6:7], v29 offset0:17 offset1:18
	v_mul_f32_e32 v2, v2, v3
	v_cndmask_b32_e32 v40, 0, v2, vcc
	v_add_u32_e32 v2, 0x2000, v27
	ds_read2_b32 v[2:3], v2 offset0:132 offset1:200
	v_cmp_gt_u32_e32 vcc, 17, v22
	v_readlane_b32 s0, v240, 30
	s_waitcnt lgkmcnt(0)
	v_mul_f32_e64 v2, v2, -v4
	v_sub_f32_e32 v4, v6, v23
	v_mul_f32_e32 v4, 0x3fb8aa3b, v4
	v_exp_f32_e32 v4, v4
	s_nop 0
	v_mul_f32_e32 v2, v2, v4
	v_cndmask_b32_e32 v54, 0, v2, vcc
	v_mul_f32_e64 v2, v3, -v5
	v_sub_f32_e32 v3, v7, v23
	v_mul_f32_e32 v3, 0x3fb8aa3b, v3
	v_exp_f32_e32 v3, v3
	v_cmp_gt_u32_e32 vcc, 18, v22
	v_mov_b32_e32 v4, s0
	ds_read2_b32 v[4:5], v4 offset1:1
	ds_read2_b32 v[6:7], v29 offset0:19 offset1:20
	v_mul_f32_e32 v2, v2, v3
	v_cndmask_b32_e32 v42, 0, v2, vcc
	ds_read2_b32 v[2:3], v8 offset0:12 offset1:80
	v_cmp_gt_u32_e32 vcc, 19, v22
	v_readlane_b32 s0, v240, 31
	s_waitcnt lgkmcnt(0)
	v_mul_f32_e64 v2, v2, -v4
	v_sub_f32_e32 v4, v6, v23
	v_mul_f32_e32 v4, 0x3fb8aa3b, v4
	v_exp_f32_e32 v4, v4
	s_nop 0
	v_mul_f32_e32 v2, v2, v4
	v_cndmask_b32_e32 v46, 0, v2, vcc
	v_mul_f32_e64 v2, v3, -v5
	v_sub_f32_e32 v3, v7, v23
	v_mul_f32_e32 v3, 0x3fb8aa3b, v3
	v_exp_f32_e32 v3, v3
	v_cmp_gt_u32_e32 vcc, 20, v22
	v_mov_b32_e32 v4, s0
	ds_read2_b32 v[4:5], v4 offset1:1
	ds_read2_b32 v[6:7], v29 offset0:21 offset1:22
	v_mul_f32_e32 v2, v2, v3
	v_cndmask_b32_e32 v45, 0, v2, vcc
	ds_read2_b32 v[2:3], v8 offset0:148 offset1:216
	v_cmp_gt_u32_e32 vcc, 21, v22
	v_readlane_b32 s0, v240, 32
	v_add_u32_e32 v8, 0x2800, v27
	s_waitcnt lgkmcnt(0)
	v_mul_f32_e64 v2, v2, -v4
	v_sub_f32_e32 v4, v6, v23
	v_mul_f32_e32 v4, 0x3fb8aa3b, v4
	v_exp_f32_e32 v4, v4
	s_nop 0
	v_mul_f32_e32 v2, v2, v4
	v_cndmask_b32_e32 v57, 0, v2, vcc
	v_mul_f32_e64 v2, v3, -v5
	v_sub_f32_e32 v3, v7, v23
	v_mul_f32_e32 v3, 0x3fb8aa3b, v3
	v_exp_f32_e32 v3, v3
	v_cmp_gt_u32_e32 vcc, 22, v22
	v_mov_b32_e32 v4, s0
	ds_read2_b32 v[4:5], v4 offset1:1
	ds_read2_b32 v[6:7], v29 offset0:23 offset1:24
	v_mul_f32_e32 v2, v2, v3
	v_cndmask_b32_e32 v47, 0, v2, vcc
	ds_read2_b32 v[2:3], v8 offset0:28 offset1:96
	v_cmp_gt_u32_e32 vcc, 23, v22
	v_readlane_b32 s0, v240, 33
	s_waitcnt lgkmcnt(0)
	v_mul_f32_e64 v2, v2, -v4
	v_sub_f32_e32 v4, v6, v23
	v_mul_f32_e32 v4, 0x3fb8aa3b, v4
	v_exp_f32_e32 v4, v4
	s_nop 0
	v_mul_f32_e32 v2, v2, v4
	v_cndmask_b32_e32 v49, 0, v2, vcc
	v_mul_f32_e64 v2, v3, -v5
	v_sub_f32_e32 v3, v7, v23
	v_mul_f32_e32 v3, 0x3fb8aa3b, v3
	v_exp_f32_e32 v3, v3
	v_cmp_gt_u32_e32 vcc, 24, v22
	v_mov_b32_e32 v4, s0
	ds_read2_b32 v[4:5], v4 offset1:1
	ds_read2_b32 v[6:7], v29 offset0:25 offset1:26
	v_mul_f32_e32 v2, v2, v3
	v_cndmask_b32_e32 v51, 0, v2, vcc
	ds_read2_b32 v[2:3], v8 offset0:164 offset1:232
	v_cmp_gt_u32_e32 vcc, 25, v22
	v_readlane_b32 s0, v240, 34
	v_add_u32_e32 v8, 0x2c00, v27
	s_waitcnt lgkmcnt(0)
; __device__ __forceinline__ int otid() { int t = threadIdx.x; asm volatile("" : "+v"(t)); return t; }
; __device__ __forceinline__ void ph_gdn_prep(const Params& p, LAS unsigned char* lds) {
;     ...
;         { const int h = wid, kh = h >> 1, c = otid() & 63; const float Gc_ = Gs[h * 64 + c];
; #pragma unroll
;             for (int j = 0; j < 64; ++j) { const float kkv = KK[kh * 64 * 68 + j * 68 + c]; const float v = -Bs[h * 64 + j] * kkv * __expf(Gs[h * 64 + j] - Gc_); mcol[j] = (j > c) ? v : 0.f; } }
	v_mul_f32_e64 v2, v2, -v4
	v_sub_f32_e32 v4, v6, v23
	v_mul_f32_e32 v4, 0x3fb8aa3b, v4
	v_exp_f32_e32 v4, v4
	s_nop 0
	v_mul_f32_e32 v2, v2, v4
	v_cndmask_b32_e32 v61, 0, v2, vcc
	v_mul_f32_e64 v2, v3, -v5
	v_sub_f32_e32 v3, v7, v23
	v_mul_f32_e32 v3, 0x3fb8aa3b, v3
	v_exp_f32_e32 v3, v3
	v_cmp_gt_u32_e32 vcc, 26, v22
	v_mov_b32_e32 v4, s0
	ds_read2_b32 v[4:5], v4 offset1:1
	ds_read2_b32 v[6:7], v29 offset0:27 offset1:28
	v_mul_f32_e32 v2, v2, v3
	v_cndmask_b32_e32 v59, 0, v2, vcc
	ds_read2_b32 v[2:3], v8 offset0:44 offset1:112
	v_cmp_gt_u32_e32 vcc, 27, v22
	v_readlane_b32 s0, v240, 35
	s_waitcnt lgkmcnt(0)
	v_mul_f32_e64 v2, v2, -v4
	v_sub_f32_e32 v4, v6, v23
	v_mul_f32_e32 v4, 0x3fb8aa3b, v4
	v_exp_f32_e32 v4, v4
	s_nop 0
	v_mul_f32_e32 v2, v2, v4
	v_cndmask_b32_e32 v68, 0, v2, vcc
	v_mul_f32_e64 v2, v3, -v5
	v_sub_f32_e32 v3, v7, v23
	v_mul_f32_e32 v3, 0x3fb8aa3b, v3
	v_exp_f32_e32 v3, v3
	v_cmp_gt_u32_e32 vcc, 28, v22
	v_mov_b32_e32 v4, s0
	ds_read2_b32 v[4:5], v4 offset1:1
	ds_read2_b32 v[6:7], v29 offset0:29 offset1:30
	v_mul_f32_e32 v2, v2, v3
	v_cndmask_b32_e32 v66, 0, v2, vcc
	ds_read2_b32 v[2:3], v8 offset0:180 offset1:248
	v_cmp_gt_u32_e32 vcc, 29, v22
	v_readlane_b32 s0, v240, 36
	v_add_u32_e32 v8, 0x4400, v27
	s_waitcnt lgkmcnt(0)
	v_mul_f32_e64 v2, v2, -v4
	v_sub_f32_e32 v4, v6, v23
	v_mul_f32_e32 v4, 0x3fb8aa3b, v4
	v_exp_f32_e32 v4, v4
	s_nop 0
	v_mul_f32_e32 v2, v2, v4
	v_cndmask_b32_e32 v67, 0, v2, vcc
	v_mul_f32_e64 v2, v3, -v5
	v_sub_f32_e32 v3, v7, v23
	v_mul_f32_e32 v3, 0x3fb8aa3b, v3
	v_exp_f32_e32 v3, v3
	v_cmp_gt_u32_e32 vcc, 30, v22
	v_mov_b32_e32 v4, s0
	ds_read2_b32 v[4:5], v4 offset1:1
	ds_read2_b32 v[6:7], v29 offset0:31 offset1:32
	v_mul_f32_e32 v2, v2, v3
	v_cndmask_b32_e32 v65, 0, v2, vcc
	v_add_u32_e32 v2, 0x3000, v27
	ds_read2_b32 v[2:3], v2 offset0:60 offset1:128
	v_cmp_gt_u32_e32 vcc, 31, v22
	v_readlane_b32 s0, v240, 37
	s_waitcnt lgkmcnt(0)
	v_mul_f32_e64 v2, v2, -v4
	v_sub_f32_e32 v4, v6, v23
	v_mul_f32_e32 v4, 0x3fb8aa3b, v4
	v_exp_f32_e32 v4, v4
	s_nop 0
	v_mul_f32_e32 v2, v2, v4
	v_cndmask_b32_e32 v63, 0, v2, vcc
	v_mul_f32_e64 v2, v3, -v5
	v_sub_f32_e32 v3, v7, v23
	v_mul_f32_e32 v3, 0x3fb8aa3b, v3
	v_exp_f32_e32 v3, v3
	v_cmp_gt_u32_e32 vcc, 32, v22
	v_mov_b32_e32 v4, s0
	ds_read2_b32 v[4:5], v4 offset1:1
	ds_read2_b32 v[6:7], v29 offset0:33 offset1:34
	v_mul_f32_e32 v2, v2, v3
	v_cndmask_b32_e32 v64, 0, v2, vcc
	v_add_u32_e32 v2, 0x3200, v27
	ds_read2_b32 v[2:3], v2 offset0:68 offset1:136
	v_cmp_gt_u32_e32 vcc, 33, v22
	v_readlane_b32 s0, v240, 38
	s_waitcnt lgkmcnt(0)
	v_mul_f32_e64 v2, v2, -v4
	v_sub_f32_e32 v4, v6, v23
	v_mul_f32_e32 v4, 0x3fb8aa3b, v4
	v_exp_f32_e32 v4, v4
	s_nop 0
	v_mul_f32_e32 v2, v2, v4
	v_cndmask_b32_e32 v62, 0, v2, vcc
	v_mul_f32_e64 v2, v3, -v5
	v_sub_f32_e32 v3, v7, v23
	v_mul_f32_e32 v3, 0x3fb8aa3b, v3
	v_exp_f32_e32 v3, v3
	v_cmp_gt_u32_e32 vcc, 34, v22
	v_mov_b32_e32 v4, s0
	ds_read2_b32 v[4:5], v4 offset1:1
	ds_read2_b32 v[6:7], v29 offset0:35 offset1:36
	v_mul_f32_e32 v2, v2, v3
	v_cndmask_b32_e32 v60, 0, v2, vcc
	v_add_u32_e32 v2, 0x3400, v27
	ds_read2_b32 v[2:3], v2 offset0:76 offset1:144
	v_cmp_gt_u32_e32 vcc, 35, v22
	v_readlane_b32 s0, v240, 39
	s_waitcnt lgkmcnt(0)
	v_mul_f32_e64 v2, v2, -v4
	v_sub_f32_e32 v4, v6, v23
	v_mul_f32_e32 v4, 0x3fb8aa3b, v4
	v_exp_f32_e32 v4, v4
	s_nop 0
	v_mul_f32_e32 v2, v2, v4
	v_cndmask_b32_e32 v58, 0, v2, vcc
	v_mul_f32_e64 v2, v3, -v5
	v_sub_f32_e32 v3, v7, v23
	v_mul_f32_e32 v3, 0x3fb8aa3b, v3
	v_exp_f32_e32 v3, v3
	v_cmp_gt_u32_e32 vcc, 36, v22
	v_mov_b32_e32 v4, s0
	ds_read2_b32 v[4:5], v4 offset1:1
	ds_read2_b32 v[6:7], v29 offset0:37 offset1:38
	v_mul_f32_e32 v2, v2, v3
	v_cndmask_b32_e32 v55, 0, v2, vcc
	v_add_u32_e32 v2, 0x3600, v27
	ds_read2_b32 v[2:3], v2 offset0:84 offset1:152
	v_cmp_gt_u32_e32 vcc, 37, v22
	v_readlane_b32 s0, v240, 40
	s_waitcnt lgkmcnt(0)
	v_mul_f32_e64 v2, v2, -v4
	v_sub_f32_e32 v4, v6, v23
	v_mul_f32_e32 v4, 0x3fb8aa3b, v4
	v_exp_f32_e32 v4, v4
	s_nop 0
	v_mul_f32_e32 v2, v2, v4
	v_cndmask_b32_e32 v53, 0, v2, vcc
	v_mul_f32_e64 v2, v3, -v5
	v_sub_f32_e32 v3, v7, v23
	v_mul_f32_e32 v3, 0x3fb8aa3b, v3
	v_exp_f32_e32 v3, v3
	v_cmp_gt_u32_e32 vcc, 38, v22
	v_mov_b32_e32 v4, s0
	ds_read2_b32 v[4:5], v4 offset1:1
	ds_read2_b32 v[6:7], v29 offset0:39 offset1:40
	v_mul_f32_e32 v2, v2, v3
	v_cndmask_b32_e32 v50, 0, v2, vcc
	v_add_u32_e32 v2, 0x3800, v27
	ds_read2_b32 v[2:3], v2 offset0:92 offset1:160
	v_cmp_gt_u32_e32 vcc, 39, v22
	v_readlane_b32 s0, v240, 41
	s_waitcnt lgkmcnt(0)
	v_mul_f32_e64 v2, v2, -v4
	v_sub_f32_e32 v4, v6, v23
	v_mul_f32_e32 v4, 0x3fb8aa3b, v4
	v_exp_f32_e32 v4, v4
	s_nop 0
	v_mul_f32_e32 v2, v2, v4
	v_cndmask_b32_e32 v48, 0, v2, vcc
	v_mul_f32_e64 v2, v3, -v5
	v_sub_f32_e32 v3, v7, v23
	v_mul_f32_e32 v3, 0x3fb8aa3b, v3
	v_exp_f32_e32 v3, v3
	v_cmp_gt_u32_e32 vcc, 40, v22
	v_mov_b32_e32 v4, s0
	ds_read2_b32 v[4:5], v4 offset1:1
	ds_read2_b32 v[6:7], v29 offset0:41 offset1:42
	v_mul_f32_e32 v2, v2, v3
	v_cndmask_b32_e32 v44, 0, v2, vcc
	v_add_u32_e32 v2, 0x3a00, v27
	ds_read2_b32 v[2:3], v2 offset0:100 offset1:168
	v_cmp_gt_u32_e32 vcc, 41, v22
	v_readlane_b32 s0, v240, 42
	s_waitcnt lgkmcnt(0)
	v_mul_f32_e64 v2, v2, -v4
	v_sub_f32_e32 v4, v6, v23
	v_mul_f32_e32 v4, 0x3fb8aa3b, v4
	v_exp_f32_e32 v4, v4
	s_nop 0
	v_mul_f32_e32 v2, v2, v4
	v_cndmask_b32_e32 v41, 0, v2, vcc
	v_mul_f32_e64 v2, v3, -v5
	v_sub_f32_e32 v3, v7, v23
	v_mul_f32_e32 v3, 0x3fb8aa3b, v3
	v_exp_f32_e32 v3, v3
	v_cmp_gt_u32_e32 vcc, 42, v22
	v_mov_b32_e32 v4, s0
	ds_read2_b32 v[4:5], v4 offset1:1
	ds_read2_b32 v[6:7], v29 offset0:43 offset1:44
	v_mul_f32_e32 v2, v2, v3
	v_cndmask_b32_e32 v37, 0, v2, vcc
	v_add_u32_e32 v2, 0x3c00, v27
	ds_read2_b32 v[2:3], v2 offset0:108 offset1:176
	v_cmp_gt_u32_e32 vcc, 43, v22
	v_readlane_b32 s0, v240, 43
	s_waitcnt lgkmcnt(0)
; __device__ __forceinline__ int otid() { int t = threadIdx.x; asm volatile("" : "+v"(t)); return t; }
; __device__ __forceinline__ void ph_gdn_prep(const Params& p, LAS unsigned char* lds) {
;     ...
;         { const int h = wid, kh = h >> 1, c = otid() & 63; const float Gc_ = Gs[h * 64 + c];
; #pragma unroll
;             for (int j = 0; j < 64; ++j) { const float kkv = KK[kh * 64 * 68 + j * 68 + c]; const float v = -Bs[h * 64 + j] * kkv * __expf(Gs[h * 64 + j] - Gc_); mcol[j] = (j > c) ? v : 0.f; } }
;         __syncthreads();
;         {
; #pragma unroll
;             for (int i = 1; i < 64; ++i) { const int mi = __float_as_int(mcol[i]); float a0 = mcol[i], a1 = 0.f;
; #pragma unroll
;                 for (int j = 0; j < i; ++j) { const float s = __int_as_float(__builtin_amdgcn_readlane(mi, j)); if (j & 1) a1 += s * mcol[j]; else a0 += s * mcol[j]; }
;                 mcol[i] = a0 + a1; }
	v_mul_f32_e64 v2, v2, -v4
	v_sub_f32_e32 v4, v6, v23
	v_mul_f32_e32 v4, 0x3fb8aa3b, v4
	v_exp_f32_e32 v4, v4
	s_nop 0
	v_mul_f32_e32 v2, v2, v4
	v_cndmask_b32_e32 v30, 0, v2, vcc
	v_mul_f32_e64 v2, v3, -v5
	v_sub_f32_e32 v3, v7, v23
	v_mul_f32_e32 v3, 0x3fb8aa3b, v3
	v_exp_f32_e32 v3, v3
	v_cmp_gt_u32_e32 vcc, 44, v22
	v_mov_b32_e32 v4, s0
	ds_read2_b32 v[4:5], v4 offset1:1
	ds_read2_b32 v[6:7], v29 offset0:45 offset1:46
	v_mul_f32_e32 v2, v2, v3
	v_cndmask_b32_e32 v21, 0, v2, vcc
	v_add_u32_e32 v2, 0x3e00, v27
	ds_read2_b32 v[2:3], v2 offset0:116 offset1:184
	v_cmp_gt_u32_e32 vcc, 45, v22
	v_readlane_b32 s0, v240, 44
	s_waitcnt lgkmcnt(0)
	v_mul_f32_e64 v2, v2, -v4
	v_sub_f32_e32 v4, v6, v23
	v_mul_f32_e32 v4, 0x3fb8aa3b, v4
	v_exp_f32_e32 v4, v4
	s_nop 0
	v_mul_f32_e32 v2, v2, v4
	v_cndmask_b32_e32 v20, 0, v2, vcc
	v_mul_f32_e64 v2, v3, -v5
	v_sub_f32_e32 v3, v7, v23
	v_mul_f32_e32 v3, 0x3fb8aa3b, v3
	v_exp_f32_e32 v3, v3
	v_cmp_gt_u32_e32 vcc, 46, v22
	v_mov_b32_e32 v4, s0
	ds_read2_b32 v[4:5], v4 offset1:1
	ds_read2_b32 v[6:7], v29 offset0:47 offset1:48
	v_mul_f32_e32 v2, v2, v3
	v_cndmask_b32_e32 v19, 0, v2, vcc
	v_add_u32_e32 v2, 0x4000, v27
	ds_read2_b32 v[2:3], v2 offset0:124 offset1:192
	v_cmp_gt_u32_e32 vcc, 47, v22
	v_readlane_b32 s0, v240, 46
	s_waitcnt lgkmcnt(0)
	v_mul_f32_e64 v2, v2, -v4
	v_sub_f32_e32 v4, v6, v23
	v_mul_f32_e32 v4, 0x3fb8aa3b, v4
	v_exp_f32_e32 v4, v4
	s_nop 0
	v_mul_f32_e32 v2, v2, v4
	v_cndmask_b32_e32 v18, 0, v2, vcc
	v_mul_f32_e64 v2, v3, -v5
	v_sub_f32_e32 v3, v7, v23
	v_mul_f32_e32 v3, 0x3fb8aa3b, v3
	v_exp_f32_e32 v3, v3
	v_cmp_gt_u32_e32 vcc, 48, v22
	v_mov_b32_e32 v4, s0
	ds_read2_b32 v[4:5], v4 offset1:1
	ds_read2_b32 v[6:7], v29 offset0:49 offset1:50
	v_mul_f32_e32 v2, v2, v3
	v_cndmask_b32_e32 v17, 0, v2, vcc
	ds_read2_b32 v[2:3], v8 offset0:4 offset1:72
	v_cmp_gt_u32_e32 vcc, 49, v22
	v_readlane_b32 s0, v240, 47
	s_waitcnt lgkmcnt(0)
	v_mul_f32_e64 v2, v2, -v4
	v_sub_f32_e32 v4, v6, v23
	v_mul_f32_e32 v4, 0x3fb8aa3b, v4
	v_exp_f32_e32 v4, v4
	s_nop 0
	v_mul_f32_e32 v2, v2, v4
	v_cndmask_b32_e32 v16, 0, v2, vcc
	v_mul_f32_e64 v2, v3, -v5
	v_sub_f32_e32 v3, v7, v23
	v_mul_f32_e32 v3, 0x3fb8aa3b, v3
	v_exp_f32_e32 v3, v3
	v_cmp_gt_u32_e32 vcc, 50, v22
	v_mov_b32_e32 v4, s0
	ds_read2_b32 v[4:5], v4 offset1:1
	ds_read2_b32 v[6:7], v29 offset0:51 offset1:52
	v_mul_f32_e32 v2, v2, v3
	v_cndmask_b32_e32 v15, 0, v2, vcc
	ds_read2_b32 v[2:3], v8 offset0:140 offset1:208
	v_cmp_gt_u32_e32 vcc, 51, v22
	v_readlane_b32 s0, v240, 48
	v_add_u32_e32 v8, 0x4800, v27
	s_waitcnt lgkmcnt(0)
	v_mul_f32_e64 v2, v2, -v4
	v_sub_f32_e32 v4, v6, v23
	v_mul_f32_e32 v4, 0x3fb8aa3b, v4
	v_exp_f32_e32 v4, v4
	s_nop 0
	v_mul_f32_e32 v2, v2, v4
	v_cndmask_b32_e32 v14, 0, v2, vcc
	v_mul_f32_e64 v2, v3, -v5
	v_sub_f32_e32 v3, v7, v23
	v_mul_f32_e32 v3, 0x3fb8aa3b, v3
	v_exp_f32_e32 v3, v3
	v_cmp_gt_u32_e32 vcc, 52, v22
	v_mov_b32_e32 v4, s0
	ds_read2_b32 v[4:5], v4 offset1:1
	ds_read2_b32 v[6:7], v29 offset0:53 offset1:54
	v_mul_f32_e32 v2, v2, v3
	v_cndmask_b32_e32 v12, 0, v2, vcc
	ds_read2_b32 v[2:3], v8 offset0:20 offset1:88
	v_cmp_gt_u32_e32 vcc, 53, v22
	v_readlane_b32 s0, v240, 49
	s_waitcnt lgkmcnt(0)
	v_mul_f32_e64 v2, v2, -v4
	v_sub_f32_e32 v4, v6, v23
	v_mul_f32_e32 v4, 0x3fb8aa3b, v4
	v_exp_f32_e32 v4, v4
	s_nop 0
	v_mul_f32_e32 v2, v2, v4
	v_cndmask_b32_e32 v11, 0, v2, vcc
	v_mul_f32_e64 v2, v3, -v5
	v_sub_f32_e32 v3, v7, v23
	v_mul_f32_e32 v3, 0x3fb8aa3b, v3
	v_exp_f32_e32 v3, v3
	v_cmp_gt_u32_e32 vcc, 54, v22
	v_mov_b32_e32 v4, s0
	ds_read2_b32 v[4:5], v4 offset1:1
	ds_read2_b32 v[6:7], v29 offset0:55 offset1:56
	v_mul_f32_e32 v2, v2, v3
	v_cndmask_b32_e32 v10, 0, v2, vcc
	ds_read2_b32 v[2:3], v8 offset0:156 offset1:224
	v_cmp_gt_u32_e32 vcc, 55, v22
	v_readlane_b32 s0, v240, 50
	s_waitcnt lgkmcnt(0)
	v_mul_f32_e64 v2, v2, -v4
	v_sub_f32_e32 v4, v6, v23
	v_mul_f32_e32 v4, 0x3fb8aa3b, v4
	v_exp_f32_e32 v4, v4
	s_nop 0
	v_mul_f32_e32 v2, v2, v4
	v_cndmask_b32_e32 v9, 0, v2, vcc
	v_mul_f32_e64 v2, v3, -v5
	v_sub_f32_e32 v3, v7, v23
	v_mul_f32_e32 v3, 0x3fb8aa3b, v3
	v_exp_f32_e32 v3, v3
	v_cmp_gt_u32_e32 vcc, 56, v22
	v_mov_b32_e32 v4, s0
	ds_read2_b32 v[4:5], v4 offset1:1
	v_mul_f32_e32 v2, v2, v3
	v_cndmask_b32_e32 v8, 0, v2, vcc
	ds_read2_b32 v[2:3], v13 offset0:36 offset1:104
	v_cmp_gt_u32_e32 vcc, 57, v22
	v_readlane_b32 s0, v240, 51
	s_waitcnt lgkmcnt(0)
	v_mul_f32_e64 v2, v2, -v4
	v_sub_f32_e32 v4, v70, v23
	v_mul_f32_e32 v4, 0x3fb8aa3b, v4
	v_exp_f32_e32 v4, v4
	s_nop 0
	v_mul_f32_e32 v2, v2, v4
	v_cndmask_b32_e32 v7, 0, v2, vcc
	v_mul_f32_e64 v2, v3, -v5
	v_sub_f32_e32 v3, v71, v23
	v_mul_f32_e32 v3, 0x3fb8aa3b, v3
	v_exp_f32_e32 v3, v3
	v_cmp_gt_u32_e32 vcc, 58, v22
	v_mov_b32_e32 v4, s0
	ds_read2_b32 v[4:5], v4 offset1:1
	ds_read2_b32 v[70:71], v29 offset0:59 offset1:60
	v_mul_f32_e32 v2, v2, v3
	v_cndmask_b32_e32 v6, 0, v2, vcc
	ds_read2_b32 v[2:3], v13 offset0:172 offset1:240
	v_cmp_gt_u32_e32 vcc, 59, v22
	v_readlane_b32 s0, v240, 52
	s_waitcnt lgkmcnt(0)
	v_mul_f32_e64 v2, v2, -v4
	v_sub_f32_e32 v4, v70, v23
	v_mul_f32_e32 v4, 0x3fb8aa3b, v4
	v_exp_f32_e32 v4, v4
	s_nop 0
	v_mul_f32_e32 v2, v2, v4
	v_cndmask_b32_e32 v13, 0, v2, vcc
	v_mul_f32_e64 v2, v3, -v5
	v_sub_f32_e32 v3, v71, v23
	v_mul_f32_e32 v3, 0x3fb8aa3b, v3
	v_exp_f32_e32 v3, v3
	v_cmp_gt_u32_e32 vcc, 60, v22
	v_sub_f32_e32 v5, v75, v23
	v_mul_f32_e32 v5, 0x3fb8aa3b, v5
	v_mul_f32_e32 v2, v2, v3
	v_cndmask_b32_e32 v4, 0, v2, vcc
	v_add_u32_e32 v2, 0x5000, v27
	ds_read2_b32 v[70:71], v2 offset0:52 offset1:120
	v_mov_b32_e32 v2, s0
	ds_read2_b32 v[72:73], v2 offset1:1
	v_sub_f32_e32 v3, v74, v23
	v_mul_f32_e32 v3, 0x3fb8aa3b, v3
	v_exp_f32_e32 v3, v3
	v_exp_f32_e32 v5, v5
	s_waitcnt lgkmcnt(0)
	v_mul_f32_e64 v2, v70, -v72
	v_cmp_gt_u32_e32 vcc, 61, v22
	v_mul_f32_e32 v2, v2, v3
	v_readlane_b32 s0, v240, 14
	v_cndmask_b32_e32 v3, 0, v2, vcc
	v_mul_f32_e64 v2, v71, -v73
	v_mul_f32_e32 v2, v2, v5
	ds_read_b32 v5, v27 offset:21232
	v_mov_b32_e32 v27, s0
	ds_read2st64_b32 v[70:71], v27 offset1:8
	v_readlane_b32 s0, v24, 0
	v_cmp_gt_u32_e32 vcc, 62, v22
	s_waitcnt lgkmcnt(0)
	v_fmac_f32_e64 v24, s0, 0
	v_sub_f32_e32 v23, v70, v23
	v_mul_f32_e32 v23, 0x3fb8aa3b, v23
	v_exp_f32_e32 v23, v23
	v_mul_f32_e64 v5, v5, -v71
	v_cndmask_b32_e32 v2, 0, v2, vcc
	v_cmp_ne_u32_e32 vcc, 63, v22
	v_mul_f32_e32 v5, v5, v23
	v_add_f32_e32 v27, 0, v24
	v_readlane_b32 s0, v25, 0
	v_cndmask_b32_e32 v29, 0, v5, vcc
	v_fma_f32 v5, v27, s1, 0
	v_fmac_f32_e64 v25, s0, 0
	v_add_f32_e32 v25, v25, v5
	s_barrier
; __device__ __forceinline__ void ph_gdn_prep(const Params& p, LAS unsigned char* lds) {
;     ...
;             for (int i = 1; i < 64; ++i) { const int mi = __float_as_int(mcol[i]); float a0 = mcol[i], a1 = 0.f;
; #pragma unroll
;                 for (int j = 0; j < i; ++j) { const float s = __int_as_float(__builtin_amdgcn_readlane(mi, j)); if (j & 1) a1 += s * mcol[j]; else a0 += s * mcol[j]; }
;                 mcol[i] = a0 + a1; }
	v_readlane_b32 s0, v28, 0
	v_readlane_b32 s98, v28, 1
	v_readlane_b32 s99, v28, 2
	v_fma_f32 v5, 0, s0, v28
	s_lshl_b32 s1, s70, 15
	v_readlane_b32 s100, v26, 0
	v_fma_f32 v22, v27, s98, 0
	v_readlane_b32 s0, v26, 1
	v_fmac_f32_e32 v5, s99, v25
	v_add_f32_e32 v23, v22, v5
	v_readlane_b32 s98, v26, 2
	v_fma_f32 v5, 0, s100, v26
	v_readlane_b32 s99, v26, 3
	v_fma_f32 v22, v27, s0, 0
	v_readlane_b32 s100, v32, 0
	v_fmac_f32_e32 v5, s98, v25
	v_readlane_b32 s0, v32, 1
	v_fmac_f32_e32 v22, s99, v23
	v_add_f32_e32 v5, v5, v22
	v_readlane_b32 s98, v32, 2
	v_fma_f32 v22, 0, s100, v32
	v_readlane_b32 s99, v32, 3
	v_fma_f32 v24, v27, s0, 0
	v_readlane_b32 s100, v32, 4
	v_fmac_f32_e32 v22, s98, v25
	v_readlane_b32 s0, v31, 0
	v_fmac_f32_e32 v24, s99, v23
	v_readlane_b32 s98, v31, 1
	v_fmac_f32_e32 v22, s100, v5
	v_add_f32_e32 v22, v24, v22
	v_readlane_b32 s99, v31, 2
	v_fma_f32 v24, 0, s0, v31
	v_readlane_b32 s100, v31, 3
	v_fma_f32 v26, v27, s98, 0
	v_readlane_b32 s0, v31, 4
	v_fmac_f32_e32 v24, s99, v25
	v_readlane_b32 s98, v31, 5
	v_fmac_f32_e32 v26, s100, v23
	v_readlane_b32 s99, v34, 0
	v_fmac_f32_e32 v24, s0, v5
	v_readlane_b32 s100, v34, 1
	v_fmac_f32_e32 v26, s98, v22
	v_add_f32_e32 v24, v24, v26
	v_readlane_b32 s0, v34, 2
	v_fma_f32 v26, 0, s99, v34
	v_readlane_b32 s98, v34, 3
	v_fma_f32 v28, v27, s100, 0
	v_readlane_b32 s99, v34, 4
	v_fmac_f32_e32 v26, s0, v25
	v_readlane_b32 s100, v34, 5
	v_fmac_f32_e32 v28, s98, v23
	v_readlane_b32 s0, v34, 6
	v_fmac_f32_e32 v26, s99, v5
	v_readlane_b32 s98, v33, 0
	v_fmac_f32_e32 v28, s100, v22
	v_readlane_b32 s99, v33, 1
	v_fmac_f32_e32 v26, s0, v24
	v_add_f32_e32 v26, v28, v26
	v_readlane_b32 s100, v33, 2
	v_fma_f32 v28, 0, s98, v33
	v_readlane_b32 s0, v33, 3
	v_fma_f32 v31, v27, s99, 0
	v_readlane_b32 s98, v33, 4
	v_fmac_f32_e32 v28, s100, v25
	v_readlane_b32 s99, v33, 5
	v_fmac_f32_e32 v31, s0, v23
	v_readlane_b32 s100, v33, 6
	v_fmac_f32_e32 v28, s98, v5
	v_readlane_b32 s0, v33, 7
	v_fmac_f32_e32 v31, s99, v22
	v_readlane_b32 s98, v36, 0
	v_fmac_f32_e32 v28, s100, v24
	v_readlane_b32 s99, v36, 1
	v_fmac_f32_e32 v31, s0, v26
	v_add_f32_e32 v28, v28, v31
	v_readlane_b32 s100, v36, 2
	v_fma_f32 v31, 0, s98, v36
	v_readlane_b32 s0, v36, 3
	v_fma_f32 v32, v27, s99, 0
	v_readlane_b32 s98, v36, 4
	v_fmac_f32_e32 v31, s100, v25
	v_readlane_b32 s99, v36, 5
	v_fmac_f32_e32 v32, s0, v23
	v_readlane_b32 s100, v36, 6
	v_fmac_f32_e32 v31, s98, v5
	v_readlane_b32 s0, v36, 7
	v_fmac_f32_e32 v32, s99, v22
	v_readlane_b32 s98, v36, 8
	v_fmac_f32_e32 v31, s100, v24
	v_readlane_b32 s99, v35, 0
	v_fmac_f32_e32 v32, s0, v26
	v_readlane_b32 s100, v35, 1
	v_fmac_f32_e32 v31, s98, v28
	v_add_f32_e32 v31, v32, v31
	v_readlane_b32 s0, v35, 2
	v_fma_f32 v32, 0, s99, v35
	v_readlane_b32 s98, v35, 3
	v_fma_f32 v33, v27, s100, 0
	v_readlane_b32 s99, v35, 4
	v_fmac_f32_e32 v32, s0, v25
	v_readlane_b32 s100, v35, 5
	v_fmac_f32_e32 v33, s98, v23
	v_readlane_b32 s0, v35, 6
	v_fmac_f32_e32 v32, s99, v5
	v_readlane_b32 s98, v35, 7
	v_fmac_f32_e32 v33, s100, v22
	v_readlane_b32 s99, v35, 8
	v_fmac_f32_e32 v32, s0, v24
	v_readlane_b32 s100, v35, 9
	v_fmac_f32_e32 v33, s98, v26
	v_readlane_b32 s0, v43, 0
	v_fmac_f32_e32 v32, s99, v28
	v_readlane_b32 s98, v43, 1
	v_fmac_f32_e32 v33, s100, v31
	v_add_f32_e32 v32, v32, v33
	v_readlane_b32 s99, v43, 2
	v_fma_f32 v33, 0, s0, v43
	v_readlane_b32 s100, v43, 3
	v_fma_f32 v34, v27, s98, 0
	v_readlane_b32 s0, v43, 4
	v_fmac_f32_e32 v33, s99, v25
	v_readlane_b32 s98, v43, 5
	v_fmac_f32_e32 v34, s100, v23
	v_readlane_b32 s99, v43, 6
	v_fmac_f32_e32 v33, s0, v5
	v_readlane_b32 s100, v43, 7
	v_fmac_f32_e32 v34, s98, v22
	v_readlane_b32 s0, v43, 8
	v_fmac_f32_e32 v33, s99, v24
	v_readlane_b32 s98, v43, 9
	v_fmac_f32_e32 v34, s100, v26
	v_readlane_b32 s99, v43, 10
	v_fmac_f32_e32 v33, s0, v28
	v_readlane_b32 s100, v38, 0
	v_fmac_f32_e32 v34, s98, v31
	v_readlane_b32 s0, v38, 1
	v_fmac_f32_e32 v33, s99, v32
	v_add_f32_e32 v33, v34, v33
	v_readlane_b32 s98, v38, 2
	v_fma_f32 v34, 0, s100, v38
	v_readlane_b32 s99, v38, 3
	v_fma_f32 v35, v27, s0, 0
	v_readlane_b32 s100, v38, 4
	v_fmac_f32_e32 v34, s98, v25
	v_readlane_b32 s0, v38, 5
	v_fmac_f32_e32 v35, s99, v23
	v_readlane_b32 s98, v38, 6
	v_fmac_f32_e32 v34, s100, v5
	v_readlane_b32 s99, v38, 7
	v_fmac_f32_e32 v35, s0, v22
	v_readlane_b32 s100, v38, 8
	v_fmac_f32_e32 v34, s98, v24
	v_readlane_b32 s0, v38, 9
	v_fmac_f32_e32 v35, s99, v26
	v_readlane_b32 s98, v38, 10
	v_fmac_f32_e32 v34, s100, v28
	v_readlane_b32 s99, v38, 11
	v_fmac_f32_e32 v35, s0, v31
	v_readlane_b32 s100, v52, 0
	v_fmac_f32_e32 v34, s98, v32
	v_readlane_b32 s0, v52, 1
	v_fmac_f32_e32 v35, s99, v33
	v_add_f32_e32 v34, v34, v35
	v_readlane_b32 s98, v52, 2
	v_fma_f32 v35, 0, s100, v52
	v_readlane_b32 s99, v52, 3
	v_fma_f32 v36, v27, s0, 0
	v_readlane_b32 s100, v52, 4
	v_fmac_f32_e32 v35, s98, v25
	v_readlane_b32 s0, v52, 5
	v_fmac_f32_e32 v36, s99, v23
	v_readlane_b32 s98, v52, 6
	v_fmac_f32_e32 v35, s100, v5
	v_readlane_b32 s99, v52, 7
	v_fmac_f32_e32 v36, s0, v22
	v_readlane_b32 s100, v52, 8
	v_fmac_f32_e32 v35, s98, v24
	v_readlane_b32 s0, v52, 9
	v_fmac_f32_e32 v36, s99, v26
	v_readlane_b32 s98, v52, 10
	v_fmac_f32_e32 v35, s100, v28
	v_readlane_b32 s99, v52, 11
	v_fmac_f32_e32 v36, s0, v31
	v_readlane_b32 s100, v52, 12
	v_fmac_f32_e32 v35, s98, v32
	v_readlane_b32 s0, v39, 0
	v_fmac_f32_e32 v36, s99, v33
	v_readlane_b32 s98, v39, 1
	v_fmac_f32_e32 v35, s100, v34
	v_add_f32_e32 v35, v36, v35
	v_readlane_b32 s99, v39, 2
	v_fma_f32 v36, 0, s0, v39
	v_readlane_b32 s100, v39, 3
	v_fma_f32 v38, v27, s98, 0
	v_readlane_b32 s0, v39, 4
	v_fmac_f32_e32 v36, s99, v25
	v_readlane_b32 s98, v39, 5
; __device__ __forceinline__ void ph_gdn_prep(const Params& p, LAS unsigned char* lds) {
;     ...
;             for (int i = 1; i < 64; ++i) { const int mi = __float_as_int(mcol[i]); float a0 = mcol[i], a1 = 0.f;
; #pragma unroll
;                 for (int j = 0; j < i; ++j) { const float s = __int_as_float(__builtin_amdgcn_readlane(mi, j)); if (j & 1) a1 += s * mcol[j]; else a0 += s * mcol[j]; }
;                 mcol[i] = a0 + a1; }
	v_fmac_f32_e32 v38, s100, v23
	v_readlane_b32 s99, v39, 6
	v_fmac_f32_e32 v36, s0, v5
	v_readlane_b32 s100, v39, 7
	v_fmac_f32_e32 v38, s98, v22
	v_readlane_b32 s0, v39, 8
	v_fmac_f32_e32 v36, s99, v24
	v_readlane_b32 s98, v39, 9
	v_fmac_f32_e32 v38, s100, v26
	v_readlane_b32 s99, v39, 10
	v_fmac_f32_e32 v36, s0, v28
	v_readlane_b32 s100, v39, 11
	v_fmac_f32_e32 v38, s98, v31
	v_readlane_b32 s0, v39, 12
	v_fmac_f32_e32 v36, s99, v32
	v_readlane_b32 s98, v39, 13
	v_fmac_f32_e32 v38, s100, v33
	v_readlane_b32 s99, v56, 0
	v_fmac_f32_e32 v36, s0, v34
	v_readlane_b32 s100, v56, 1
	v_fmac_f32_e32 v38, s98, v35
	v_add_f32_e32 v36, v36, v38
	v_readlane_b32 s0, v56, 2
	v_fma_f32 v38, 0, s99, v56
	v_readlane_b32 s98, v56, 3
	v_fma_f32 v39, v27, s100, 0
	v_readlane_b32 s99, v56, 4
	v_fmac_f32_e32 v38, s0, v25
	v_readlane_b32 s100, v56, 5
	v_fmac_f32_e32 v39, s98, v23
	v_readlane_b32 s0, v56, 6
	v_fmac_f32_e32 v38, s99, v5
	v_readlane_b32 s98, v56, 7
	v_fmac_f32_e32 v39, s100, v22
	v_readlane_b32 s99, v56, 8
	v_fmac_f32_e32 v38, s0, v24
	v_readlane_b32 s100, v56, 9
	v_fmac_f32_e32 v39, s98, v26
	v_readlane_b32 s0, v56, 10
	v_fmac_f32_e32 v38, s99, v28
	v_readlane_b32 s98, v56, 11
	v_fmac_f32_e32 v39, s100, v31
	v_readlane_b32 s99, v56, 12
	v_fmac_f32_e32 v38, s0, v32
	v_readlane_b32 s100, v56, 13
	v_fmac_f32_e32 v39, s98, v33
	v_readlane_b32 s0, v56, 14
	v_fmac_f32_e32 v38, s99, v34
	v_readlane_b32 s98, v40, 0
	v_fmac_f32_e32 v39, s100, v35
	v_readlane_b32 s99, v40, 1
	v_fmac_f32_e32 v38, s0, v36
	v_add_f32_e32 v38, v39, v38
	v_readlane_b32 s100, v40, 2
	v_fma_f32 v39, 0, s98, v40
	v_readlane_b32 s0, v40, 3
	v_fma_f32 v43, v27, s99, 0
	v_readlane_b32 s98, v40, 4
	v_fmac_f32_e32 v39, s100, v25
	v_readlane_b32 s99, v40, 5
	v_fmac_f32_e32 v43, s0, v23
	v_readlane_b32 s100, v40, 6
	v_fmac_f32_e32 v39, s98, v5
	v_readlane_b32 s0, v40, 7
	v_fmac_f32_e32 v43, s99, v22
	v_readlane_b32 s98, v40, 8
	v_fmac_f32_e32 v39, s100, v24
	v_readlane_b32 s99, v40, 9
	v_fmac_f32_e32 v43, s0, v26
	v_readlane_b32 s100, v40, 10
	v_fmac_f32_e32 v39, s98, v28
	v_readlane_b32 s0, v40, 11
	v_fmac_f32_e32 v43, s99, v31
	v_readlane_b32 s98, v40, 12
	v_fmac_f32_e32 v39, s100, v32
	v_readlane_b32 s99, v40, 13
	v_fmac_f32_e32 v43, s0, v33
	v_readlane_b32 s100, v40, 14
	v_fmac_f32_e32 v39, s98, v34
	v_readlane_b32 s0, v40, 15
	v_fmac_f32_e32 v43, s99, v35
	v_readlane_b32 s98, v54, 0
	v_fmac_f32_e32 v39, s100, v36
	v_readlane_b32 s99, v54, 1
	v_fmac_f32_e32 v43, s0, v38
	v_add_f32_e32 v39, v39, v43
	v_readlane_b32 s100, v54, 2
	v_fma_f32 v40, 0, s98, v54
	v_readlane_b32 s0, v54, 3
	v_fma_f32 v43, v27, s99, 0
	v_readlane_b32 s98, v54, 4
	v_fmac_f32_e32 v40, s100, v25
	v_readlane_b32 s99, v54, 5
	v_fmac_f32_e32 v43, s0, v23
	v_readlane_b32 s100, v54, 6
	v_fmac_f32_e32 v40, s98, v5
	v_readlane_b32 s0, v54, 7
	v_fmac_f32_e32 v43, s99, v22
	v_readlane_b32 s98, v54, 8
	v_fmac_f32_e32 v40, s100, v24
	v_readlane_b32 s99, v54, 9
	v_fmac_f32_e32 v43, s0, v26
	v_readlane_b32 s100, v54, 10
	v_fmac_f32_e32 v40, s98, v28
	v_readlane_b32 s0, v54, 11
	v_fmac_f32_e32 v43, s99, v31
	v_readlane_b32 s98, v54, 12
	v_fmac_f32_e32 v40, s100, v32
	v_readlane_b32 s99, v54, 13
	v_fmac_f32_e32 v43, s0, v33
	v_readlane_b32 s100, v54, 14
	v_fmac_f32_e32 v40, s98, v34
	v_readlane_b32 s0, v54, 15
	v_fmac_f32_e32 v43, s99, v35
	v_readlane_b32 s98, v54, 16
	v_fmac_f32_e32 v40, s100, v36
	v_readlane_b32 s99, v42, 0
	v_fmac_f32_e32 v43, s0, v38
	v_readlane_b32 s100, v42, 1
	v_fmac_f32_e32 v40, s98, v39
	v_add_f32_e32 v40, v43, v40
	v_readlane_b32 s0, v42, 2
	v_fma_f32 v43, 0, s99, v42
	v_readlane_b32 s98, v42, 3
	v_fma_f32 v52, v27, s100, 0
	v_readlane_b32 s99, v42, 4
	v_fmac_f32_e32 v43, s0, v25
	v_readlane_b32 s100, v42, 5
	v_fmac_f32_e32 v52, s98, v23
	v_readlane_b32 s0, v42, 6
	v_fmac_f32_e32 v43, s99, v5
	v_readlane_b32 s98, v42, 7
	v_fmac_f32_e32 v52, s100, v22
	v_readlane_b32 s99, v42, 8
	v_fmac_f32_e32 v43, s0, v24
	v_readlane_b32 s100, v42, 9
	v_fmac_f32_e32 v52, s98, v26
	v_readlane_b32 s0, v42, 10
	v_fmac_f32_e32 v43, s99, v28
	v_readlane_b32 s98, v42, 11
	v_fmac_f32_e32 v52, s100, v31
	v_readlane_b32 s99, v42, 12
	v_fmac_f32_e32 v43, s0, v32
	v_readlane_b32 s100, v42, 13
	v_fmac_f32_e32 v52, s98, v33
	v_readlane_b32 s0, v42, 14
	v_fmac_f32_e32 v43, s99, v34
	v_readlane_b32 s98, v42, 15
	v_fmac_f32_e32 v52, s100, v35
	v_readlane_b32 s99, v42, 16
	v_fmac_f32_e32 v43, s0, v36
	v_readlane_b32 s100, v42, 17
	v_fmac_f32_e32 v52, s98, v38
	v_readlane_b32 s0, v46, 0
	v_fmac_f32_e32 v43, s99, v39
	v_readlane_b32 s98, v46, 1
	v_fmac_f32_e32 v52, s100, v40
	v_add_f32_e32 v42, v43, v52
	v_readlane_b32 s99, v46, 2
	v_fma_f32 v43, 0, s0, v46
	v_readlane_b32 s100, v46, 3
	v_fma_f32 v52, v27, s98, 0
	v_readlane_b32 s0, v46, 4
	v_fmac_f32_e32 v43, s99, v25
	v_readlane_b32 s98, v46, 5
	v_fmac_f32_e32 v52, s100, v23
	v_readlane_b32 s99, v46, 6
	v_fmac_f32_e32 v43, s0, v5
	v_readlane_b32 s100, v46, 7
	v_fmac_f32_e32 v52, s98, v22
	v_readlane_b32 s0, v46, 8
	v_fmac_f32_e32 v43, s99, v24
	v_readlane_b32 s98, v46, 9
	v_fmac_f32_e32 v52, s100, v26
	v_readlane_b32 s99, v46, 10
	v_fmac_f32_e32 v43, s0, v28
	v_readlane_b32 s100, v46, 11
	v_fmac_f32_e32 v52, s98, v31
	v_readlane_b32 s0, v46, 12
	v_fmac_f32_e32 v43, s99, v32
	v_readlane_b32 s98, v46, 13
	v_fmac_f32_e32 v52, s100, v33
	v_readlane_b32 s99, v46, 14
	v_fmac_f32_e32 v43, s0, v34
	v_readlane_b32 s100, v46, 15
	v_fmac_f32_e32 v52, s98, v35
	v_readlane_b32 s0, v46, 16
	v_fmac_f32_e32 v43, s99, v36
	v_readlane_b32 s98, v46, 17
	v_fmac_f32_e32 v52, s100, v38
	v_readlane_b32 s99, v46, 18
	v_fmac_f32_e32 v43, s0, v39
	v_readlane_b32 s100, v45, 0
	v_fmac_f32_e32 v52, s98, v40
; __device__ __forceinline__ void ph_gdn_prep(const Params& p, LAS unsigned char* lds) {
;     ...
;             for (int i = 1; i < 64; ++i) { const int mi = __float_as_int(mcol[i]); float a0 = mcol[i], a1 = 0.f;
; #pragma unroll
;                 for (int j = 0; j < i; ++j) { const float s = __int_as_float(__builtin_amdgcn_readlane(mi, j)); if (j & 1) a1 += s * mcol[j]; else a0 += s * mcol[j]; }
;                 mcol[i] = a0 + a1; }
	v_readlane_b32 s0, v45, 1
	v_fmac_f32_e32 v43, s99, v42
	v_add_f32_e32 v43, v52, v43
	v_readlane_b32 s98, v45, 2
	v_fma_f32 v46, 0, s100, v45
	v_readlane_b32 s99, v45, 3
	v_fma_f32 v52, v27, s0, 0
	v_readlane_b32 s100, v45, 4
	v_fmac_f32_e32 v46, s98, v25
	v_readlane_b32 s0, v45, 5
	v_fmac_f32_e32 v52, s99, v23
	v_readlane_b32 s98, v45, 6
	v_fmac_f32_e32 v46, s100, v5
	v_readlane_b32 s99, v45, 7
	v_fmac_f32_e32 v52, s0, v22
	v_readlane_b32 s100, v45, 8
	v_fmac_f32_e32 v46, s98, v24
	v_readlane_b32 s0, v45, 9
	v_fmac_f32_e32 v52, s99, v26
	v_readlane_b32 s98, v45, 10
	v_fmac_f32_e32 v46, s100, v28
	v_readlane_b32 s99, v45, 11
	v_fmac_f32_e32 v52, s0, v31
	v_readlane_b32 s100, v45, 12
	v_fmac_f32_e32 v46, s98, v32
	v_readlane_b32 s0, v45, 13
	v_fmac_f32_e32 v52, s99, v33
	v_readlane_b32 s98, v45, 14
	v_fmac_f32_e32 v46, s100, v34
	v_readlane_b32 s99, v45, 15
	v_fmac_f32_e32 v52, s0, v35
	v_readlane_b32 s100, v45, 16
	v_fmac_f32_e32 v46, s98, v36
	v_readlane_b32 s0, v45, 17
	v_fmac_f32_e32 v52, s99, v38
	v_readlane_b32 s98, v45, 18
	v_fmac_f32_e32 v46, s100, v39
	v_readlane_b32 s99, v45, 19
	v_fmac_f32_e32 v52, s0, v40
	v_readlane_b32 s100, v57, 0
	v_fmac_f32_e32 v46, s98, v42
	v_readlane_b32 s0, v57, 1
	v_fmac_f32_e32 v52, s99, v43
	v_add_f32_e32 v45, v46, v52
	v_readlane_b32 s98, v57, 2
	v_fma_f32 v46, 0, s100, v57
	v_readlane_b32 s99, v57, 3
	v_fma_f32 v52, v27, s0, 0
	v_readlane_b32 s100, v57, 4
	v_fmac_f32_e32 v46, s98, v25
	v_readlane_b32 s0, v57, 5
	v_fmac_f32_e32 v52, s99, v23
	v_readlane_b32 s98, v57, 6
	v_fmac_f32_e32 v46, s100, v5
	v_readlane_b32 s99, v57, 7
	v_fmac_f32_e32 v52, s0, v22
	v_readlane_b32 s100, v57, 8
	v_fmac_f32_e32 v46, s98, v24
	v_readlane_b32 s0, v57, 9
	v_fmac_f32_e32 v52, s99, v26
	v_readlane_b32 s98, v57, 10
	v_fmac_f32_e32 v46, s100, v28
	v_readlane_b32 s99, v57, 11
	v_fmac_f32_e32 v52, s0, v31
	v_readlane_b32 s100, v57, 12
	v_fmac_f32_e32 v46, s98, v32
	v_readlane_b32 s0, v57, 13
	v_fmac_f32_e32 v52, s99, v33
	v_readlane_b32 s98, v57, 14
	v_fmac_f32_e32 v46, s100, v34
	v_readlane_b32 s99, v57, 15
	v_fmac_f32_e32 v52, s0, v35
	v_readlane_b32 s100, v57, 16
	v_fmac_f32_e32 v46, s98, v36
	v_readlane_b32 s0, v57, 17
	v_fmac_f32_e32 v52, s99, v38
	v_readlane_b32 s98, v57, 18
	v_fmac_f32_e32 v46, s100, v39
	v_readlane_b32 s99, v57, 19
	v_fmac_f32_e32 v52, s0, v40
	v_readlane_b32 s100, v57, 20
	v_fmac_f32_e32 v46, s98, v42
	v_readlane_b32 s0, v47, 0
	v_fmac_f32_e32 v52, s99, v43
	v_readlane_b32 s98, v47, 1
	v_fmac_f32_e32 v46, s100, v45
	v_add_f32_e32 v46, v52, v46
	v_readlane_b32 s99, v47, 2
	v_fma_f32 v52, 0, s0, v47
	v_readlane_b32 s100, v47, 3
	v_fma_f32 v54, v27, s98, 0
	v_readlane_b32 s0, v47, 4
	v_fmac_f32_e32 v52, s99, v25
	v_readlane_b32 s98, v47, 5
	v_fmac_f32_e32 v54, s100, v23
	v_readlane_b32 s99, v47, 6
	v_fmac_f32_e32 v52, s0, v5
	v_readlane_b32 s100, v47, 7
	v_fmac_f32_e32 v54, s98, v22
	v_readlane_b32 s0, v47, 8
	v_fmac_f32_e32 v52, s99, v24
	v_readlane_b32 s98, v47, 9
	v_fmac_f32_e32 v54, s100, v26
	v_readlane_b32 s99, v47, 10
	v_fmac_f32_e32 v52, s0, v28
	v_readlane_b32 s100, v47, 11
	v_fmac_f32_e32 v54, s98, v31
	v_readlane_b32 s0, v47, 12
	v_fmac_f32_e32 v52, s99, v32
	v_readlane_b32 s98, v47, 13
	v_fmac_f32_e32 v54, s100, v33
	v_readlane_b32 s99, v47, 14
	v_fmac_f32_e32 v52, s0, v34
	v_readlane_b32 s100, v47, 15
	v_fmac_f32_e32 v54, s98, v35
	v_readlane_b32 s0, v47, 16
	v_fmac_f32_e32 v52, s99, v36
	v_readlane_b32 s98, v47, 17
	v_fmac_f32_e32 v54, s100, v38
	v_readlane_b32 s99, v47, 18
	v_fmac_f32_e32 v52, s0, v39
	v_readlane_b32 s100, v47, 19
	v_fmac_f32_e32 v54, s98, v40
	v_readlane_b32 s0, v47, 20
	v_fmac_f32_e32 v52, s99, v42
	v_readlane_b32 s98, v47, 21
	v_fmac_f32_e32 v54, s100, v43
	v_readlane_b32 s99, v49, 0
	v_fmac_f32_e32 v52, s0, v45
	v_readlane_b32 s100, v49, 1
	v_fmac_f32_e32 v54, s98, v46
	v_add_f32_e32 v47, v52, v54
	v_readlane_b32 s0, v49, 2
	v_fma_f32 v52, 0, s99, v49
	v_readlane_b32 s98, v49, 3
	v_fma_f32 v54, v27, s100, 0
	v_readlane_b32 s99, v49, 4
	v_fmac_f32_e32 v52, s0, v25
	v_readlane_b32 s100, v49, 5
	v_fmac_f32_e32 v54, s98, v23
	v_readlane_b32 s0, v49, 6
	v_fmac_f32_e32 v52, s99, v5
	v_readlane_b32 s98, v49, 7
	v_fmac_f32_e32 v54, s100, v22
	v_readlane_b32 s99, v49, 8
	v_fmac_f32_e32 v52, s0, v24
	v_readlane_b32 s100, v49, 9
	v_fmac_f32_e32 v54, s98, v26
	v_readlane_b32 s0, v49, 10
	v_fmac_f32_e32 v52, s99, v28
	v_readlane_b32 s98, v49, 11
	v_fmac_f32_e32 v54, s100, v31
	v_readlane_b32 s99, v49, 12
	v_fmac_f32_e32 v52, s0, v32
	v_readlane_b32 s100, v49, 13
	v_fmac_f32_e32 v54, s98, v33
	v_readlane_b32 s0, v49, 14
	v_fmac_f32_e32 v52, s99, v34
	v_readlane_b32 s98, v49, 15
	v_fmac_f32_e32 v54, s100, v35
	v_readlane_b32 s99, v49, 16
	v_fmac_f32_e32 v52, s0, v36
	v_readlane_b32 s100, v49, 17
	v_fmac_f32_e32 v54, s98, v38
	v_readlane_b32 s0, v49, 18
	v_fmac_f32_e32 v52, s99, v39
	v_readlane_b32 s98, v49, 19
	v_fmac_f32_e32 v54, s100, v40
	v_readlane_b32 s99, v49, 20
	v_fmac_f32_e32 v52, s0, v42
	v_readlane_b32 s100, v49, 21
	v_fmac_f32_e32 v54, s98, v43
	v_readlane_b32 s0, v49, 22
	v_fmac_f32_e32 v52, s99, v45
	v_readlane_b32 s98, v51, 0
	v_fmac_f32_e32 v54, s100, v46
	v_readlane_b32 s99, v51, 1
	v_fmac_f32_e32 v52, s0, v47
	v_add_f32_e32 v49, v54, v52
	v_readlane_b32 s100, v51, 2
	v_fma_f32 v52, 0, s98, v51
	v_readlane_b32 s0, v51, 3
	v_fma_f32 v54, v27, s99, 0
	v_readlane_b32 s98, v51, 4
	v_fmac_f32_e32 v52, s100, v25
	v_readlane_b32 s99, v51, 5
	v_fmac_f32_e32 v54, s0, v23
	v_readlane_b32 s100, v51, 6
	v_fmac_f32_e32 v52, s98, v5
	v_readlane_b32 s0, v51, 7
	v_fmac_f32_e32 v54, s99, v22
	v_readlane_b32 s98, v51, 8
	v_fmac_f32_e32 v52, s100, v24
	v_readlane_b32 s99, v51, 9
; __device__ __forceinline__ void ph_gdn_prep(const Params& p, LAS unsigned char* lds) {
;     ...
;             for (int i = 1; i < 64; ++i) { const int mi = __float_as_int(mcol[i]); float a0 = mcol[i], a1 = 0.f;
; #pragma unroll
;                 for (int j = 0; j < i; ++j) { const float s = __int_as_float(__builtin_amdgcn_readlane(mi, j)); if (j & 1) a1 += s * mcol[j]; else a0 += s * mcol[j]; }
;                 mcol[i] = a0 + a1; }
	v_fmac_f32_e32 v54, s0, v26
	v_readlane_b32 s100, v51, 10
	v_fmac_f32_e32 v52, s98, v28
	v_readlane_b32 s0, v51, 11
	v_fmac_f32_e32 v54, s99, v31
	v_readlane_b32 s98, v51, 12
	v_fmac_f32_e32 v52, s100, v32
	v_readlane_b32 s99, v51, 13
	v_fmac_f32_e32 v54, s0, v33
	v_readlane_b32 s100, v51, 14
	v_fmac_f32_e32 v52, s98, v34
	v_readlane_b32 s0, v51, 15
	v_fmac_f32_e32 v54, s99, v35
	v_readlane_b32 s98, v51, 16
	v_fmac_f32_e32 v52, s100, v36
	v_readlane_b32 s99, v51, 17
	v_fmac_f32_e32 v54, s0, v38
	v_readlane_b32 s100, v51, 18
	v_fmac_f32_e32 v52, s98, v39
	v_readlane_b32 s0, v51, 19
	v_fmac_f32_e32 v54, s99, v40
	v_readlane_b32 s98, v51, 20
	v_fmac_f32_e32 v52, s100, v42
	v_readlane_b32 s99, v51, 21
	v_fmac_f32_e32 v54, s0, v43
	v_readlane_b32 s100, v51, 22
	v_fmac_f32_e32 v52, s98, v45
	v_readlane_b32 s0, v51, 23
	v_fmac_f32_e32 v54, s99, v46
	v_readlane_b32 s98, v61, 0
	v_fmac_f32_e32 v52, s100, v47
	v_readlane_b32 s99, v61, 1
	v_fmac_f32_e32 v54, s0, v49
	v_add_f32_e32 v51, v52, v54
	v_readlane_b32 s100, v61, 2
	v_fma_f32 v52, 0, s98, v61
	v_readlane_b32 s0, v61, 3
	v_fma_f32 v54, v27, s99, 0
	v_readlane_b32 s98, v61, 4
	v_fmac_f32_e32 v52, s100, v25
	v_readlane_b32 s99, v61, 5
	v_fmac_f32_e32 v54, s0, v23
	v_readlane_b32 s100, v61, 6
	v_fmac_f32_e32 v52, s98, v5
	v_readlane_b32 s0, v61, 7
	v_fmac_f32_e32 v54, s99, v22
	v_readlane_b32 s98, v61, 8
	v_fmac_f32_e32 v52, s100, v24
	v_readlane_b32 s99, v61, 9
	v_fmac_f32_e32 v54, s0, v26
	v_readlane_b32 s100, v61, 10
	v_fmac_f32_e32 v52, s98, v28
	v_readlane_b32 s0, v61, 11
	v_fmac_f32_e32 v54, s99, v31
	v_readlane_b32 s98, v61, 12
	v_fmac_f32_e32 v52, s100, v32
	v_readlane_b32 s99, v61, 13
	v_fmac_f32_e32 v54, s0, v33
	v_readlane_b32 s100, v61, 14
	v_fmac_f32_e32 v52, s98, v34
	v_readlane_b32 s0, v61, 15
	v_fmac_f32_e32 v54, s99, v35
	v_readlane_b32 s98, v61, 16
	v_fmac_f32_e32 v52, s100, v36
	v_readlane_b32 s99, v61, 17
	v_fmac_f32_e32 v54, s0, v38
	v_readlane_b32 s100, v61, 18
	v_fmac_f32_e32 v52, s98, v39
	v_readlane_b32 s0, v61, 19
	v_fmac_f32_e32 v54, s99, v40
	v_readlane_b32 s98, v61, 20
	v_fmac_f32_e32 v52, s100, v42
	v_readlane_b32 s99, v61, 21
	v_fmac_f32_e32 v54, s0, v43
	v_readlane_b32 s100, v61, 22
	v_fmac_f32_e32 v52, s98, v45
	v_readlane_b32 s0, v61, 23
	v_fmac_f32_e32 v54, s99, v46
	v_readlane_b32 s98, v61, 24
	v_fmac_f32_e32 v52, s100, v47
	v_readlane_b32 s99, v59, 0
	v_fmac_f32_e32 v54, s0, v49
	v_readlane_b32 s100, v59, 1
	v_fmac_f32_e32 v52, s98, v51
	v_add_f32_e32 v52, v54, v52
	v_readlane_b32 s0, v59, 2
	v_fma_f32 v54, 0, s99, v59
	v_readlane_b32 s98, v59, 3
	v_fma_f32 v56, v27, s100, 0
	v_readlane_b32 s99, v59, 4
	v_fmac_f32_e32 v54, s0, v25
	v_readlane_b32 s100, v59, 5
	v_fmac_f32_e32 v56, s98, v23
	v_readlane_b32 s0, v59, 6
	v_fmac_f32_e32 v54, s99, v5
	v_readlane_b32 s98, v59, 7
	v_fmac_f32_e32 v56, s100, v22
	v_readlane_b32 s99, v59, 8
	v_fmac_f32_e32 v54, s0, v24
	v_readlane_b32 s100, v59, 9
	v_fmac_f32_e32 v56, s98, v26
	v_readlane_b32 s0, v59, 10
	v_fmac_f32_e32 v54, s99, v28
	v_readlane_b32 s98, v59, 11
	v_fmac_f32_e32 v56, s100, v31
	v_readlane_b32 s99, v59, 12
	v_fmac_f32_e32 v54, s0, v32
	v_readlane_b32 s100, v59, 13
	v_fmac_f32_e32 v56, s98, v33
	v_readlane_b32 s0, v59, 14
	v_fmac_f32_e32 v54, s99, v34
	v_readlane_b32 s98, v59, 15
	v_fmac_f32_e32 v56, s100, v35
	v_readlane_b32 s99, v59, 16
	v_fmac_f32_e32 v54, s0, v36
	v_readlane_b32 s100, v59, 17
	v_fmac_f32_e32 v56, s98, v38
	v_readlane_b32 s0, v59, 18
	v_fmac_f32_e32 v54, s99, v39
	v_readlane_b32 s98, v59, 19
	v_fmac_f32_e32 v56, s100, v40
	v_readlane_b32 s99, v59, 20
	v_fmac_f32_e32 v54, s0, v42
	v_readlane_b32 s100, v59, 21
	v_fmac_f32_e32 v56, s98, v43
	v_readlane_b32 s0, v59, 22
	v_fmac_f32_e32 v54, s99, v45
	v_readlane_b32 s98, v59, 23
	v_fmac_f32_e32 v56, s100, v46
	v_readlane_b32 s99, v59, 24
	v_fmac_f32_e32 v54, s0, v47
	v_readlane_b32 s100, v59, 25
	v_fmac_f32_e32 v56, s98, v49
	v_readlane_b32 s0, v68, 0
	v_fmac_f32_e32 v54, s99, v51
	v_readlane_b32 s98, v68, 1
	v_fmac_f32_e32 v56, s100, v52
	v_add_f32_e32 v54, v54, v56
	v_readlane_b32 s99, v68, 2
	v_fma_f32 v56, 0, s0, v68
	v_readlane_b32 s100, v68, 3
	v_fma_f32 v57, v27, s98, 0
	v_readlane_b32 s0, v68, 4
	v_fmac_f32_e32 v56, s99, v25
	v_readlane_b32 s98, v68, 5
	v_fmac_f32_e32 v57, s100, v23
	v_readlane_b32 s99, v68, 6
	v_fmac_f32_e32 v56, s0, v5
	v_readlane_b32 s100, v68, 7
	v_fmac_f32_e32 v57, s98, v22
	v_readlane_b32 s0, v68, 8
	v_fmac_f32_e32 v56, s99, v24
	v_readlane_b32 s98, v68, 9
	v_fmac_f32_e32 v57, s100, v26
	v_readlane_b32 s99, v68, 10
	v_fmac_f32_e32 v56, s0, v28
	v_readlane_b32 s100, v68, 11
	v_fmac_f32_e32 v57, s98, v31
	v_readlane_b32 s0, v68, 12
	v_fmac_f32_e32 v56, s99, v32
	v_readlane_b32 s98, v68, 13
	v_fmac_f32_e32 v57, s100, v33
	v_readlane_b32 s99, v68, 14
	v_fmac_f32_e32 v56, s0, v34
	v_readlane_b32 s100, v68, 15
	v_fmac_f32_e32 v57, s98, v35
	v_readlane_b32 s0, v68, 16
	v_fmac_f32_e32 v56, s99, v36
	v_readlane_b32 s98, v68, 17
	v_fmac_f32_e32 v57, s100, v38
	v_readlane_b32 s99, v68, 18
	v_fmac_f32_e32 v56, s0, v39
	v_readlane_b32 s100, v68, 19
	v_fmac_f32_e32 v57, s98, v40
	v_readlane_b32 s0, v68, 20
	v_fmac_f32_e32 v56, s99, v42
	v_readlane_b32 s98, v68, 21
	v_fmac_f32_e32 v57, s100, v43
	v_readlane_b32 s99, v68, 22
	v_fmac_f32_e32 v56, s0, v45
	v_readlane_b32 s100, v68, 23
	v_fmac_f32_e32 v57, s98, v46
	v_readlane_b32 s0, v68, 24
	v_fmac_f32_e32 v56, s99, v47
	v_readlane_b32 s98, v68, 25
	v_fmac_f32_e32 v57, s100, v49
	v_readlane_b32 s99, v68, 26
	v_fmac_f32_e32 v56, s0, v51
	v_readlane_b32 s100, v66, 0
	v_fmac_f32_e32 v57, s98, v52
	v_readlane_b32 s0, v66, 1
	v_fmac_f32_e32 v56, s99, v54
	v_add_f32_e32 v56, v57, v56
; __device__ __forceinline__ void ph_gdn_prep(const Params& p, LAS unsigned char* lds) {
;     ...
;             for (int i = 1; i < 64; ++i) { const int mi = __float_as_int(mcol[i]); float a0 = mcol[i], a1 = 0.f;
; #pragma unroll
;                 for (int j = 0; j < i; ++j) { const float s = __int_as_float(__builtin_amdgcn_readlane(mi, j)); if (j & 1) a1 += s * mcol[j]; else a0 += s * mcol[j]; }
;                 mcol[i] = a0 + a1; }
	v_readlane_b32 s98, v66, 2
	v_fma_f32 v57, 0, s100, v66
	v_readlane_b32 s99, v66, 3
	v_fma_f32 v59, v27, s0, 0
	v_readlane_b32 s100, v66, 4
	v_fmac_f32_e32 v57, s98, v25
	v_readlane_b32 s0, v66, 5
	v_fmac_f32_e32 v59, s99, v23
	v_readlane_b32 s98, v66, 6
	v_fmac_f32_e32 v57, s100, v5
	v_readlane_b32 s99, v66, 7
	v_fmac_f32_e32 v59, s0, v22
	v_readlane_b32 s100, v66, 8
	v_fmac_f32_e32 v57, s98, v24
	v_readlane_b32 s0, v66, 9
	v_fmac_f32_e32 v59, s99, v26
	v_readlane_b32 s98, v66, 10
	v_fmac_f32_e32 v57, s100, v28
	v_readlane_b32 s99, v66, 11
	v_fmac_f32_e32 v59, s0, v31
	v_readlane_b32 s100, v66, 12
	v_fmac_f32_e32 v57, s98, v32
	v_readlane_b32 s0, v66, 13
	v_fmac_f32_e32 v59, s99, v33
	v_readlane_b32 s98, v66, 14
	v_fmac_f32_e32 v57, s100, v34
	v_readlane_b32 s99, v66, 15
	v_fmac_f32_e32 v59, s0, v35
	v_readlane_b32 s100, v66, 16
	v_fmac_f32_e32 v57, s98, v36
	v_readlane_b32 s0, v66, 17
	v_fmac_f32_e32 v59, s99, v38
	v_readlane_b32 s98, v66, 18
	v_fmac_f32_e32 v57, s100, v39
	v_readlane_b32 s99, v66, 19
	v_fmac_f32_e32 v59, s0, v40
	v_readlane_b32 s100, v66, 20
	v_fmac_f32_e32 v57, s98, v42
	v_readlane_b32 s0, v66, 21
	v_fmac_f32_e32 v59, s99, v43
	v_readlane_b32 s98, v66, 22
	v_fmac_f32_e32 v57, s100, v45
	v_readlane_b32 s99, v66, 23
	v_fmac_f32_e32 v59, s0, v46
	v_readlane_b32 s100, v66, 24
	v_fmac_f32_e32 v57, s98, v47
	v_readlane_b32 s0, v66, 25
	v_fmac_f32_e32 v59, s99, v49
	v_readlane_b32 s98, v66, 26
	v_fmac_f32_e32 v57, s100, v51
	v_readlane_b32 s99, v66, 27
	v_fmac_f32_e32 v59, s0, v52
	v_readlane_b32 s100, v67, 0
	v_fmac_f32_e32 v57, s98, v54
	v_readlane_b32 s0, v67, 1
	v_fmac_f32_e32 v59, s99, v56
	v_add_f32_e32 v57, v57, v59
	v_readlane_b32 s98, v67, 2
	v_fma_f32 v59, 0, s100, v67
	v_readlane_b32 s99, v67, 3
	v_fma_f32 v61, v27, s0, 0
	v_readlane_b32 s100, v67, 4
	v_fmac_f32_e32 v59, s98, v25
	v_readlane_b32 s0, v67, 5
	v_fmac_f32_e32 v61, s99, v23
	v_readlane_b32 s98, v67, 6
	v_fmac_f32_e32 v59, s100, v5
	v_readlane_b32 s99, v67, 7
	v_fmac_f32_e32 v61, s0, v22
	v_readlane_b32 s100, v67, 8
	v_fmac_f32_e32 v59, s98, v24
	v_readlane_b32 s0, v67, 9
	v_fmac_f32_e32 v61, s99, v26
	v_readlane_b32 s98, v67, 10
	v_fmac_f32_e32 v59, s100, v28
	v_readlane_b32 s99, v67, 11
	v_fmac_f32_e32 v61, s0, v31
	v_readlane_b32 s100, v67, 12
	v_fmac_f32_e32 v59, s98, v32
	v_readlane_b32 s0, v67, 13
	v_fmac_f32_e32 v61, s99, v33
	v_readlane_b32 s98, v67, 14
	v_fmac_f32_e32 v59, s100, v34
	v_readlane_b32 s99, v67, 15
	v_fmac_f32_e32 v61, s0, v35
	v_readlane_b32 s100, v67, 16
	v_fmac_f32_e32 v59, s98, v36
	v_readlane_b32 s0, v67, 17
	v_fmac_f32_e32 v61, s99, v38
	v_readlane_b32 s98, v67, 18
	v_fmac_f32_e32 v59, s100, v39
	v_readlane_b32 s99, v67, 19
	v_fmac_f32_e32 v61, s0, v40
	v_readlane_b32 s100, v67, 20
	v_fmac_f32_e32 v59, s98, v42
	v_readlane_b32 s0, v67, 21
	v_fmac_f32_e32 v61, s99, v43
	v_readlane_b32 s98, v67, 22
	v_fmac_f32_e32 v59, s100, v45
	v_readlane_b32 s99, v67, 23
	v_fmac_f32_e32 v61, s0, v46
	v_readlane_b32 s100, v67, 24
	v_fmac_f32_e32 v59, s98, v47
	v_readlane_b32 s0, v67, 25
	v_fmac_f32_e32 v61, s99, v49
	v_readlane_b32 s98, v67, 26
	v_fmac_f32_e32 v59, s100, v51
	v_readlane_b32 s99, v67, 27
	v_fmac_f32_e32 v61, s0, v52
	v_readlane_b32 s100, v67, 28
	v_fmac_f32_e32 v59, s98, v54
	v_readlane_b32 s0, v65, 0
	v_fmac_f32_e32 v61, s99, v56
	v_readlane_b32 s98, v65, 1
	v_fmac_f32_e32 v59, s100, v57
	v_add_f32_e32 v59, v61, v59
	v_readlane_b32 s99, v65, 2
	v_fma_f32 v61, 0, s0, v65
	v_readlane_b32 s100, v65, 3
	v_fma_f32 v66, v27, s98, 0
	v_readlane_b32 s0, v65, 4
	v_fmac_f32_e32 v61, s99, v25
	v_readlane_b32 s98, v65, 5
	v_fmac_f32_e32 v66, s100, v23
	v_readlane_b32 s99, v65, 6
	v_fmac_f32_e32 v61, s0, v5
	v_readlane_b32 s100, v65, 7
	v_fmac_f32_e32 v66, s98, v22
	v_readlane_b32 s0, v65, 8
	v_fmac_f32_e32 v61, s99, v24
	v_readlane_b32 s98, v65, 9
	v_fmac_f32_e32 v66, s100, v26
	v_readlane_b32 s99, v65, 10
	v_fmac_f32_e32 v61, s0, v28
	v_readlane_b32 s100, v65, 11
	v_fmac_f32_e32 v66, s98, v31
	v_readlane_b32 s0, v65, 12
	v_fmac_f32_e32 v61, s99, v32
	v_readlane_b32 s98, v65, 13
	v_fmac_f32_e32 v66, s100, v33
	v_readlane_b32 s99, v65, 14
	v_fmac_f32_e32 v61, s0, v34
	v_readlane_b32 s100, v65, 15
	v_fmac_f32_e32 v66, s98, v35
	v_readlane_b32 s0, v65, 16
	v_fmac_f32_e32 v61, s99, v36
	v_readlane_b32 s98, v65, 17
	v_fmac_f32_e32 v66, s100, v38
	v_readlane_b32 s99, v65, 18
	v_fmac_f32_e32 v61, s0, v39
	v_readlane_b32 s100, v65, 19
	v_fmac_f32_e32 v66, s98, v40
	v_readlane_b32 s0, v65, 20
	v_fmac_f32_e32 v61, s99, v42
	v_readlane_b32 s98, v65, 21
	v_fmac_f32_e32 v66, s100, v43
	v_readlane_b32 s99, v65, 22
	v_fmac_f32_e32 v61, s0, v45
	v_readlane_b32 s100, v65, 23
	v_fmac_f32_e32 v66, s98, v46
	v_readlane_b32 s0, v65, 24
	v_fmac_f32_e32 v61, s99, v47
	v_readlane_b32 s98, v65, 25
	v_fmac_f32_e32 v66, s100, v49
	v_readlane_b32 s99, v65, 26
	v_fmac_f32_e32 v61, s0, v51
	v_readlane_b32 s100, v65, 27
	v_fmac_f32_e32 v66, s98, v52
	v_readlane_b32 s0, v65, 28
	v_fmac_f32_e32 v61, s99, v54
	v_readlane_b32 s98, v65, 29
	v_fmac_f32_e32 v66, s100, v56
	v_readlane_b32 s99, v63, 0
	v_fmac_f32_e32 v61, s0, v57
	v_readlane_b32 s100, v63, 1
	v_fmac_f32_e32 v66, s98, v59
	v_add_f32_e32 v61, v61, v66
	v_readlane_b32 s0, v63, 2
	v_fma_f32 v65, 0, s99, v63
	v_readlane_b32 s98, v63, 3
	v_fma_f32 v66, v27, s100, 0
	v_readlane_b32 s99, v63, 4
	v_fmac_f32_e32 v65, s0, v25
	v_readlane_b32 s100, v63, 5
	v_fmac_f32_e32 v66, s98, v23
	v_readlane_b32 s0, v63, 6
	v_fmac_f32_e32 v65, s99, v5
	v_readlane_b32 s98, v63, 7
	v_fmac_f32_e32 v66, s100, v22
	v_readlane_b32 s99, v63, 8
	v_fmac_f32_e32 v65, s0, v24
	v_readlane_b32 s100, v63, 9
	v_fmac_f32_e32 v66, s98, v26
; __device__ __forceinline__ void ph_gdn_prep(const Params& p, LAS unsigned char* lds) {
;     ...
;             for (int i = 1; i < 64; ++i) { const int mi = __float_as_int(mcol[i]); float a0 = mcol[i], a1 = 0.f;
; #pragma unroll
;                 for (int j = 0; j < i; ++j) { const float s = __int_as_float(__builtin_amdgcn_readlane(mi, j)); if (j & 1) a1 += s * mcol[j]; else a0 += s * mcol[j]; }
;                 mcol[i] = a0 + a1; }
	v_readlane_b32 s0, v63, 10
	v_fmac_f32_e32 v65, s99, v28
	v_readlane_b32 s98, v63, 11
	v_fmac_f32_e32 v66, s100, v31
	v_readlane_b32 s99, v63, 12
	v_fmac_f32_e32 v65, s0, v32
	v_readlane_b32 s100, v63, 13
	v_fmac_f32_e32 v66, s98, v33
	v_readlane_b32 s0, v63, 14
	v_fmac_f32_e32 v65, s99, v34
	v_readlane_b32 s98, v63, 15
	v_fmac_f32_e32 v66, s100, v35
	v_readlane_b32 s99, v63, 16
	v_fmac_f32_e32 v65, s0, v36
	v_readlane_b32 s100, v63, 17
	v_fmac_f32_e32 v66, s98, v38
	v_readlane_b32 s0, v63, 18
	v_fmac_f32_e32 v65, s99, v39
	v_readlane_b32 s98, v63, 19
	v_fmac_f32_e32 v66, s100, v40
	v_readlane_b32 s99, v63, 20
	v_fmac_f32_e32 v65, s0, v42
	v_readlane_b32 s100, v63, 21
	v_fmac_f32_e32 v66, s98, v43
	v_readlane_b32 s0, v63, 22
	v_fmac_f32_e32 v65, s99, v45
	v_readlane_b32 s98, v63, 23
	v_fmac_f32_e32 v66, s100, v46
	v_readlane_b32 s99, v63, 24
	v_fmac_f32_e32 v65, s0, v47
	v_readlane_b32 s100, v63, 25
	v_fmac_f32_e32 v66, s98, v49
	v_readlane_b32 s0, v63, 26
	v_fmac_f32_e32 v65, s99, v51
	v_readlane_b32 s98, v63, 27
	v_fmac_f32_e32 v66, s100, v52
	v_readlane_b32 s99, v63, 28
	v_fmac_f32_e32 v65, s0, v54
	v_readlane_b32 s100, v63, 29
	v_fmac_f32_e32 v66, s98, v56
	v_readlane_b32 s0, v63, 30
	v_fmac_f32_e32 v65, s99, v57
	v_readlane_b32 s98, v64, 0
	v_fmac_f32_e32 v66, s100, v59
	v_readlane_b32 s99, v64, 1
	v_fmac_f32_e32 v65, s0, v61
	v_add_f32_e32 v63, v66, v65
	v_readlane_b32 s100, v64, 2
	v_fma_f32 v65, 0, s98, v64
	v_readlane_b32 s0, v64, 3
	v_fma_f32 v66, v27, s99, 0
	v_readlane_b32 s98, v64, 4
	v_fmac_f32_e32 v65, s100, v25
	v_readlane_b32 s99, v64, 5
	v_fmac_f32_e32 v66, s0, v23
	v_readlane_b32 s100, v64, 6
	v_fmac_f32_e32 v65, s98, v5
	v_readlane_b32 s0, v64, 7
	v_fmac_f32_e32 v66, s99, v22
	v_readlane_b32 s98, v64, 8
	v_fmac_f32_e32 v65, s100, v24
	v_readlane_b32 s99, v64, 9
	v_fmac_f32_e32 v66, s0, v26
	v_readlane_b32 s100, v64, 10
	v_fmac_f32_e32 v65, s98, v28
	v_readlane_b32 s0, v64, 11
	v_fmac_f32_e32 v66, s99, v31
	v_readlane_b32 s98, v64, 12
	v_fmac_f32_e32 v65, s100, v32
	v_readlane_b32 s99, v64, 13
	v_fmac_f32_e32 v66, s0, v33
	v_readlane_b32 s100, v64, 14
	v_fmac_f32_e32 v65, s98, v34
	v_readlane_b32 s0, v64, 15
	v_fmac_f32_e32 v66, s99, v35
	v_readlane_b32 s98, v64, 16
	v_fmac_f32_e32 v65, s100, v36
	v_readlane_b32 s99, v64, 17
	v_fmac_f32_e32 v66, s0, v38
	v_readlane_b32 s100, v64, 18
	v_fmac_f32_e32 v65, s98, v39
	v_readlane_b32 s0, v64, 19
	v_fmac_f32_e32 v66, s99, v40
	v_readlane_b32 s98, v64, 20
	v_fmac_f32_e32 v65, s100, v42
	v_readlane_b32 s99, v64, 21
	v_fmac_f32_e32 v66, s0, v43
	v_readlane_b32 s100, v64, 22
	v_fmac_f32_e32 v65, s98, v45
	v_readlane_b32 s0, v64, 23
	v_fmac_f32_e32 v66, s99, v46
	v_readlane_b32 s98, v64, 24
	v_fmac_f32_e32 v65, s100, v47
	v_readlane_b32 s99, v64, 25
	v_fmac_f32_e32 v66, s0, v49
	v_readlane_b32 s100, v64, 26
	v_fmac_f32_e32 v65, s98, v51
	v_readlane_b32 s0, v64, 27
	v_fmac_f32_e32 v66, s99, v52
	v_readlane_b32 s98, v64, 28
	v_fmac_f32_e32 v65, s100, v54
	v_readlane_b32 s99, v64, 29
	v_fmac_f32_e32 v66, s0, v56
	v_readlane_b32 s100, v64, 30
	v_fmac_f32_e32 v65, s98, v57
	v_readlane_b32 s0, v64, 31
	v_fmac_f32_e32 v66, s99, v59
	v_readlane_b32 s98, v62, 0
	v_fmac_f32_e32 v65, s100, v61
	v_readlane_b32 s99, v62, 1
	v_fmac_f32_e32 v66, s0, v63
	v_add_f32_e32 v64, v65, v66
	v_readlane_b32 s100, v62, 2
	v_fma_f32 v65, 0, s98, v62
	v_readlane_b32 s0, v62, 3
	v_fma_f32 v66, v27, s99, 0
	v_readlane_b32 s98, v62, 4
	v_fmac_f32_e32 v65, s100, v25
	v_readlane_b32 s99, v62, 5
	v_fmac_f32_e32 v66, s0, v23
	v_readlane_b32 s100, v62, 6
	v_fmac_f32_e32 v65, s98, v5
	v_readlane_b32 s0, v62, 7
	v_fmac_f32_e32 v66, s99, v22
	v_readlane_b32 s98, v62, 8
	v_fmac_f32_e32 v65, s100, v24
	v_readlane_b32 s99, v62, 9
	v_fmac_f32_e32 v66, s0, v26
	v_readlane_b32 s100, v62, 10
	v_fmac_f32_e32 v65, s98, v28
	v_readlane_b32 s0, v62, 11
	v_fmac_f32_e32 v66, s99, v31
	v_readlane_b32 s98, v62, 12
	v_fmac_f32_e32 v65, s100, v32
	v_readlane_b32 s99, v62, 13
	v_fmac_f32_e32 v66, s0, v33
	v_readlane_b32 s100, v62, 14
	v_fmac_f32_e32 v65, s98, v34
	v_readlane_b32 s0, v62, 15
	v_fmac_f32_e32 v66, s99, v35
	v_readlane_b32 s98, v62, 16
	v_fmac_f32_e32 v65, s100, v36
	v_readlane_b32 s99, v62, 17
	v_fmac_f32_e32 v66, s0, v38
	v_readlane_b32 s100, v62, 18
	v_fmac_f32_e32 v65, s98, v39
	v_readlane_b32 s0, v62, 19
	v_fmac_f32_e32 v66, s99, v40
	v_readlane_b32 s98, v62, 20
	v_fmac_f32_e32 v65, s100, v42
	v_readlane_b32 s99, v62, 21
	v_fmac_f32_e32 v66, s0, v43
	v_readlane_b32 s100, v62, 22
	v_fmac_f32_e32 v65, s98, v45
	v_readlane_b32 s0, v62, 23
	v_fmac_f32_e32 v66, s99, v46
	v_readlane_b32 s98, v62, 24
	v_fmac_f32_e32 v65, s100, v47
	v_readlane_b32 s99, v62, 25
	v_fmac_f32_e32 v66, s0, v49
	v_readlane_b32 s100, v62, 26
	v_fmac_f32_e32 v65, s98, v51
	v_readlane_b32 s0, v62, 27
	v_fmac_f32_e32 v66, s99, v52
	v_readlane_b32 s98, v62, 28
	v_fmac_f32_e32 v65, s100, v54
	v_readlane_b32 s99, v62, 29
	v_fmac_f32_e32 v66, s0, v56
	v_readlane_b32 s100, v62, 30
	v_fmac_f32_e32 v65, s98, v57
	v_readlane_b32 s0, v62, 31
	v_fmac_f32_e32 v66, s99, v59
	v_readlane_b32 s98, v62, 32
	v_fmac_f32_e32 v65, s100, v61
	v_readlane_b32 s99, v60, 0
	v_fmac_f32_e32 v66, s0, v63
	v_readlane_b32 s100, v60, 1
	v_fmac_f32_e32 v65, s98, v64
	v_add_f32_e32 v62, v66, v65
	v_readlane_b32 s0, v60, 2
	v_fma_f32 v65, 0, s99, v60
	v_readlane_b32 s98, v60, 3
	v_fma_f32 v66, v27, s100, 0
	v_readlane_b32 s99, v60, 4
	v_fmac_f32_e32 v65, s0, v25
	v_readlane_b32 s100, v60, 5
	v_fmac_f32_e32 v66, s98, v23
	v_readlane_b32 s0, v60, 6
	v_fmac_f32_e32 v65, s99, v5
	v_readlane_b32 s98, v60, 7
	v_fmac_f32_e32 v66, s100, v22
	v_readlane_b32 s99, v60, 8
	v_fmac_f32_e32 v65, s0, v24
; __device__ __forceinline__ void ph_gdn_prep(const Params& p, LAS unsigned char* lds) {
;     ...
;             for (int i = 1; i < 64; ++i) { const int mi = __float_as_int(mcol[i]); float a0 = mcol[i], a1 = 0.f;
; #pragma unroll
;                 for (int j = 0; j < i; ++j) { const float s = __int_as_float(__builtin_amdgcn_readlane(mi, j)); if (j & 1) a1 += s * mcol[j]; else a0 += s * mcol[j]; }
;                 mcol[i] = a0 + a1; }
	v_readlane_b32 s100, v60, 9
	v_fmac_f32_e32 v66, s98, v26
	v_readlane_b32 s0, v60, 10
	v_fmac_f32_e32 v65, s99, v28
	v_readlane_b32 s98, v60, 11
	v_fmac_f32_e32 v66, s100, v31
	v_readlane_b32 s99, v60, 12
	v_fmac_f32_e32 v65, s0, v32
	v_readlane_b32 s100, v60, 13
	v_fmac_f32_e32 v66, s98, v33
	v_readlane_b32 s0, v60, 14
	v_fmac_f32_e32 v65, s99, v34
	v_readlane_b32 s98, v60, 15
	v_fmac_f32_e32 v66, s100, v35
	v_readlane_b32 s99, v60, 16
	v_fmac_f32_e32 v65, s0, v36
	v_readlane_b32 s100, v60, 17
	v_fmac_f32_e32 v66, s98, v38
	v_readlane_b32 s0, v60, 18
	v_fmac_f32_e32 v65, s99, v39
	v_readlane_b32 s98, v60, 19
	v_fmac_f32_e32 v66, s100, v40
	v_readlane_b32 s99, v60, 20
	v_fmac_f32_e32 v65, s0, v42
	v_readlane_b32 s100, v60, 21
	v_fmac_f32_e32 v66, s98, v43
	v_readlane_b32 s0, v60, 22
	v_fmac_f32_e32 v65, s99, v45
	v_readlane_b32 s98, v60, 23
	v_fmac_f32_e32 v66, s100, v46
	v_readlane_b32 s99, v60, 24
	v_fmac_f32_e32 v65, s0, v47
	v_readlane_b32 s100, v60, 25
	v_fmac_f32_e32 v66, s98, v49
	v_readlane_b32 s0, v60, 26
	v_fmac_f32_e32 v65, s99, v51
	v_readlane_b32 s98, v60, 27
	v_fmac_f32_e32 v66, s100, v52
	v_readlane_b32 s99, v60, 28
	v_fmac_f32_e32 v65, s0, v54
	v_readlane_b32 s100, v60, 29
	v_fmac_f32_e32 v66, s98, v56
	v_readlane_b32 s0, v60, 30
	v_fmac_f32_e32 v65, s99, v57
	v_readlane_b32 s98, v60, 31
	v_fmac_f32_e32 v66, s100, v59
	v_readlane_b32 s99, v60, 32
	v_fmac_f32_e32 v65, s0, v61
	v_readlane_b32 s100, v60, 33
	v_fmac_f32_e32 v66, s98, v63
	v_readlane_b32 s0, v58, 0
	v_fmac_f32_e32 v65, s99, v64
	v_readlane_b32 s98, v58, 1
	v_fmac_f32_e32 v66, s100, v62
	v_add_f32_e32 v60, v65, v66
	v_readlane_b32 s99, v58, 2
	v_fma_f32 v65, 0, s0, v58
	v_readlane_b32 s100, v58, 3
	v_fma_f32 v66, v27, s98, 0
	v_readlane_b32 s0, v58, 4
	v_fmac_f32_e32 v65, s99, v25
	v_readlane_b32 s98, v58, 5
	v_fmac_f32_e32 v66, s100, v23
	v_readlane_b32 s99, v58, 6
	v_fmac_f32_e32 v65, s0, v5
	v_readlane_b32 s100, v58, 7
	v_fmac_f32_e32 v66, s98, v22
	v_readlane_b32 s0, v58, 8
	v_fmac_f32_e32 v65, s99, v24
	v_readlane_b32 s98, v58, 9
	v_fmac_f32_e32 v66, s100, v26
	v_readlane_b32 s99, v58, 10
	v_fmac_f32_e32 v65, s0, v28
	v_readlane_b32 s100, v58, 11
	v_fmac_f32_e32 v66, s98, v31
	v_readlane_b32 s0, v58, 12
	v_fmac_f32_e32 v65, s99, v32
	v_readlane_b32 s98, v58, 13
	v_fmac_f32_e32 v66, s100, v33
	v_readlane_b32 s99, v58, 14
	v_fmac_f32_e32 v65, s0, v34
	v_readlane_b32 s100, v58, 15
	v_fmac_f32_e32 v66, s98, v35
	v_readlane_b32 s0, v58, 16
	v_fmac_f32_e32 v65, s99, v36
	v_readlane_b32 s98, v58, 17
	v_fmac_f32_e32 v66, s100, v38
	v_readlane_b32 s99, v58, 18
	v_fmac_f32_e32 v65, s0, v39
	v_readlane_b32 s100, v58, 19
	v_fmac_f32_e32 v66, s98, v40
	v_readlane_b32 s0, v58, 20
	v_fmac_f32_e32 v65, s99, v42
	v_readlane_b32 s98, v58, 21
	v_fmac_f32_e32 v66, s100, v43
	v_readlane_b32 s99, v58, 22
	v_fmac_f32_e32 v65, s0, v45
	v_readlane_b32 s100, v58, 23
	v_fmac_f32_e32 v66, s98, v46
	v_readlane_b32 s0, v58, 24
	v_fmac_f32_e32 v65, s99, v47
	v_readlane_b32 s98, v58, 25
	v_fmac_f32_e32 v66, s100, v49
	v_readlane_b32 s99, v58, 26
	v_fmac_f32_e32 v65, s0, v51
	v_readlane_b32 s100, v58, 27
	v_fmac_f32_e32 v66, s98, v52
	v_readlane_b32 s0, v58, 28
	v_fmac_f32_e32 v65, s99, v54
	v_readlane_b32 s98, v58, 29
	v_fmac_f32_e32 v66, s100, v56
	v_readlane_b32 s99, v58, 30
	v_fmac_f32_e32 v65, s0, v57
	v_readlane_b32 s100, v58, 31
	v_fmac_f32_e32 v66, s98, v59
	v_readlane_b32 s0, v58, 32
	v_fmac_f32_e32 v65, s99, v61
	v_readlane_b32 s98, v58, 33
	v_fmac_f32_e32 v66, s100, v63
	v_readlane_b32 s99, v58, 34
	v_fmac_f32_e32 v65, s0, v64
	v_readlane_b32 s100, v55, 0
	v_fmac_f32_e32 v66, s98, v62
	v_readlane_b32 s0, v55, 1
	v_fmac_f32_e32 v65, s99, v60
	v_add_f32_e32 v58, v66, v65
	v_readlane_b32 s98, v55, 2
	v_fma_f32 v65, 0, s100, v55
	v_readlane_b32 s99, v55, 3
	v_fma_f32 v66, v27, s0, 0
	v_readlane_b32 s100, v55, 4
	v_fmac_f32_e32 v65, s98, v25
	v_readlane_b32 s0, v55, 5
	v_fmac_f32_e32 v66, s99, v23
	v_readlane_b32 s98, v55, 6
	v_fmac_f32_e32 v65, s100, v5
	v_readlane_b32 s99, v55, 7
	v_fmac_f32_e32 v66, s0, v22
	v_readlane_b32 s100, v55, 8
	v_fmac_f32_e32 v65, s98, v24
	v_readlane_b32 s0, v55, 9
	v_fmac_f32_e32 v66, s99, v26
	v_readlane_b32 s98, v55, 10
	v_fmac_f32_e32 v65, s100, v28
	v_readlane_b32 s99, v55, 11
	v_fmac_f32_e32 v66, s0, v31
	v_readlane_b32 s100, v55, 12
	v_fmac_f32_e32 v65, s98, v32
	v_readlane_b32 s0, v55, 13
	v_fmac_f32_e32 v66, s99, v33
	v_readlane_b32 s98, v55, 14
	v_fmac_f32_e32 v65, s100, v34
	v_readlane_b32 s99, v55, 15
	v_fmac_f32_e32 v66, s0, v35
	v_readlane_b32 s100, v55, 16
	v_fmac_f32_e32 v65, s98, v36
	v_readlane_b32 s0, v55, 17
	v_fmac_f32_e32 v66, s99, v38
	v_readlane_b32 s98, v55, 18
	v_fmac_f32_e32 v65, s100, v39
	v_readlane_b32 s99, v55, 19
	v_fmac_f32_e32 v66, s0, v40
	v_readlane_b32 s100, v55, 20
	v_fmac_f32_e32 v65, s98, v42
	v_readlane_b32 s0, v55, 21
	v_fmac_f32_e32 v66, s99, v43
	v_readlane_b32 s98, v55, 22
	v_fmac_f32_e32 v65, s100, v45
	v_readlane_b32 s99, v55, 23
	v_fmac_f32_e32 v66, s0, v46
	v_readlane_b32 s100, v55, 24
	v_fmac_f32_e32 v65, s98, v47
	v_readlane_b32 s0, v55, 25
	v_fmac_f32_e32 v66, s99, v49
	v_readlane_b32 s98, v55, 26
	v_fmac_f32_e32 v65, s100, v51
	v_readlane_b32 s99, v55, 27
	v_fmac_f32_e32 v66, s0, v52
	v_readlane_b32 s100, v55, 28
	v_fmac_f32_e32 v65, s98, v54
	v_readlane_b32 s0, v55, 29
	v_fmac_f32_e32 v66, s99, v56
	v_readlane_b32 s98, v55, 30
	v_fmac_f32_e32 v65, s100, v57
	v_readlane_b32 s99, v55, 31
	v_fmac_f32_e32 v66, s0, v59
	v_readlane_b32 s100, v55, 32
	v_fmac_f32_e32 v65, s98, v61
	v_readlane_b32 s0, v55, 33
	v_fmac_f32_e32 v66, s99, v63
	v_readlane_b32 s98, v55, 34
	v_fmac_f32_e32 v65, s100, v64
; __device__ __forceinline__ void ph_gdn_prep(const Params& p, LAS unsigned char* lds) {
;     ...
;             for (int i = 1; i < 64; ++i) { const int mi = __float_as_int(mcol[i]); float a0 = mcol[i], a1 = 0.f;
; #pragma unroll
;                 for (int j = 0; j < i; ++j) { const float s = __int_as_float(__builtin_amdgcn_readlane(mi, j)); if (j & 1) a1 += s * mcol[j]; else a0 += s * mcol[j]; }
;                 mcol[i] = a0 + a1; }
	v_readlane_b32 s99, v55, 35
	v_fmac_f32_e32 v66, s0, v62
	v_readlane_b32 s100, v53, 0
	v_fmac_f32_e32 v65, s98, v60
	v_readlane_b32 s0, v53, 1
	v_fmac_f32_e32 v66, s99, v58
	v_add_f32_e32 v55, v65, v66
	v_readlane_b32 s98, v53, 2
	v_fma_f32 v65, 0, s100, v53
	v_readlane_b32 s99, v53, 3
	v_fma_f32 v66, v27, s0, 0
	v_readlane_b32 s100, v53, 4
	v_fmac_f32_e32 v65, s98, v25
	v_readlane_b32 s0, v53, 5
	v_fmac_f32_e32 v66, s99, v23
	v_readlane_b32 s98, v53, 6
	v_fmac_f32_e32 v65, s100, v5
	v_readlane_b32 s99, v53, 7
	v_fmac_f32_e32 v66, s0, v22
	v_readlane_b32 s100, v53, 8
	v_fmac_f32_e32 v65, s98, v24
	v_readlane_b32 s0, v53, 9
	v_fmac_f32_e32 v66, s99, v26
	v_readlane_b32 s98, v53, 10
	v_fmac_f32_e32 v65, s100, v28
	v_readlane_b32 s99, v53, 11
	v_fmac_f32_e32 v66, s0, v31
	v_readlane_b32 s100, v53, 12
	v_fmac_f32_e32 v65, s98, v32
	v_readlane_b32 s0, v53, 13
	v_fmac_f32_e32 v66, s99, v33
	v_readlane_b32 s98, v53, 14
	v_fmac_f32_e32 v65, s100, v34
	v_readlane_b32 s99, v53, 15
	v_fmac_f32_e32 v66, s0, v35
	v_readlane_b32 s100, v53, 16
	v_fmac_f32_e32 v65, s98, v36
	v_readlane_b32 s0, v53, 17
	v_fmac_f32_e32 v66, s99, v38
	v_readlane_b32 s98, v53, 18
	v_fmac_f32_e32 v65, s100, v39
	v_readlane_b32 s99, v53, 19
	v_fmac_f32_e32 v66, s0, v40
	v_readlane_b32 s100, v53, 20
	v_fmac_f32_e32 v65, s98, v42
	v_readlane_b32 s0, v53, 21
	v_fmac_f32_e32 v66, s99, v43
	v_readlane_b32 s98, v53, 22
	v_fmac_f32_e32 v65, s100, v45
	v_readlane_b32 s99, v53, 23
	v_fmac_f32_e32 v66, s0, v46
	v_readlane_b32 s100, v53, 24
	v_fmac_f32_e32 v65, s98, v47
	v_readlane_b32 s0, v53, 25
	v_fmac_f32_e32 v66, s99, v49
	v_readlane_b32 s98, v53, 26
	v_fmac_f32_e32 v65, s100, v51
	v_readlane_b32 s99, v53, 27
	v_fmac_f32_e32 v66, s0, v52
	v_readlane_b32 s100, v53, 28
	v_fmac_f32_e32 v65, s98, v54
	v_readlane_b32 s0, v53, 29
	v_fmac_f32_e32 v66, s99, v56
	v_readlane_b32 s98, v53, 30
	v_fmac_f32_e32 v65, s100, v57
	v_readlane_b32 s99, v53, 31
	v_fmac_f32_e32 v66, s0, v59
	v_readlane_b32 s100, v53, 32
	v_fmac_f32_e32 v65, s98, v61
	v_readlane_b32 s0, v53, 33
	v_fmac_f32_e32 v66, s99, v63
	v_readlane_b32 s98, v53, 34
	v_fmac_f32_e32 v65, s100, v64
	v_readlane_b32 s99, v53, 35
	v_fmac_f32_e32 v66, s0, v62
	v_readlane_b32 s100, v53, 36
	v_fmac_f32_e32 v65, s98, v60
	v_readlane_b32 s0, v50, 0
	v_fmac_f32_e32 v66, s99, v58
	v_readlane_b32 s98, v50, 1
	v_fmac_f32_e32 v65, s100, v55
	v_add_f32_e32 v53, v66, v65
	v_readlane_b32 s99, v50, 2
	v_fma_f32 v65, 0, s0, v50
	v_readlane_b32 s100, v50, 3
	v_fma_f32 v66, v27, s98, 0
	v_readlane_b32 s0, v50, 4
	v_fmac_f32_e32 v65, s99, v25
	v_readlane_b32 s98, v50, 5
	v_fmac_f32_e32 v66, s100, v23
	v_readlane_b32 s99, v50, 6
	v_fmac_f32_e32 v65, s0, v5
	v_readlane_b32 s100, v50, 7
	v_fmac_f32_e32 v66, s98, v22
	v_readlane_b32 s0, v50, 8
	v_fmac_f32_e32 v65, s99, v24
	v_readlane_b32 s98, v50, 9
	v_fmac_f32_e32 v66, s100, v26
	v_readlane_b32 s99, v50, 10
	v_fmac_f32_e32 v65, s0, v28
	v_readlane_b32 s100, v50, 11
	v_fmac_f32_e32 v66, s98, v31
	v_readlane_b32 s0, v50, 12
	v_fmac_f32_e32 v65, s99, v32
	v_readlane_b32 s98, v50, 13
	v_fmac_f32_e32 v66, s100, v33
	v_readlane_b32 s99, v50, 14
	v_fmac_f32_e32 v65, s0, v34
	v_readlane_b32 s100, v50, 15
	v_fmac_f32_e32 v66, s98, v35
	v_readlane_b32 s0, v50, 16
	v_fmac_f32_e32 v65, s99, v36
	v_readlane_b32 s98, v50, 17
	v_fmac_f32_e32 v66, s100, v38
	v_readlane_b32 s99, v50, 18
	v_fmac_f32_e32 v65, s0, v39
	v_readlane_b32 s100, v50, 19
	v_fmac_f32_e32 v66, s98, v40
	v_readlane_b32 s0, v50, 20
	v_fmac_f32_e32 v65, s99, v42
	v_readlane_b32 s98, v50, 21
	v_fmac_f32_e32 v66, s100, v43
	v_readlane_b32 s99, v50, 22
	v_fmac_f32_e32 v65, s0, v45
	v_readlane_b32 s100, v50, 23
	v_fmac_f32_e32 v66, s98, v46
	v_readlane_b32 s0, v50, 24
	v_fmac_f32_e32 v65, s99, v47
	v_readlane_b32 s98, v50, 25
	v_fmac_f32_e32 v66, s100, v49
	v_readlane_b32 s99, v50, 26
	v_fmac_f32_e32 v65, s0, v51
	v_readlane_b32 s100, v50, 27
	v_fmac_f32_e32 v66, s98, v52
	v_readlane_b32 s0, v50, 28
	v_fmac_f32_e32 v65, s99, v54
	v_readlane_b32 s98, v50, 29
	v_fmac_f32_e32 v66, s100, v56
	v_readlane_b32 s99, v50, 30
	v_fmac_f32_e32 v65, s0, v57
	v_readlane_b32 s100, v50, 31
	v_fmac_f32_e32 v66, s98, v59
	v_readlane_b32 s0, v50, 32
	v_fmac_f32_e32 v65, s99, v61
	v_readlane_b32 s98, v50, 33
	v_fmac_f32_e32 v66, s100, v63
	v_readlane_b32 s99, v50, 34
	v_fmac_f32_e32 v65, s0, v64
	v_readlane_b32 s100, v50, 35
	v_fmac_f32_e32 v66, s98, v62
	v_readlane_b32 s0, v50, 36
	v_fmac_f32_e32 v65, s99, v60
	v_readlane_b32 s98, v50, 37
	v_fmac_f32_e32 v66, s100, v58
	v_readlane_b32 s99, v48, 0
	v_fmac_f32_e32 v65, s0, v55
	v_readlane_b32 s100, v48, 1
	v_fmac_f32_e32 v66, s98, v53
	v_add_f32_e32 v50, v65, v66
	v_readlane_b32 s0, v48, 2
	v_fma_f32 v65, 0, s99, v48
	v_readlane_b32 s98, v48, 3
	v_fma_f32 v66, v27, s100, 0
	v_readlane_b32 s99, v48, 4
	v_fmac_f32_e32 v65, s0, v25
	v_readlane_b32 s100, v48, 5
	v_fmac_f32_e32 v66, s98, v23
	v_readlane_b32 s0, v48, 6
	v_fmac_f32_e32 v65, s99, v5
	v_readlane_b32 s98, v48, 7
	v_fmac_f32_e32 v66, s100, v22
	v_readlane_b32 s99, v48, 8
	v_fmac_f32_e32 v65, s0, v24
	v_readlane_b32 s100, v48, 9
	v_fmac_f32_e32 v66, s98, v26
	v_readlane_b32 s0, v48, 10
	v_fmac_f32_e32 v65, s99, v28
	v_readlane_b32 s98, v48, 11
	v_fmac_f32_e32 v66, s100, v31
	v_readlane_b32 s99, v48, 12
	v_fmac_f32_e32 v65, s0, v32
	v_readlane_b32 s100, v48, 13
	v_fmac_f32_e32 v66, s98, v33
	v_readlane_b32 s0, v48, 14
	v_fmac_f32_e32 v65, s99, v34
	v_readlane_b32 s98, v48, 15
	v_fmac_f32_e32 v66, s100, v35
	v_readlane_b32 s99, v48, 16
	v_fmac_f32_e32 v65, s0, v36
	v_readlane_b32 s100, v48, 17
	v_fmac_f32_e32 v66, s98, v38
	v_readlane_b32 s0, v48, 18
	v_fmac_f32_e32 v65, s99, v39
; __device__ __forceinline__ void ph_gdn_prep(const Params& p, LAS unsigned char* lds) {
;     ...
;             for (int i = 1; i < 64; ++i) { const int mi = __float_as_int(mcol[i]); float a0 = mcol[i], a1 = 0.f;
; #pragma unroll
;                 for (int j = 0; j < i; ++j) { const float s = __int_as_float(__builtin_amdgcn_readlane(mi, j)); if (j & 1) a1 += s * mcol[j]; else a0 += s * mcol[j]; }
;                 mcol[i] = a0 + a1; }
	v_readlane_b32 s98, v48, 19
	v_fmac_f32_e32 v66, s100, v40
	v_readlane_b32 s99, v48, 20
	v_fmac_f32_e32 v65, s0, v42
	v_readlane_b32 s100, v48, 21
	v_fmac_f32_e32 v66, s98, v43
	v_readlane_b32 s0, v48, 22
	v_fmac_f32_e32 v65, s99, v45
	v_readlane_b32 s98, v48, 23
	v_fmac_f32_e32 v66, s100, v46
	v_readlane_b32 s99, v48, 24
	v_fmac_f32_e32 v65, s0, v47
	v_readlane_b32 s100, v48, 25
	v_fmac_f32_e32 v66, s98, v49
	v_readlane_b32 s0, v48, 26
	v_fmac_f32_e32 v65, s99, v51
	v_readlane_b32 s98, v48, 27
	v_fmac_f32_e32 v66, s100, v52
	v_readlane_b32 s99, v48, 28
	v_fmac_f32_e32 v65, s0, v54
	v_readlane_b32 s100, v48, 29
	v_fmac_f32_e32 v66, s98, v56
	v_readlane_b32 s0, v48, 30
	v_fmac_f32_e32 v65, s99, v57
	v_readlane_b32 s98, v48, 31
	v_fmac_f32_e32 v66, s100, v59
	v_readlane_b32 s99, v48, 32
	v_fmac_f32_e32 v65, s0, v61
	v_readlane_b32 s100, v48, 33
	v_fmac_f32_e32 v66, s98, v63
	v_readlane_b32 s0, v48, 34
	v_fmac_f32_e32 v65, s99, v64
	v_readlane_b32 s98, v48, 35
	v_fmac_f32_e32 v66, s100, v62
	v_readlane_b32 s99, v48, 36
	v_fmac_f32_e32 v65, s0, v60
	v_readlane_b32 s100, v48, 37
	v_fmac_f32_e32 v66, s98, v58
	v_readlane_b32 s0, v48, 38
	v_fmac_f32_e32 v65, s99, v55
	v_readlane_b32 s98, v44, 0
	v_fmac_f32_e32 v66, s100, v53
	v_readlane_b32 s99, v44, 1
	v_fmac_f32_e32 v65, s0, v50
	v_add_f32_e32 v48, v66, v65
	v_readlane_b32 s100, v44, 2
	v_fma_f32 v65, 0, s98, v44
	v_readlane_b32 s0, v44, 3
	v_fma_f32 v66, v27, s99, 0
	v_readlane_b32 s98, v44, 4
	v_fmac_f32_e32 v65, s100, v25
	v_readlane_b32 s99, v44, 5
	v_fmac_f32_e32 v66, s0, v23
	v_readlane_b32 s100, v44, 6
	v_fmac_f32_e32 v65, s98, v5
	v_readlane_b32 s0, v44, 7
	v_fmac_f32_e32 v66, s99, v22
	v_readlane_b32 s98, v44, 8
	v_fmac_f32_e32 v65, s100, v24
	v_readlane_b32 s99, v44, 9
	v_fmac_f32_e32 v66, s0, v26
	v_readlane_b32 s100, v44, 10
	v_fmac_f32_e32 v65, s98, v28
	v_readlane_b32 s0, v44, 11
	v_fmac_f32_e32 v66, s99, v31
	v_readlane_b32 s98, v44, 12
	v_fmac_f32_e32 v65, s100, v32
	v_readlane_b32 s99, v44, 13
	v_fmac_f32_e32 v66, s0, v33
	v_readlane_b32 s100, v44, 14
	v_fmac_f32_e32 v65, s98, v34
	v_readlane_b32 s0, v44, 15
	v_fmac_f32_e32 v66, s99, v35
	v_readlane_b32 s98, v44, 16
	v_fmac_f32_e32 v65, s100, v36
	v_readlane_b32 s99, v44, 17
	v_fmac_f32_e32 v66, s0, v38
	v_readlane_b32 s100, v44, 18
	v_fmac_f32_e32 v65, s98, v39
	v_readlane_b32 s0, v44, 19
	v_fmac_f32_e32 v66, s99, v40
	v_readlane_b32 s98, v44, 20
	v_fmac_f32_e32 v65, s100, v42
	v_readlane_b32 s99, v44, 21
	v_fmac_f32_e32 v66, s0, v43
	v_readlane_b32 s100, v44, 22
	v_fmac_f32_e32 v65, s98, v45
	v_readlane_b32 s0, v44, 23
	v_fmac_f32_e32 v66, s99, v46
	v_readlane_b32 s98, v44, 24
	v_fmac_f32_e32 v65, s100, v47
	v_readlane_b32 s99, v44, 25
	v_fmac_f32_e32 v66, s0, v49
	v_readlane_b32 s100, v44, 26
	v_fmac_f32_e32 v65, s98, v51
	v_readlane_b32 s0, v44, 27
	v_fmac_f32_e32 v66, s99, v52
	v_readlane_b32 s98, v44, 28
	v_fmac_f32_e32 v65, s100, v54
	v_readlane_b32 s99, v44, 29
	v_fmac_f32_e32 v66, s0, v56
	v_readlane_b32 s100, v44, 30
	v_fmac_f32_e32 v65, s98, v57
	v_readlane_b32 s0, v44, 31
	v_fmac_f32_e32 v66, s99, v59
	v_readlane_b32 s98, v44, 32
	v_fmac_f32_e32 v65, s100, v61
	v_readlane_b32 s99, v44, 33
	v_fmac_f32_e32 v66, s0, v63
	v_readlane_b32 s100, v44, 34
	v_fmac_f32_e32 v65, s98, v64
	v_readlane_b32 s0, v44, 35
	v_fmac_f32_e32 v66, s99, v62
	v_readlane_b32 s98, v44, 36
	v_fmac_f32_e32 v65, s100, v60
	v_readlane_b32 s99, v44, 37
	v_fmac_f32_e32 v66, s0, v58
	v_readlane_b32 s100, v44, 38
	v_fmac_f32_e32 v65, s98, v55
	v_readlane_b32 s0, v44, 39
	v_fmac_f32_e32 v66, s99, v53
	v_readlane_b32 s98, v41, 0
	v_fmac_f32_e32 v65, s100, v50
	v_readlane_b32 s99, v41, 1
	v_fmac_f32_e32 v66, s0, v48
	v_add_f32_e32 v44, v65, v66
	v_readlane_b32 s100, v41, 2
	v_fma_f32 v65, 0, s98, v41
	v_readlane_b32 s0, v41, 3
	v_fma_f32 v66, v27, s99, 0
	v_readlane_b32 s98, v41, 4
	v_fmac_f32_e32 v65, s100, v25
	v_readlane_b32 s99, v41, 5
	v_fmac_f32_e32 v66, s0, v23
	v_readlane_b32 s100, v41, 6
	v_fmac_f32_e32 v65, s98, v5
	v_readlane_b32 s0, v41, 7
	v_fmac_f32_e32 v66, s99, v22
	v_readlane_b32 s98, v41, 8
	v_fmac_f32_e32 v65, s100, v24
	v_readlane_b32 s99, v41, 9
	v_fmac_f32_e32 v66, s0, v26
	v_readlane_b32 s100, v41, 10
	v_fmac_f32_e32 v65, s98, v28
	v_readlane_b32 s0, v41, 11
	v_fmac_f32_e32 v66, s99, v31
	v_readlane_b32 s98, v41, 12
	v_fmac_f32_e32 v65, s100, v32
	v_readlane_b32 s99, v41, 13
	v_fmac_f32_e32 v66, s0, v33
	v_readlane_b32 s100, v41, 14
	v_fmac_f32_e32 v65, s98, v34
	v_readlane_b32 s0, v41, 15
	v_fmac_f32_e32 v66, s99, v35
	v_readlane_b32 s98, v41, 16
	v_fmac_f32_e32 v65, s100, v36
	v_readlane_b32 s99, v41, 17
	v_fmac_f32_e32 v66, s0, v38
	v_readlane_b32 s100, v41, 18
	v_fmac_f32_e32 v65, s98, v39
	v_readlane_b32 s0, v41, 19
	v_fmac_f32_e32 v66, s99, v40
	v_readlane_b32 s98, v41, 20
	v_fmac_f32_e32 v65, s100, v42
	v_readlane_b32 s99, v41, 21
	v_fmac_f32_e32 v66, s0, v43
	v_readlane_b32 s100, v41, 22
	v_fmac_f32_e32 v65, s98, v45
	v_readlane_b32 s0, v41, 23
	v_fmac_f32_e32 v66, s99, v46
	v_readlane_b32 s98, v41, 24
	v_fmac_f32_e32 v65, s100, v47
	v_readlane_b32 s99, v41, 25
	v_fmac_f32_e32 v66, s0, v49
	v_readlane_b32 s100, v41, 26
	v_fmac_f32_e32 v65, s98, v51
	v_readlane_b32 s0, v41, 27
	v_fmac_f32_e32 v66, s99, v52
	v_readlane_b32 s98, v41, 28
	v_fmac_f32_e32 v65, s100, v54
	v_readlane_b32 s99, v41, 29
	v_fmac_f32_e32 v66, s0, v56
	v_readlane_b32 s100, v41, 30
	v_fmac_f32_e32 v65, s98, v57
	v_readlane_b32 s0, v41, 31
	v_fmac_f32_e32 v66, s99, v59
	v_readlane_b32 s98, v41, 32
	v_fmac_f32_e32 v65, s100, v61
	v_readlane_b32 s99, v41, 33
	v_fmac_f32_e32 v66, s0, v63
	v_readlane_b32 s100, v41, 34
	v_fmac_f32_e32 v65, s98, v64
; __device__ __forceinline__ void ph_gdn_prep(const Params& p, LAS unsigned char* lds) {
;     ...
;             for (int i = 1; i < 64; ++i) { const int mi = __float_as_int(mcol[i]); float a0 = mcol[i], a1 = 0.f;
; #pragma unroll
;                 for (int j = 0; j < i; ++j) { const float s = __int_as_float(__builtin_amdgcn_readlane(mi, j)); if (j & 1) a1 += s * mcol[j]; else a0 += s * mcol[j]; }
;                 mcol[i] = a0 + a1; }
	v_readlane_b32 s0, v41, 35
	v_fmac_f32_e32 v66, s99, v62
	v_readlane_b32 s98, v41, 36
	v_fmac_f32_e32 v65, s100, v60
	v_readlane_b32 s99, v41, 37
	v_fmac_f32_e32 v66, s0, v58
	v_readlane_b32 s100, v41, 38
	v_fmac_f32_e32 v65, s98, v55
	v_readlane_b32 s0, v41, 39
	v_fmac_f32_e32 v66, s99, v53
	v_readlane_b32 s98, v41, 40
	v_fmac_f32_e32 v65, s100, v50
	v_readlane_b32 s99, v37, 0
	v_fmac_f32_e32 v66, s0, v48
	v_readlane_b32 s100, v37, 1
	v_fmac_f32_e32 v65, s98, v44
	v_add_f32_e32 v41, v66, v65
	v_readlane_b32 s0, v37, 2
	v_fma_f32 v65, 0, s99, v37
	v_readlane_b32 s98, v37, 3
	v_fma_f32 v66, v27, s100, 0
	v_readlane_b32 s99, v37, 4
	v_fmac_f32_e32 v65, s0, v25
	v_readlane_b32 s100, v37, 5
	v_fmac_f32_e32 v66, s98, v23
	v_readlane_b32 s0, v37, 6
	v_fmac_f32_e32 v65, s99, v5
	v_readlane_b32 s98, v37, 7
	v_fmac_f32_e32 v66, s100, v22
	v_readlane_b32 s99, v37, 8
	v_fmac_f32_e32 v65, s0, v24
	v_readlane_b32 s100, v37, 9
	v_fmac_f32_e32 v66, s98, v26
	v_readlane_b32 s0, v37, 10
	v_fmac_f32_e32 v65, s99, v28
	v_readlane_b32 s98, v37, 11
	v_fmac_f32_e32 v66, s100, v31
	v_readlane_b32 s99, v37, 12
	v_fmac_f32_e32 v65, s0, v32
	v_readlane_b32 s100, v37, 13
	v_fmac_f32_e32 v66, s98, v33
	v_readlane_b32 s0, v37, 14
	v_fmac_f32_e32 v65, s99, v34
	v_readlane_b32 s98, v37, 15
	v_fmac_f32_e32 v66, s100, v35
	v_readlane_b32 s99, v37, 16
	v_fmac_f32_e32 v65, s0, v36
	v_readlane_b32 s100, v37, 17
	v_fmac_f32_e32 v66, s98, v38
	v_readlane_b32 s0, v37, 18
	v_fmac_f32_e32 v65, s99, v39
	v_readlane_b32 s98, v37, 19
	v_fmac_f32_e32 v66, s100, v40
	v_readlane_b32 s99, v37, 20
	v_fmac_f32_e32 v65, s0, v42
	v_readlane_b32 s100, v37, 21
	v_fmac_f32_e32 v66, s98, v43
	v_readlane_b32 s0, v37, 22
	v_fmac_f32_e32 v65, s99, v45
	v_readlane_b32 s98, v37, 23
	v_fmac_f32_e32 v66, s100, v46
	v_readlane_b32 s99, v37, 24
	v_fmac_f32_e32 v65, s0, v47
	v_readlane_b32 s100, v37, 25
	v_fmac_f32_e32 v66, s98, v49
	v_readlane_b32 s0, v37, 26
	v_fmac_f32_e32 v65, s99, v51
	v_readlane_b32 s98, v37, 27
	v_fmac_f32_e32 v66, s100, v52
	v_readlane_b32 s99, v37, 28
	v_fmac_f32_e32 v65, s0, v54
	v_readlane_b32 s100, v37, 29
	v_fmac_f32_e32 v66, s98, v56
	v_readlane_b32 s0, v37, 30
	v_fmac_f32_e32 v65, s99, v57
	v_readlane_b32 s98, v37, 31
	v_fmac_f32_e32 v66, s100, v59
	v_readlane_b32 s99, v37, 32
	v_fmac_f32_e32 v65, s0, v61
	v_readlane_b32 s100, v37, 33
	v_fmac_f32_e32 v66, s98, v63
	v_readlane_b32 s0, v37, 34
	v_fmac_f32_e32 v65, s99, v64
	v_readlane_b32 s98, v37, 35
	v_fmac_f32_e32 v66, s100, v62
	v_readlane_b32 s99, v37, 36
	v_fmac_f32_e32 v65, s0, v60
	v_readlane_b32 s100, v37, 37
	v_fmac_f32_e32 v66, s98, v58
	v_readlane_b32 s0, v37, 38
	v_fmac_f32_e32 v65, s99, v55
	v_readlane_b32 s98, v37, 39
	v_fmac_f32_e32 v66, s100, v53
	v_readlane_b32 s99, v37, 40
	v_fmac_f32_e32 v65, s0, v50
	v_readlane_b32 s100, v37, 41
	v_fmac_f32_e32 v66, s98, v48
	v_readlane_b32 s0, v30, 0
	v_fmac_f32_e32 v65, s99, v44
	v_readlane_b32 s98, v30, 1
	v_fmac_f32_e32 v66, s100, v41
	v_add_f32_e32 v37, v65, v66
	v_readlane_b32 s99, v30, 2
	v_fma_f32 v65, 0, s0, v30
	v_readlane_b32 s100, v30, 3
	v_fma_f32 v66, v27, s98, 0
	v_readlane_b32 s0, v30, 4
	v_fmac_f32_e32 v65, s99, v25
	v_readlane_b32 s98, v30, 5
	v_fmac_f32_e32 v66, s100, v23
	v_readlane_b32 s99, v30, 6
	v_fmac_f32_e32 v65, s0, v5
	v_readlane_b32 s100, v30, 7
	v_fmac_f32_e32 v66, s98, v22
	v_readlane_b32 s0, v30, 8
	v_fmac_f32_e32 v65, s99, v24
	v_readlane_b32 s98, v30, 9
	v_fmac_f32_e32 v66, s100, v26
	v_readlane_b32 s99, v30, 10
	v_fmac_f32_e32 v65, s0, v28
	v_readlane_b32 s100, v30, 11
	v_fmac_f32_e32 v66, s98, v31
	v_readlane_b32 s0, v30, 12
	v_fmac_f32_e32 v65, s99, v32
	v_readlane_b32 s98, v30, 13
	v_fmac_f32_e32 v66, s100, v33
	v_readlane_b32 s99, v30, 14
	v_fmac_f32_e32 v65, s0, v34
	v_readlane_b32 s100, v30, 15
	v_fmac_f32_e32 v66, s98, v35
	v_readlane_b32 s0, v30, 16
	v_fmac_f32_e32 v65, s99, v36
	v_readlane_b32 s98, v30, 17
	v_fmac_f32_e32 v66, s100, v38
	v_readlane_b32 s99, v30, 18
	v_fmac_f32_e32 v65, s0, v39
	v_readlane_b32 s100, v30, 19
	v_fmac_f32_e32 v66, s98, v40
	v_readlane_b32 s0, v30, 20
	v_fmac_f32_e32 v65, s99, v42
	v_readlane_b32 s98, v30, 21
	v_fmac_f32_e32 v66, s100, v43
	v_readlane_b32 s99, v30, 22
	v_fmac_f32_e32 v65, s0, v45
	v_readlane_b32 s100, v30, 23
	v_fmac_f32_e32 v66, s98, v46
	v_readlane_b32 s0, v30, 24
	v_fmac_f32_e32 v65, s99, v47
	v_readlane_b32 s98, v30, 25
	v_fmac_f32_e32 v66, s100, v49
	v_readlane_b32 s99, v30, 26
	v_fmac_f32_e32 v65, s0, v51
	v_readlane_b32 s100, v30, 27
	v_fmac_f32_e32 v66, s98, v52
	v_readlane_b32 s0, v30, 28
	v_fmac_f32_e32 v65, s99, v54
	v_readlane_b32 s98, v30, 29
	v_fmac_f32_e32 v66, s100, v56
	v_readlane_b32 s99, v30, 30
	v_fmac_f32_e32 v65, s0, v57
	v_readlane_b32 s100, v30, 31
	v_fmac_f32_e32 v66, s98, v59
	v_readlane_b32 s0, v30, 32
	v_fmac_f32_e32 v65, s99, v61
	v_readlane_b32 s98, v30, 33
	v_fmac_f32_e32 v66, s100, v63
	v_readlane_b32 s99, v30, 34
	v_fmac_f32_e32 v65, s0, v64
	v_readlane_b32 s100, v30, 35
	v_fmac_f32_e32 v66, s98, v62
	v_readlane_b32 s0, v30, 36
	v_fmac_f32_e32 v65, s99, v60
	v_readlane_b32 s98, v30, 37
	v_fmac_f32_e32 v66, s100, v58
	v_readlane_b32 s99, v30, 38
	v_fmac_f32_e32 v65, s0, v55
	v_readlane_b32 s100, v30, 39
	v_fmac_f32_e32 v66, s98, v53
	v_readlane_b32 s0, v30, 40
	v_fmac_f32_e32 v65, s99, v50
	v_readlane_b32 s98, v30, 41
	v_fmac_f32_e32 v66, s100, v48
	v_readlane_b32 s99, v30, 42
	v_fmac_f32_e32 v65, s0, v44
	v_readlane_b32 s100, v21, 0
	v_fmac_f32_e32 v66, s98, v41
	v_readlane_b32 s0, v21, 1
	v_fmac_f32_e32 v65, s99, v37
	v_add_f32_e32 v30, v66, v65
	v_readlane_b32 s98, v21, 2
	v_fma_f32 v65, 0, s100, v21
	v_readlane_b32 s99, v21, 3
	v_fma_f32 v66, v27, s0, 0
; __device__ __forceinline__ void ph_gdn_prep(const Params& p, LAS unsigned char* lds) {
;     ...
;             for (int i = 1; i < 64; ++i) { const int mi = __float_as_int(mcol[i]); float a0 = mcol[i], a1 = 0.f;
; #pragma unroll
;                 for (int j = 0; j < i; ++j) { const float s = __int_as_float(__builtin_amdgcn_readlane(mi, j)); if (j & 1) a1 += s * mcol[j]; else a0 += s * mcol[j]; }
;                 mcol[i] = a0 + a1; }
	v_readlane_b32 s100, v21, 4
	v_fmac_f32_e32 v65, s98, v25
	v_readlane_b32 s0, v21, 5
	v_fmac_f32_e32 v66, s99, v23
	v_readlane_b32 s98, v21, 6
	v_fmac_f32_e32 v65, s100, v5
	v_readlane_b32 s99, v21, 7
	v_fmac_f32_e32 v66, s0, v22
	v_readlane_b32 s100, v21, 8
	v_fmac_f32_e32 v65, s98, v24
	v_readlane_b32 s0, v21, 9
	v_fmac_f32_e32 v66, s99, v26
	v_readlane_b32 s98, v21, 10
	v_fmac_f32_e32 v65, s100, v28
	v_readlane_b32 s99, v21, 11
	v_fmac_f32_e32 v66, s0, v31
	v_readlane_b32 s100, v21, 12
	v_fmac_f32_e32 v65, s98, v32
	v_readlane_b32 s0, v21, 13
	v_fmac_f32_e32 v66, s99, v33
	v_readlane_b32 s98, v21, 14
	v_fmac_f32_e32 v65, s100, v34
	v_readlane_b32 s99, v21, 15
	v_fmac_f32_e32 v66, s0, v35
	v_readlane_b32 s100, v21, 16
	v_fmac_f32_e32 v65, s98, v36
	v_readlane_b32 s0, v21, 17
	v_fmac_f32_e32 v66, s99, v38
	v_readlane_b32 s98, v21, 18
	v_fmac_f32_e32 v65, s100, v39
	v_readlane_b32 s99, v21, 19
	v_fmac_f32_e32 v66, s0, v40
	v_readlane_b32 s100, v21, 20
	v_fmac_f32_e32 v65, s98, v42
	v_readlane_b32 s0, v21, 21
	v_fmac_f32_e32 v66, s99, v43
	v_readlane_b32 s98, v21, 22
	v_fmac_f32_e32 v65, s100, v45
	v_readlane_b32 s99, v21, 23
	v_fmac_f32_e32 v66, s0, v46
	v_readlane_b32 s100, v21, 24
	v_fmac_f32_e32 v65, s98, v47
	v_readlane_b32 s0, v21, 25
	v_fmac_f32_e32 v66, s99, v49
	v_readlane_b32 s98, v21, 26
	v_fmac_f32_e32 v65, s100, v51
	v_readlane_b32 s99, v21, 27
	v_fmac_f32_e32 v66, s0, v52
	v_readlane_b32 s100, v21, 28
	v_fmac_f32_e32 v65, s98, v54
	v_readlane_b32 s0, v21, 29
	v_fmac_f32_e32 v66, s99, v56
	v_readlane_b32 s98, v21, 30
	v_fmac_f32_e32 v65, s100, v57
	v_readlane_b32 s99, v21, 31
	v_fmac_f32_e32 v66, s0, v59
	v_readlane_b32 s100, v21, 32
	v_fmac_f32_e32 v65, s98, v61
	v_readlane_b32 s0, v21, 33
	v_fmac_f32_e32 v66, s99, v63
	v_readlane_b32 s98, v21, 34
	v_fmac_f32_e32 v65, s100, v64
	v_readlane_b32 s99, v21, 35
	v_fmac_f32_e32 v66, s0, v62
	v_readlane_b32 s100, v21, 36
	v_fmac_f32_e32 v65, s98, v60
	v_readlane_b32 s0, v21, 37
	v_fmac_f32_e32 v66, s99, v58
	v_readlane_b32 s98, v21, 38
	v_fmac_f32_e32 v65, s100, v55
	v_readlane_b32 s99, v21, 39
	v_fmac_f32_e32 v66, s0, v53
	v_readlane_b32 s100, v21, 40
	v_fmac_f32_e32 v65, s98, v50
	v_readlane_b32 s0, v21, 41
	v_fmac_f32_e32 v66, s99, v48
	v_readlane_b32 s98, v21, 42
	v_fmac_f32_e32 v65, s100, v44
	v_readlane_b32 s99, v21, 43
	v_fmac_f32_e32 v66, s0, v41
	v_readlane_b32 s100, v20, 0
	v_fmac_f32_e32 v65, s98, v37
	v_readlane_b32 s0, v20, 1
	v_fmac_f32_e32 v66, s99, v30
	v_add_f32_e32 v21, v65, v66
	v_readlane_b32 s98, v20, 2
	v_fma_f32 v65, 0, s100, v20
	v_readlane_b32 s99, v20, 3
	v_fma_f32 v66, v27, s0, 0
	v_readlane_b32 s100, v20, 4
	v_fmac_f32_e32 v65, s98, v25
	v_readlane_b32 s0, v20, 5
	v_fmac_f32_e32 v66, s99, v23
	v_readlane_b32 s98, v20, 6
	v_fmac_f32_e32 v65, s100, v5
	v_readlane_b32 s99, v20, 7
	v_fmac_f32_e32 v66, s0, v22
	v_readlane_b32 s100, v20, 8
	v_fmac_f32_e32 v65, s98, v24
	v_readlane_b32 s0, v20, 9
	v_fmac_f32_e32 v66, s99, v26
	v_readlane_b32 s98, v20, 10
	v_fmac_f32_e32 v65, s100, v28
	v_readlane_b32 s99, v20, 11
	v_fmac_f32_e32 v66, s0, v31
	v_readlane_b32 s100, v20, 12
	v_fmac_f32_e32 v65, s98, v32
	v_readlane_b32 s0, v20, 13
	v_fmac_f32_e32 v66, s99, v33
	v_readlane_b32 s98, v20, 14
	v_fmac_f32_e32 v65, s100, v34
	v_readlane_b32 s99, v20, 15
	v_fmac_f32_e32 v66, s0, v35
	v_readlane_b32 s100, v20, 16
	v_fmac_f32_e32 v65, s98, v36
	v_readlane_b32 s0, v20, 17
	v_fmac_f32_e32 v66, s99, v38
	v_readlane_b32 s98, v20, 18
	v_fmac_f32_e32 v65, s100, v39
	v_readlane_b32 s99, v20, 19
	v_fmac_f32_e32 v66, s0, v40
	v_readlane_b32 s100, v20, 20
	v_fmac_f32_e32 v65, s98, v42
	v_readlane_b32 s0, v20, 21
	v_fmac_f32_e32 v66, s99, v43
	v_readlane_b32 s98, v20, 22
	v_fmac_f32_e32 v65, s100, v45
	v_readlane_b32 s99, v20, 23
	v_fmac_f32_e32 v66, s0, v46
	v_readlane_b32 s100, v20, 24
	v_fmac_f32_e32 v65, s98, v47
	v_readlane_b32 s0, v20, 25
	v_fmac_f32_e32 v66, s99, v49
	v_readlane_b32 s98, v20, 26
	v_fmac_f32_e32 v65, s100, v51
	v_readlane_b32 s99, v20, 27
	v_fmac_f32_e32 v66, s0, v52
	v_readlane_b32 s100, v20, 28
	v_fmac_f32_e32 v65, s98, v54
	v_readlane_b32 s0, v20, 29
	v_fmac_f32_e32 v66, s99, v56
	v_readlane_b32 s98, v20, 30
	v_fmac_f32_e32 v65, s100, v57
	v_readlane_b32 s99, v20, 31
	v_fmac_f32_e32 v66, s0, v59
	v_readlane_b32 s100, v20, 32
	v_fmac_f32_e32 v65, s98, v61
	v_readlane_b32 s0, v20, 33
	v_fmac_f32_e32 v66, s99, v63
	v_readlane_b32 s98, v20, 34
	v_fmac_f32_e32 v65, s100, v64
	v_readlane_b32 s99, v20, 35
	v_fmac_f32_e32 v66, s0, v62
	v_readlane_b32 s100, v20, 36
	v_fmac_f32_e32 v65, s98, v60
	v_readlane_b32 s0, v20, 37
	v_fmac_f32_e32 v66, s99, v58
	v_readlane_b32 s98, v20, 38
	v_fmac_f32_e32 v65, s100, v55
	v_readlane_b32 s99, v20, 39
	v_fmac_f32_e32 v66, s0, v53
	v_readlane_b32 s100, v20, 40
	v_fmac_f32_e32 v65, s98, v50
	v_readlane_b32 s0, v20, 41
	v_fmac_f32_e32 v66, s99, v48
	v_readlane_b32 s98, v20, 42
	v_fmac_f32_e32 v65, s100, v44
	v_readlane_b32 s99, v20, 43
	v_fmac_f32_e32 v66, s0, v41
	v_readlane_b32 s100, v20, 44
	v_fmac_f32_e32 v65, s98, v37
	v_readlane_b32 s0, v19, 0
	v_fmac_f32_e32 v66, s99, v30
	v_readlane_b32 s98, v19, 1
	v_fmac_f32_e32 v65, s100, v21
	v_add_f32_e32 v20, v66, v65
	v_readlane_b32 s99, v19, 2
	v_fma_f32 v65, 0, s0, v19
	v_readlane_b32 s100, v19, 3
	v_fma_f32 v66, v27, s98, 0
	v_readlane_b32 s0, v19, 4
	v_fmac_f32_e32 v65, s99, v25
	v_readlane_b32 s98, v19, 5
	v_fmac_f32_e32 v66, s100, v23
	v_readlane_b32 s99, v19, 6
	v_fmac_f32_e32 v65, s0, v5
	v_readlane_b32 s100, v19, 7
	v_fmac_f32_e32 v66, s98, v22
	v_readlane_b32 s0, v19, 8
	v_fmac_f32_e32 v65, s99, v24
	v_readlane_b32 s98, v19, 9
	v_fmac_f32_e32 v66, s100, v26
; __device__ __forceinline__ void ph_gdn_prep(const Params& p, LAS unsigned char* lds) {
;     ...
;             for (int i = 1; i < 64; ++i) { const int mi = __float_as_int(mcol[i]); float a0 = mcol[i], a1 = 0.f;
; #pragma unroll
;                 for (int j = 0; j < i; ++j) { const float s = __int_as_float(__builtin_amdgcn_readlane(mi, j)); if (j & 1) a1 += s * mcol[j]; else a0 += s * mcol[j]; }
;                 mcol[i] = a0 + a1; }
	v_readlane_b32 s99, v19, 10
	v_fmac_f32_e32 v65, s0, v28
	v_readlane_b32 s100, v19, 11
	v_fmac_f32_e32 v66, s98, v31
	v_readlane_b32 s0, v19, 12
	v_fmac_f32_e32 v65, s99, v32
	v_readlane_b32 s98, v19, 13
	v_fmac_f32_e32 v66, s100, v33
	v_readlane_b32 s99, v19, 14
	v_fmac_f32_e32 v65, s0, v34
	v_readlane_b32 s100, v19, 15
	v_fmac_f32_e32 v66, s98, v35
	v_readlane_b32 s0, v19, 16
	v_fmac_f32_e32 v65, s99, v36
	v_readlane_b32 s98, v19, 17
	v_fmac_f32_e32 v66, s100, v38
	v_readlane_b32 s99, v19, 18
	v_fmac_f32_e32 v65, s0, v39
	v_readlane_b32 s100, v19, 19
	v_fmac_f32_e32 v66, s98, v40
	v_readlane_b32 s0, v19, 20
	v_fmac_f32_e32 v65, s99, v42
	v_readlane_b32 s98, v19, 21
	v_fmac_f32_e32 v66, s100, v43
	v_readlane_b32 s99, v19, 22
	v_fmac_f32_e32 v65, s0, v45
	v_readlane_b32 s100, v19, 23
	v_fmac_f32_e32 v66, s98, v46
	v_readlane_b32 s0, v19, 24
	v_fmac_f32_e32 v65, s99, v47
	v_readlane_b32 s98, v19, 25
	v_fmac_f32_e32 v66, s100, v49
	v_readlane_b32 s99, v19, 26
	v_fmac_f32_e32 v65, s0, v51
	v_readlane_b32 s100, v19, 27
	v_fmac_f32_e32 v66, s98, v52
	v_readlane_b32 s0, v19, 28
	v_fmac_f32_e32 v65, s99, v54
	v_readlane_b32 s98, v19, 29
	v_fmac_f32_e32 v66, s100, v56
	v_readlane_b32 s99, v19, 30
	v_fmac_f32_e32 v65, s0, v57
	v_readlane_b32 s100, v19, 31
	v_fmac_f32_e32 v66, s98, v59
	v_readlane_b32 s0, v19, 32
	v_fmac_f32_e32 v65, s99, v61
	v_readlane_b32 s98, v19, 33
	v_fmac_f32_e32 v66, s100, v63
	v_readlane_b32 s99, v19, 34
	v_fmac_f32_e32 v65, s0, v64
	v_readlane_b32 s100, v19, 35
	v_fmac_f32_e32 v66, s98, v62
	v_readlane_b32 s0, v19, 36
	v_fmac_f32_e32 v65, s99, v60
	v_readlane_b32 s98, v19, 37
	v_fmac_f32_e32 v66, s100, v58
	v_readlane_b32 s99, v19, 38
	v_fmac_f32_e32 v65, s0, v55
	v_readlane_b32 s100, v19, 39
	v_fmac_f32_e32 v66, s98, v53
	v_readlane_b32 s0, v19, 40
	v_fmac_f32_e32 v65, s99, v50
	v_readlane_b32 s98, v19, 41
	v_fmac_f32_e32 v66, s100, v48
	v_readlane_b32 s99, v19, 42
	v_fmac_f32_e32 v65, s0, v44
	v_readlane_b32 s100, v19, 43
	v_fmac_f32_e32 v66, s98, v41
	v_readlane_b32 s0, v19, 44
	v_fmac_f32_e32 v65, s99, v37
	v_readlane_b32 s98, v19, 45
	v_fmac_f32_e32 v66, s100, v30
	v_readlane_b32 s99, v18, 0
	v_fmac_f32_e32 v65, s0, v21
	v_readlane_b32 s100, v18, 1
	v_fmac_f32_e32 v66, s98, v20
	v_add_f32_e32 v19, v65, v66
	v_readlane_b32 s0, v18, 2
	v_fma_f32 v65, 0, s99, v18
	v_readlane_b32 s98, v18, 3
	v_fma_f32 v66, v27, s100, 0
	v_readlane_b32 s99, v18, 4
	v_fmac_f32_e32 v65, s0, v25
	v_readlane_b32 s100, v18, 5
	v_fmac_f32_e32 v66, s98, v23
	v_readlane_b32 s0, v18, 6
	v_fmac_f32_e32 v65, s99, v5
	v_readlane_b32 s98, v18, 7
	v_fmac_f32_e32 v66, s100, v22
	v_readlane_b32 s99, v18, 8
	v_fmac_f32_e32 v65, s0, v24
	v_readlane_b32 s100, v18, 9
	v_fmac_f32_e32 v66, s98, v26
	v_readlane_b32 s0, v18, 10
	v_fmac_f32_e32 v65, s99, v28
	v_readlane_b32 s98, v18, 11
	v_fmac_f32_e32 v66, s100, v31
	v_readlane_b32 s99, v18, 12
	v_fmac_f32_e32 v65, s0, v32
	v_readlane_b32 s100, v18, 13
	v_fmac_f32_e32 v66, s98, v33
	v_readlane_b32 s0, v18, 14
	v_fmac_f32_e32 v65, s99, v34
	v_readlane_b32 s98, v18, 15
	v_fmac_f32_e32 v66, s100, v35
	v_readlane_b32 s99, v18, 16
	v_fmac_f32_e32 v65, s0, v36
	v_readlane_b32 s100, v18, 17
	v_fmac_f32_e32 v66, s98, v38
	v_readlane_b32 s0, v18, 18
	v_fmac_f32_e32 v65, s99, v39
	v_readlane_b32 s98, v18, 19
	v_fmac_f32_e32 v66, s100, v40
	v_readlane_b32 s99, v18, 20
	v_fmac_f32_e32 v65, s0, v42
	v_readlane_b32 s100, v18, 21
	v_fmac_f32_e32 v66, s98, v43
	v_readlane_b32 s0, v18, 22
	v_fmac_f32_e32 v65, s99, v45
	v_readlane_b32 s98, v18, 23
	v_fmac_f32_e32 v66, s100, v46
	v_readlane_b32 s99, v18, 24
	v_fmac_f32_e32 v65, s0, v47
	v_readlane_b32 s100, v18, 25
	v_fmac_f32_e32 v66, s98, v49
	v_readlane_b32 s0, v18, 26
	v_fmac_f32_e32 v65, s99, v51
	v_readlane_b32 s98, v18, 27
	v_fmac_f32_e32 v66, s100, v52
	v_readlane_b32 s99, v18, 28
	v_fmac_f32_e32 v65, s0, v54
	v_readlane_b32 s100, v18, 29
	v_fmac_f32_e32 v66, s98, v56
	v_readlane_b32 s0, v18, 30
	v_fmac_f32_e32 v65, s99, v57
	v_readlane_b32 s98, v18, 31
	v_fmac_f32_e32 v66, s100, v59
	v_readlane_b32 s99, v18, 32
	v_fmac_f32_e32 v65, s0, v61
	v_readlane_b32 s100, v18, 33
	v_fmac_f32_e32 v66, s98, v63
	v_readlane_b32 s0, v18, 34
	v_fmac_f32_e32 v65, s99, v64
	v_readlane_b32 s98, v18, 35
	v_fmac_f32_e32 v66, s100, v62
	v_readlane_b32 s99, v18, 36
	v_fmac_f32_e32 v65, s0, v60
	v_readlane_b32 s100, v18, 37
	v_fmac_f32_e32 v66, s98, v58
	v_readlane_b32 s0, v18, 38
	v_fmac_f32_e32 v65, s99, v55
	v_readlane_b32 s98, v18, 39
	v_fmac_f32_e32 v66, s100, v53
	v_readlane_b32 s99, v18, 40
	v_fmac_f32_e32 v65, s0, v50
	v_readlane_b32 s100, v18, 41
	v_fmac_f32_e32 v66, s98, v48
	v_readlane_b32 s0, v18, 42
	v_fmac_f32_e32 v65, s99, v44
	v_readlane_b32 s98, v18, 43
	v_fmac_f32_e32 v66, s100, v41
	v_readlane_b32 s99, v18, 44
	v_fmac_f32_e32 v65, s0, v37
	v_readlane_b32 s100, v18, 45
	v_fmac_f32_e32 v66, s98, v30
	v_readlane_b32 s0, v18, 46
	v_fmac_f32_e32 v65, s99, v21
	v_readlane_b32 s98, v17, 0
	v_fmac_f32_e32 v66, s100, v20
	v_readlane_b32 s99, v17, 1
	v_fmac_f32_e32 v65, s0, v19
	v_add_f32_e32 v18, v66, v65
	v_readlane_b32 s100, v17, 2
	v_fma_f32 v65, 0, s98, v17
	v_readlane_b32 s0, v17, 3
	v_fma_f32 v66, v27, s99, 0
	v_readlane_b32 s98, v17, 4
	v_fmac_f32_e32 v65, s100, v25
	v_readlane_b32 s99, v17, 5
	v_fmac_f32_e32 v66, s0, v23
	v_readlane_b32 s100, v17, 6
	v_fmac_f32_e32 v65, s98, v5
	v_readlane_b32 s0, v17, 7
	v_fmac_f32_e32 v66, s99, v22
	v_readlane_b32 s98, v17, 8
	v_fmac_f32_e32 v65, s100, v24
	v_readlane_b32 s99, v17, 9
	v_fmac_f32_e32 v66, s0, v26
	v_readlane_b32 s100, v17, 10
	v_fmac_f32_e32 v65, s98, v28
	v_readlane_b32 s0, v17, 11
	v_fmac_f32_e32 v66, s99, v31
; __device__ __forceinline__ void ph_gdn_prep(const Params& p, LAS unsigned char* lds) {
;     ...
;             for (int i = 1; i < 64; ++i) { const int mi = __float_as_int(mcol[i]); float a0 = mcol[i], a1 = 0.f;
; #pragma unroll
;                 for (int j = 0; j < i; ++j) { const float s = __int_as_float(__builtin_amdgcn_readlane(mi, j)); if (j & 1) a1 += s * mcol[j]; else a0 += s * mcol[j]; }
;                 mcol[i] = a0 + a1; }
	v_readlane_b32 s98, v17, 12
	v_fmac_f32_e32 v65, s100, v32
	v_readlane_b32 s99, v17, 13
	v_fmac_f32_e32 v66, s0, v33
	v_readlane_b32 s100, v17, 14
	v_fmac_f32_e32 v65, s98, v34
	v_readlane_b32 s0, v17, 15
	v_fmac_f32_e32 v66, s99, v35
	v_readlane_b32 s98, v17, 16
	v_fmac_f32_e32 v65, s100, v36
	v_readlane_b32 s99, v17, 17
	v_fmac_f32_e32 v66, s0, v38
	v_readlane_b32 s100, v17, 18
	v_fmac_f32_e32 v65, s98, v39
	v_readlane_b32 s0, v17, 19
	v_fmac_f32_e32 v66, s99, v40
	v_readlane_b32 s98, v17, 20
	v_fmac_f32_e32 v65, s100, v42
	v_readlane_b32 s99, v17, 21
	v_fmac_f32_e32 v66, s0, v43
	v_readlane_b32 s100, v17, 22
	v_fmac_f32_e32 v65, s98, v45
	v_readlane_b32 s0, v17, 23
	v_fmac_f32_e32 v66, s99, v46
	v_readlane_b32 s98, v17, 24
	v_fmac_f32_e32 v65, s100, v47
	v_readlane_b32 s99, v17, 25
	v_fmac_f32_e32 v66, s0, v49
	v_readlane_b32 s100, v17, 26
	v_fmac_f32_e32 v65, s98, v51
	v_readlane_b32 s0, v17, 27
	v_fmac_f32_e32 v66, s99, v52
	v_readlane_b32 s98, v17, 28
	v_fmac_f32_e32 v65, s100, v54
	v_readlane_b32 s99, v17, 29
	v_fmac_f32_e32 v66, s0, v56
	v_readlane_b32 s100, v17, 30
	v_fmac_f32_e32 v65, s98, v57
	v_readlane_b32 s0, v17, 31
	v_fmac_f32_e32 v66, s99, v59
	v_readlane_b32 s98, v17, 32
	v_fmac_f32_e32 v65, s100, v61
	v_readlane_b32 s99, v17, 33
	v_fmac_f32_e32 v66, s0, v63
	v_readlane_b32 s100, v17, 34
	v_fmac_f32_e32 v65, s98, v64
	v_readlane_b32 s0, v17, 35
	v_fmac_f32_e32 v66, s99, v62
	v_readlane_b32 s98, v17, 36
	v_fmac_f32_e32 v65, s100, v60
	v_readlane_b32 s99, v17, 37
	v_fmac_f32_e32 v66, s0, v58
	v_readlane_b32 s100, v17, 38
	v_fmac_f32_e32 v65, s98, v55
	v_readlane_b32 s0, v17, 39
	v_fmac_f32_e32 v66, s99, v53
	v_readlane_b32 s98, v17, 40
	v_fmac_f32_e32 v65, s100, v50
	v_readlane_b32 s99, v17, 41
	v_fmac_f32_e32 v66, s0, v48
	v_readlane_b32 s100, v17, 42
	v_fmac_f32_e32 v65, s98, v44
	v_readlane_b32 s0, v17, 43
	v_fmac_f32_e32 v66, s99, v41
	v_readlane_b32 s98, v17, 44
	v_fmac_f32_e32 v65, s100, v37
	v_readlane_b32 s99, v17, 45
	v_fmac_f32_e32 v66, s0, v30
	v_readlane_b32 s100, v17, 46
	v_fmac_f32_e32 v65, s98, v21
	v_readlane_b32 s0, v17, 47
	v_fmac_f32_e32 v66, s99, v20
	v_readlane_b32 s98, v16, 0
	v_fmac_f32_e32 v65, s100, v19
	v_readlane_b32 s99, v16, 1
	v_fmac_f32_e32 v66, s0, v18
	v_add_f32_e32 v17, v65, v66
	v_readlane_b32 s100, v16, 2
	v_fma_f32 v65, 0, s98, v16
	v_readlane_b32 s0, v16, 3
	v_fma_f32 v66, v27, s99, 0
	v_readlane_b32 s98, v16, 4
	v_fmac_f32_e32 v65, s100, v25
	v_readlane_b32 s99, v16, 5
	v_fmac_f32_e32 v66, s0, v23
	v_readlane_b32 s100, v16, 6
	v_fmac_f32_e32 v65, s98, v5
	v_readlane_b32 s0, v16, 7
	v_fmac_f32_e32 v66, s99, v22
	v_readlane_b32 s98, v16, 8
	v_fmac_f32_e32 v65, s100, v24
	v_readlane_b32 s99, v16, 9
	v_fmac_f32_e32 v66, s0, v26
	v_readlane_b32 s100, v16, 10
	v_fmac_f32_e32 v65, s98, v28
	v_readlane_b32 s0, v16, 11
	v_fmac_f32_e32 v66, s99, v31
	v_readlane_b32 s98, v16, 12
	v_fmac_f32_e32 v65, s100, v32
	v_readlane_b32 s99, v16, 13
	v_fmac_f32_e32 v66, s0, v33
	v_readlane_b32 s100, v16, 14
	v_fmac_f32_e32 v65, s98, v34
	v_readlane_b32 s0, v16, 15
	v_fmac_f32_e32 v66, s99, v35
	v_readlane_b32 s98, v16, 16
	v_fmac_f32_e32 v65, s100, v36
	v_readlane_b32 s99, v16, 17
	v_fmac_f32_e32 v66, s0, v38
	v_readlane_b32 s100, v16, 18
	v_fmac_f32_e32 v65, s98, v39
	v_readlane_b32 s0, v16, 19
	v_fmac_f32_e32 v66, s99, v40
	v_readlane_b32 s98, v16, 20
	v_fmac_f32_e32 v65, s100, v42
	v_readlane_b32 s99, v16, 21
	v_fmac_f32_e32 v66, s0, v43
	v_readlane_b32 s100, v16, 22
	v_fmac_f32_e32 v65, s98, v45
	v_readlane_b32 s0, v16, 23
	v_fmac_f32_e32 v66, s99, v46
	v_readlane_b32 s98, v16, 24
	v_fmac_f32_e32 v65, s100, v47
	v_readlane_b32 s99, v16, 25
	v_fmac_f32_e32 v66, s0, v49
	v_readlane_b32 s100, v16, 26
	v_fmac_f32_e32 v65, s98, v51
	v_readlane_b32 s0, v16, 27
	v_fmac_f32_e32 v66, s99, v52
	v_readlane_b32 s98, v16, 28
	v_fmac_f32_e32 v65, s100, v54
	v_readlane_b32 s99, v16, 29
	v_fmac_f32_e32 v66, s0, v56
	v_readlane_b32 s100, v16, 30
	v_fmac_f32_e32 v65, s98, v57
	v_readlane_b32 s0, v16, 31
	v_fmac_f32_e32 v66, s99, v59
	v_readlane_b32 s98, v16, 32
	v_fmac_f32_e32 v65, s100, v61
	v_readlane_b32 s99, v16, 33
	v_fmac_f32_e32 v66, s0, v63
	v_readlane_b32 s100, v16, 34
	v_fmac_f32_e32 v65, s98, v64
	v_readlane_b32 s0, v16, 35
	v_fmac_f32_e32 v66, s99, v62
	v_readlane_b32 s98, v16, 36
	v_fmac_f32_e32 v65, s100, v60
	v_readlane_b32 s99, v16, 37
	v_fmac_f32_e32 v66, s0, v58
	v_readlane_b32 s100, v16, 38
	v_fmac_f32_e32 v65, s98, v55
	v_readlane_b32 s0, v16, 39
	v_fmac_f32_e32 v66, s99, v53
	v_readlane_b32 s98, v16, 40
	v_fmac_f32_e32 v65, s100, v50
	v_readlane_b32 s99, v16, 41
	v_fmac_f32_e32 v66, s0, v48
	v_readlane_b32 s100, v16, 42
	v_fmac_f32_e32 v65, s98, v44
	v_readlane_b32 s0, v16, 43
	v_fmac_f32_e32 v66, s99, v41
	v_readlane_b32 s98, v16, 44
	v_fmac_f32_e32 v65, s100, v37
	v_readlane_b32 s99, v16, 45
	v_fmac_f32_e32 v66, s0, v30
	v_readlane_b32 s100, v16, 46
	v_fmac_f32_e32 v65, s98, v21
	v_readlane_b32 s0, v16, 47
	v_fmac_f32_e32 v66, s99, v20
	v_readlane_b32 s98, v16, 48
	v_fmac_f32_e32 v65, s100, v19
	v_readlane_b32 s99, v15, 0
	v_fmac_f32_e32 v66, s0, v18
	v_readlane_b32 s100, v15, 1
	v_fmac_f32_e32 v65, s98, v17
	v_add_f32_e32 v16, v66, v65
	v_readlane_b32 s0, v15, 2
	v_fma_f32 v65, 0, s99, v15
	v_readlane_b32 s98, v15, 3
	v_fma_f32 v66, v27, s100, 0
	v_readlane_b32 s99, v15, 4
	v_fmac_f32_e32 v65, s0, v25
	v_readlane_b32 s100, v15, 5
	v_fmac_f32_e32 v66, s98, v23
	v_readlane_b32 s0, v15, 6
	v_fmac_f32_e32 v65, s99, v5
	v_readlane_b32 s98, v15, 7
	v_fmac_f32_e32 v66, s100, v22
	v_readlane_b32 s99, v15, 8
	v_fmac_f32_e32 v65, s0, v24
	v_readlane_b32 s100, v15, 9
	v_fmac_f32_e32 v66, s98, v26
; __device__ __forceinline__ void ph_gdn_prep(const Params& p, LAS unsigned char* lds) {
;     ...
;             for (int i = 1; i < 64; ++i) { const int mi = __float_as_int(mcol[i]); float a0 = mcol[i], a1 = 0.f;
; #pragma unroll
;                 for (int j = 0; j < i; ++j) { const float s = __int_as_float(__builtin_amdgcn_readlane(mi, j)); if (j & 1) a1 += s * mcol[j]; else a0 += s * mcol[j]; }
;                 mcol[i] = a0 + a1; }
	v_readlane_b32 s0, v15, 10
	v_fmac_f32_e32 v65, s99, v28
	v_readlane_b32 s98, v15, 11
	v_fmac_f32_e32 v66, s100, v31
	v_readlane_b32 s99, v15, 12
	v_fmac_f32_e32 v65, s0, v32
	v_readlane_b32 s100, v15, 13
	v_fmac_f32_e32 v66, s98, v33
	v_readlane_b32 s0, v15, 14
	v_fmac_f32_e32 v65, s99, v34
	v_readlane_b32 s98, v15, 15
	v_fmac_f32_e32 v66, s100, v35
	v_readlane_b32 s99, v15, 16
	v_fmac_f32_e32 v65, s0, v36
	v_readlane_b32 s100, v15, 17
	v_fmac_f32_e32 v66, s98, v38
	v_readlane_b32 s0, v15, 18
	v_fmac_f32_e32 v65, s99, v39
	v_readlane_b32 s98, v15, 19
	v_fmac_f32_e32 v66, s100, v40
	v_readlane_b32 s99, v15, 20
	v_fmac_f32_e32 v65, s0, v42
	v_readlane_b32 s100, v15, 21
	v_fmac_f32_e32 v66, s98, v43
	v_readlane_b32 s0, v15, 22
	v_fmac_f32_e32 v65, s99, v45
	v_readlane_b32 s98, v15, 23
	v_fmac_f32_e32 v66, s100, v46
	v_readlane_b32 s99, v15, 24
	v_fmac_f32_e32 v65, s0, v47
	v_readlane_b32 s100, v15, 25
	v_fmac_f32_e32 v66, s98, v49
	v_readlane_b32 s0, v15, 26
	v_fmac_f32_e32 v65, s99, v51
	v_readlane_b32 s98, v15, 27
	v_fmac_f32_e32 v66, s100, v52
	v_readlane_b32 s99, v15, 28
	v_fmac_f32_e32 v65, s0, v54
	v_readlane_b32 s100, v15, 29
	v_fmac_f32_e32 v66, s98, v56
	v_readlane_b32 s0, v15, 30
	v_fmac_f32_e32 v65, s99, v57
	v_readlane_b32 s98, v15, 31
	v_fmac_f32_e32 v66, s100, v59
	v_readlane_b32 s99, v15, 32
	v_fmac_f32_e32 v65, s0, v61
	v_readlane_b32 s100, v15, 33
	v_fmac_f32_e32 v66, s98, v63
	v_readlane_b32 s0, v15, 34
	v_fmac_f32_e32 v65, s99, v64
	v_readlane_b32 s98, v15, 35
	v_fmac_f32_e32 v66, s100, v62
	v_readlane_b32 s99, v15, 36
	v_fmac_f32_e32 v65, s0, v60
	v_readlane_b32 s100, v15, 37
	v_fmac_f32_e32 v66, s98, v58
	v_readlane_b32 s0, v15, 38
	v_fmac_f32_e32 v65, s99, v55
	v_readlane_b32 s98, v15, 39
	v_fmac_f32_e32 v66, s100, v53
	v_readlane_b32 s99, v15, 40
	v_fmac_f32_e32 v65, s0, v50
	v_readlane_b32 s100, v15, 41
	v_fmac_f32_e32 v66, s98, v48
	v_readlane_b32 s0, v15, 42
	v_fmac_f32_e32 v65, s99, v44
	v_readlane_b32 s98, v15, 43
	v_fmac_f32_e32 v66, s100, v41
	v_readlane_b32 s99, v15, 44
	v_fmac_f32_e32 v65, s0, v37
	v_readlane_b32 s100, v15, 45
	v_fmac_f32_e32 v66, s98, v30
	v_readlane_b32 s0, v15, 46
	v_fmac_f32_e32 v65, s99, v21
	v_readlane_b32 s98, v15, 47
	v_fmac_f32_e32 v66, s100, v20
	v_readlane_b32 s99, v15, 48
	v_fmac_f32_e32 v65, s0, v19
	v_readlane_b32 s100, v15, 49
	v_fmac_f32_e32 v66, s98, v18
	v_readlane_b32 s0, v14, 0
	v_fmac_f32_e32 v65, s99, v17
	v_readlane_b32 s98, v14, 1
	v_fmac_f32_e32 v66, s100, v16
	v_add_f32_e32 v15, v65, v66
	v_readlane_b32 s99, v14, 2
	v_fma_f32 v65, 0, s0, v14
	v_readlane_b32 s100, v14, 3
	v_fma_f32 v66, v27, s98, 0
	v_readlane_b32 s0, v14, 4
	v_fmac_f32_e32 v65, s99, v25
	v_readlane_b32 s98, v14, 5
	v_fmac_f32_e32 v66, s100, v23
	v_readlane_b32 s99, v14, 6
	v_fmac_f32_e32 v65, s0, v5
	v_readlane_b32 s100, v14, 7
	v_fmac_f32_e32 v66, s98, v22
	v_readlane_b32 s0, v14, 8
	v_fmac_f32_e32 v65, s99, v24
	v_readlane_b32 s98, v14, 9
	v_fmac_f32_e32 v66, s100, v26
	v_readlane_b32 s99, v14, 10
	v_fmac_f32_e32 v65, s0, v28
	v_readlane_b32 s100, v14, 11
	v_fmac_f32_e32 v66, s98, v31
	v_readlane_b32 s0, v14, 12
	v_fmac_f32_e32 v65, s99, v32
	v_readlane_b32 s98, v14, 13
	v_fmac_f32_e32 v66, s100, v33
	v_readlane_b32 s99, v14, 14
	v_fmac_f32_e32 v65, s0, v34
	v_readlane_b32 s100, v14, 15
	v_fmac_f32_e32 v66, s98, v35
	v_readlane_b32 s0, v14, 16
	v_fmac_f32_e32 v65, s99, v36
	v_readlane_b32 s98, v14, 17
	v_fmac_f32_e32 v66, s100, v38
	v_readlane_b32 s99, v14, 18
	v_fmac_f32_e32 v65, s0, v39
	v_readlane_b32 s100, v14, 19
	v_fmac_f32_e32 v66, s98, v40
	v_readlane_b32 s0, v14, 20
	v_fmac_f32_e32 v65, s99, v42
	v_readlane_b32 s98, v14, 21
	v_fmac_f32_e32 v66, s100, v43
	v_readlane_b32 s99, v14, 22
	v_fmac_f32_e32 v65, s0, v45
	v_readlane_b32 s100, v14, 23
	v_fmac_f32_e32 v66, s98, v46
	v_readlane_b32 s0, v14, 24
	v_fmac_f32_e32 v65, s99, v47
	v_readlane_b32 s98, v14, 25
	v_fmac_f32_e32 v66, s100, v49
	v_readlane_b32 s99, v14, 26
	v_fmac_f32_e32 v65, s0, v51
	v_readlane_b32 s100, v14, 27
	v_fmac_f32_e32 v66, s98, v52
	v_readlane_b32 s0, v14, 28
	v_fmac_f32_e32 v65, s99, v54
	v_readlane_b32 s98, v14, 29
	v_fmac_f32_e32 v66, s100, v56
	v_readlane_b32 s99, v14, 30
	v_fmac_f32_e32 v65, s0, v57
	v_readlane_b32 s100, v14, 31
	v_fmac_f32_e32 v66, s98, v59
	v_readlane_b32 s0, v14, 32
	v_fmac_f32_e32 v65, s99, v61
	v_readlane_b32 s98, v14, 33
	v_fmac_f32_e32 v66, s100, v63
	v_readlane_b32 s99, v14, 34
	v_fmac_f32_e32 v65, s0, v64
	v_readlane_b32 s100, v14, 35
	v_fmac_f32_e32 v66, s98, v62
	v_readlane_b32 s0, v14, 36
	v_fmac_f32_e32 v65, s99, v60
	v_readlane_b32 s98, v14, 37
	v_fmac_f32_e32 v66, s100, v58
	v_readlane_b32 s99, v14, 38
	v_fmac_f32_e32 v65, s0, v55
	v_readlane_b32 s100, v14, 39
	v_fmac_f32_e32 v66, s98, v53
	v_readlane_b32 s0, v14, 40
	v_fmac_f32_e32 v65, s99, v50
	v_readlane_b32 s98, v14, 41
	v_fmac_f32_e32 v66, s100, v48
	v_readlane_b32 s99, v14, 42
	v_fmac_f32_e32 v65, s0, v44
	v_readlane_b32 s100, v14, 43
	v_fmac_f32_e32 v66, s98, v41
	v_readlane_b32 s0, v14, 44
	v_fmac_f32_e32 v65, s99, v37
	v_readlane_b32 s98, v14, 45
	v_fmac_f32_e32 v66, s100, v30
	v_readlane_b32 s99, v14, 46
	v_fmac_f32_e32 v65, s0, v21
	v_readlane_b32 s100, v14, 47
	v_fmac_f32_e32 v66, s98, v20
	v_readlane_b32 s0, v14, 48
	v_fmac_f32_e32 v65, s99, v19
	v_readlane_b32 s98, v14, 49
	v_fmac_f32_e32 v66, s100, v18
	v_readlane_b32 s99, v14, 50
	v_fmac_f32_e32 v65, s0, v17
	v_readlane_b32 s100, v12, 0
	v_fmac_f32_e32 v66, s98, v16
	v_readlane_b32 s0, v12, 1
	v_fmac_f32_e32 v65, s99, v15
	v_add_f32_e32 v14, v66, v65
	v_readlane_b32 s98, v12, 2
	v_fma_f32 v65, 0, s100, v12
	v_readlane_b32 s99, v12, 3
	v_fma_f32 v66, v27, s0, 0
; __device__ __forceinline__ void ph_gdn_prep(const Params& p, LAS unsigned char* lds) {
;     ...
;             for (int i = 1; i < 64; ++i) { const int mi = __float_as_int(mcol[i]); float a0 = mcol[i], a1 = 0.f;
; #pragma unroll
;                 for (int j = 0; j < i; ++j) { const float s = __int_as_float(__builtin_amdgcn_readlane(mi, j)); if (j & 1) a1 += s * mcol[j]; else a0 += s * mcol[j]; }
;                 mcol[i] = a0 + a1; }
	v_readlane_b32 s100, v12, 4
	v_fmac_f32_e32 v65, s98, v25
	v_readlane_b32 s0, v12, 5
	v_fmac_f32_e32 v66, s99, v23
	v_readlane_b32 s98, v12, 6
	v_fmac_f32_e32 v65, s100, v5
	v_readlane_b32 s99, v12, 7
	v_fmac_f32_e32 v66, s0, v22
	v_readlane_b32 s100, v12, 8
	v_fmac_f32_e32 v65, s98, v24
	v_readlane_b32 s0, v12, 9
	v_fmac_f32_e32 v66, s99, v26
	v_readlane_b32 s98, v12, 10
	v_fmac_f32_e32 v65, s100, v28
	v_readlane_b32 s99, v12, 11
	v_fmac_f32_e32 v66, s0, v31
	v_readlane_b32 s100, v12, 12
	v_fmac_f32_e32 v65, s98, v32
	v_readlane_b32 s0, v12, 13
	v_fmac_f32_e32 v66, s99, v33
	v_readlane_b32 s98, v12, 14
	v_fmac_f32_e32 v65, s100, v34
	v_readlane_b32 s99, v12, 15
	v_fmac_f32_e32 v66, s0, v35
	v_readlane_b32 s100, v12, 16
	v_fmac_f32_e32 v65, s98, v36
	v_readlane_b32 s0, v12, 17
	v_fmac_f32_e32 v66, s99, v38
	v_readlane_b32 s98, v12, 18
	v_fmac_f32_e32 v65, s100, v39
	v_readlane_b32 s99, v12, 19
	v_fmac_f32_e32 v66, s0, v40
	v_readlane_b32 s100, v12, 20
	v_fmac_f32_e32 v65, s98, v42
	v_readlane_b32 s0, v12, 21
	v_fmac_f32_e32 v66, s99, v43
	v_readlane_b32 s98, v12, 22
	v_fmac_f32_e32 v65, s100, v45
	v_readlane_b32 s99, v12, 23
	v_fmac_f32_e32 v66, s0, v46
	v_readlane_b32 s100, v12, 24
	v_fmac_f32_e32 v65, s98, v47
	v_readlane_b32 s0, v12, 25
	v_fmac_f32_e32 v66, s99, v49
	v_readlane_b32 s98, v12, 26
	v_fmac_f32_e32 v65, s100, v51
	v_readlane_b32 s99, v12, 27
	v_fmac_f32_e32 v66, s0, v52
	v_readlane_b32 s100, v12, 28
	v_fmac_f32_e32 v65, s98, v54
	v_readlane_b32 s0, v12, 29
	v_fmac_f32_e32 v66, s99, v56
	v_readlane_b32 s98, v12, 30
	v_fmac_f32_e32 v65, s100, v57
	v_readlane_b32 s99, v12, 31
	v_fmac_f32_e32 v66, s0, v59
	v_readlane_b32 s100, v12, 32
	v_fmac_f32_e32 v65, s98, v61
	v_readlane_b32 s0, v12, 33
	v_fmac_f32_e32 v66, s99, v63
	v_readlane_b32 s98, v12, 34
	v_fmac_f32_e32 v65, s100, v64
	v_readlane_b32 s99, v12, 35
	v_fmac_f32_e32 v66, s0, v62
	v_readlane_b32 s100, v12, 36
	v_fmac_f32_e32 v65, s98, v60
	v_readlane_b32 s0, v12, 37
	v_fmac_f32_e32 v66, s99, v58
	v_readlane_b32 s98, v12, 38
	v_fmac_f32_e32 v65, s100, v55
	v_readlane_b32 s99, v12, 39
	v_fmac_f32_e32 v66, s0, v53
	v_readlane_b32 s100, v12, 40
	v_fmac_f32_e32 v65, s98, v50
	v_readlane_b32 s0, v12, 41
	v_fmac_f32_e32 v66, s99, v48
	v_readlane_b32 s98, v12, 42
	v_fmac_f32_e32 v65, s100, v44
	v_readlane_b32 s99, v12, 43
	v_fmac_f32_e32 v66, s0, v41
	v_readlane_b32 s100, v12, 44
	v_fmac_f32_e32 v65, s98, v37
	v_readlane_b32 s0, v12, 45
	v_fmac_f32_e32 v66, s99, v30
	v_readlane_b32 s98, v12, 46
	v_fmac_f32_e32 v65, s100, v21
	v_readlane_b32 s99, v12, 47
	v_fmac_f32_e32 v66, s0, v20
	v_readlane_b32 s100, v12, 48
	v_fmac_f32_e32 v65, s98, v19
	v_readlane_b32 s0, v12, 49
	v_fmac_f32_e32 v66, s99, v18
	v_readlane_b32 s98, v12, 50
	v_fmac_f32_e32 v65, s100, v17
	v_readlane_b32 s99, v12, 51
	v_fmac_f32_e32 v66, s0, v16
	v_readlane_b32 s100, v11, 0
	v_fmac_f32_e32 v65, s98, v15
	v_readlane_b32 s0, v11, 1
	v_fmac_f32_e32 v66, s99, v14
	v_add_f32_e32 v12, v65, v66
	v_readlane_b32 s98, v11, 2
	v_fma_f32 v65, 0, s100, v11
	v_readlane_b32 s99, v11, 3
	v_fma_f32 v66, v27, s0, 0
	v_readlane_b32 s100, v11, 4
	v_fmac_f32_e32 v65, s98, v25
	v_readlane_b32 s0, v11, 5
	v_fmac_f32_e32 v66, s99, v23
	v_readlane_b32 s98, v11, 6
	v_fmac_f32_e32 v65, s100, v5
	v_readlane_b32 s99, v11, 7
	v_fmac_f32_e32 v66, s0, v22
	v_readlane_b32 s100, v11, 8
	v_fmac_f32_e32 v65, s98, v24
	v_readlane_b32 s0, v11, 9
	v_fmac_f32_e32 v66, s99, v26
	v_readlane_b32 s98, v11, 10
	v_fmac_f32_e32 v65, s100, v28
	v_readlane_b32 s99, v11, 11
	v_fmac_f32_e32 v66, s0, v31
	v_readlane_b32 s100, v11, 12
	v_fmac_f32_e32 v65, s98, v32
	v_readlane_b32 s0, v11, 13
	v_fmac_f32_e32 v66, s99, v33
	v_readlane_b32 s98, v11, 14
	v_fmac_f32_e32 v65, s100, v34
	v_readlane_b32 s99, v11, 15
	v_fmac_f32_e32 v66, s0, v35
	v_readlane_b32 s100, v11, 16
	v_fmac_f32_e32 v65, s98, v36
	v_readlane_b32 s0, v11, 17
	v_fmac_f32_e32 v66, s99, v38
	v_readlane_b32 s98, v11, 18
	v_fmac_f32_e32 v65, s100, v39
	v_readlane_b32 s99, v11, 19
	v_fmac_f32_e32 v66, s0, v40
	v_readlane_b32 s100, v11, 20
	v_fmac_f32_e32 v65, s98, v42
	v_readlane_b32 s0, v11, 21
	v_fmac_f32_e32 v66, s99, v43
	v_readlane_b32 s98, v11, 22
	v_fmac_f32_e32 v65, s100, v45
	v_readlane_b32 s99, v11, 23
	v_fmac_f32_e32 v66, s0, v46
	v_readlane_b32 s100, v11, 24
	v_fmac_f32_e32 v65, s98, v47
	v_readlane_b32 s0, v11, 25
	v_fmac_f32_e32 v66, s99, v49
	v_readlane_b32 s98, v11, 26
	v_fmac_f32_e32 v65, s100, v51
	v_readlane_b32 s99, v11, 27
	v_fmac_f32_e32 v66, s0, v52
	v_readlane_b32 s100, v11, 28
	v_fmac_f32_e32 v65, s98, v54
	v_readlane_b32 s0, v11, 29
	v_fmac_f32_e32 v66, s99, v56
	v_readlane_b32 s98, v11, 30
	v_fmac_f32_e32 v65, s100, v57
	v_readlane_b32 s99, v11, 31
	v_fmac_f32_e32 v66, s0, v59
	v_readlane_b32 s100, v11, 32
	v_fmac_f32_e32 v65, s98, v61
	v_readlane_b32 s0, v11, 33
	v_fmac_f32_e32 v66, s99, v63
	v_readlane_b32 s98, v11, 34
	v_fmac_f32_e32 v65, s100, v64
	v_readlane_b32 s99, v11, 35
	v_fmac_f32_e32 v66, s0, v62
	v_readlane_b32 s100, v11, 36
	v_fmac_f32_e32 v65, s98, v60
	v_readlane_b32 s0, v11, 37
	v_fmac_f32_e32 v66, s99, v58
	v_readlane_b32 s98, v11, 38
	v_fmac_f32_e32 v65, s100, v55
	v_readlane_b32 s99, v11, 39
	v_fmac_f32_e32 v66, s0, v53
	v_readlane_b32 s100, v11, 40
	v_fmac_f32_e32 v65, s98, v50
	v_readlane_b32 s0, v11, 41
	v_fmac_f32_e32 v66, s99, v48
	v_readlane_b32 s98, v11, 42
	v_fmac_f32_e32 v65, s100, v44
	v_readlane_b32 s99, v11, 43
	v_fmac_f32_e32 v66, s0, v41
	v_readlane_b32 s100, v11, 44
	v_fmac_f32_e32 v65, s98, v37
	v_readlane_b32 s0, v11, 45
	v_fmac_f32_e32 v66, s99, v30
	v_readlane_b32 s98, v11, 46
	v_fmac_f32_e32 v65, s100, v21
	v_readlane_b32 s99, v11, 47
; __device__ __forceinline__ void ph_gdn_prep(const Params& p, LAS unsigned char* lds) {
;     ...
;             for (int i = 1; i < 64; ++i) { const int mi = __float_as_int(mcol[i]); float a0 = mcol[i], a1 = 0.f;
; #pragma unroll
;                 for (int j = 0; j < i; ++j) { const float s = __int_as_float(__builtin_amdgcn_readlane(mi, j)); if (j & 1) a1 += s * mcol[j]; else a0 += s * mcol[j]; }
;                 mcol[i] = a0 + a1; }
	v_fmac_f32_e32 v66, s0, v20
	v_readlane_b32 s100, v11, 48
	v_fmac_f32_e32 v65, s98, v19
	v_readlane_b32 s0, v11, 49
	v_fmac_f32_e32 v66, s99, v18
	v_readlane_b32 s98, v11, 50
	v_fmac_f32_e32 v65, s100, v17
	v_readlane_b32 s99, v11, 51
	v_fmac_f32_e32 v66, s0, v16
	v_readlane_b32 s100, v11, 52
	v_fmac_f32_e32 v65, s98, v15
	v_readlane_b32 s0, v10, 0
	v_fmac_f32_e32 v66, s99, v14
	v_readlane_b32 s98, v10, 1
	v_fmac_f32_e32 v65, s100, v12
	v_add_f32_e32 v11, v66, v65
	v_readlane_b32 s99, v10, 2
	v_fma_f32 v65, 0, s0, v10
	v_readlane_b32 s100, v10, 3
	v_fma_f32 v66, v27, s98, 0
	v_readlane_b32 s0, v10, 4
	v_fmac_f32_e32 v65, s99, v25
	v_readlane_b32 s98, v10, 5
	v_fmac_f32_e32 v66, s100, v23
	v_readlane_b32 s99, v10, 6
	v_fmac_f32_e32 v65, s0, v5
	v_readlane_b32 s100, v10, 7
	v_fmac_f32_e32 v66, s98, v22
	v_readlane_b32 s0, v10, 8
	v_fmac_f32_e32 v65, s99, v24
	v_readlane_b32 s98, v10, 9
	v_fmac_f32_e32 v66, s100, v26
	v_readlane_b32 s99, v10, 10
	v_fmac_f32_e32 v65, s0, v28
	v_readlane_b32 s100, v10, 11
	v_fmac_f32_e32 v66, s98, v31
	v_readlane_b32 s0, v10, 12
	v_fmac_f32_e32 v65, s99, v32
	v_readlane_b32 s98, v10, 13
	v_fmac_f32_e32 v66, s100, v33
	v_readlane_b32 s99, v10, 14
	v_fmac_f32_e32 v65, s0, v34
	v_readlane_b32 s100, v10, 15
	v_fmac_f32_e32 v66, s98, v35
	v_readlane_b32 s0, v10, 16
	v_fmac_f32_e32 v65, s99, v36
	v_readlane_b32 s98, v10, 17
	v_fmac_f32_e32 v66, s100, v38
	v_readlane_b32 s99, v10, 18
	v_fmac_f32_e32 v65, s0, v39
	v_readlane_b32 s100, v10, 19
	v_fmac_f32_e32 v66, s98, v40
	v_readlane_b32 s0, v10, 20
	v_fmac_f32_e32 v65, s99, v42
	v_readlane_b32 s98, v10, 21
	v_fmac_f32_e32 v66, s100, v43
	v_readlane_b32 s99, v10, 22
	v_fmac_f32_e32 v65, s0, v45
	v_readlane_b32 s100, v10, 23
	v_fmac_f32_e32 v66, s98, v46
	v_readlane_b32 s0, v10, 24
	v_fmac_f32_e32 v65, s99, v47
	v_readlane_b32 s98, v10, 25
	v_fmac_f32_e32 v66, s100, v49
	v_readlane_b32 s99, v10, 26
	v_fmac_f32_e32 v65, s0, v51
	v_readlane_b32 s100, v10, 27
	v_fmac_f32_e32 v66, s98, v52
	v_readlane_b32 s0, v10, 28
	v_fmac_f32_e32 v65, s99, v54
	v_readlane_b32 s98, v10, 29
	v_fmac_f32_e32 v66, s100, v56
	v_readlane_b32 s99, v10, 30
	v_fmac_f32_e32 v65, s0, v57
	v_readlane_b32 s100, v10, 31
	v_fmac_f32_e32 v66, s98, v59
	v_readlane_b32 s0, v10, 32
	v_fmac_f32_e32 v65, s99, v61
	v_readlane_b32 s98, v10, 33
	v_fmac_f32_e32 v66, s100, v63
	v_readlane_b32 s99, v10, 34
	v_fmac_f32_e32 v65, s0, v64
	v_readlane_b32 s100, v10, 35
	v_fmac_f32_e32 v66, s98, v62
	v_readlane_b32 s0, v10, 36
	v_fmac_f32_e32 v65, s99, v60
	v_readlane_b32 s98, v10, 37
	v_fmac_f32_e32 v66, s100, v58
	v_readlane_b32 s99, v10, 38
	v_fmac_f32_e32 v65, s0, v55
	v_readlane_b32 s100, v10, 39
	v_fmac_f32_e32 v66, s98, v53
	v_readlane_b32 s0, v10, 40
	v_fmac_f32_e32 v65, s99, v50
	v_readlane_b32 s98, v10, 41
	v_fmac_f32_e32 v66, s100, v48
	v_readlane_b32 s99, v10, 42
	v_fmac_f32_e32 v65, s0, v44
	v_readlane_b32 s100, v10, 43
	v_fmac_f32_e32 v66, s98, v41
	v_readlane_b32 s0, v10, 44
	v_fmac_f32_e32 v65, s99, v37
	v_readlane_b32 s98, v10, 45
	v_fmac_f32_e32 v66, s100, v30
	v_readlane_b32 s99, v10, 46
	v_fmac_f32_e32 v65, s0, v21
	v_readlane_b32 s100, v10, 47
	v_fmac_f32_e32 v66, s98, v20
	v_readlane_b32 s0, v10, 48
	v_fmac_f32_e32 v65, s99, v19
	v_readlane_b32 s98, v10, 49
	v_fmac_f32_e32 v66, s100, v18
	v_readlane_b32 s99, v10, 50
	v_fmac_f32_e32 v65, s0, v17
	v_readlane_b32 s100, v10, 51
	v_fmac_f32_e32 v66, s98, v16
	v_readlane_b32 s0, v10, 52
	v_fmac_f32_e32 v65, s99, v15
	v_readlane_b32 s98, v10, 53
	v_fmac_f32_e32 v66, s100, v14
	v_readlane_b32 s99, v9, 0
	v_fmac_f32_e32 v65, s0, v12
	v_readlane_b32 s100, v9, 1
	v_fmac_f32_e32 v66, s98, v11
	v_add_f32_e32 v10, v65, v66
	v_readlane_b32 s0, v9, 2
	v_fma_f32 v65, 0, s99, v9
	v_readlane_b32 s98, v9, 3
	v_fma_f32 v66, v27, s100, 0
	v_readlane_b32 s99, v9, 4
	v_fmac_f32_e32 v65, s0, v25
	v_readlane_b32 s100, v9, 5
	v_fmac_f32_e32 v66, s98, v23
	v_readlane_b32 s0, v9, 6
	v_fmac_f32_e32 v65, s99, v5
	v_readlane_b32 s98, v9, 7
	v_fmac_f32_e32 v66, s100, v22
	v_readlane_b32 s99, v9, 8
	v_fmac_f32_e32 v65, s0, v24
	v_readlane_b32 s100, v9, 9
	v_fmac_f32_e32 v66, s98, v26
	v_readlane_b32 s0, v9, 10
	v_fmac_f32_e32 v65, s99, v28
	v_readlane_b32 s98, v9, 11
	v_fmac_f32_e32 v66, s100, v31
	v_readlane_b32 s99, v9, 12
	v_fmac_f32_e32 v65, s0, v32
	v_readlane_b32 s100, v9, 13
	v_fmac_f32_e32 v66, s98, v33
	v_readlane_b32 s0, v9, 14
	v_fmac_f32_e32 v65, s99, v34
	v_readlane_b32 s98, v9, 15
	v_fmac_f32_e32 v66, s100, v35
	v_readlane_b32 s99, v9, 16
	v_fmac_f32_e32 v65, s0, v36
	v_readlane_b32 s100, v9, 17
	v_fmac_f32_e32 v66, s98, v38
	v_readlane_b32 s0, v9, 18
	v_fmac_f32_e32 v65, s99, v39
	v_readlane_b32 s98, v9, 19
	v_fmac_f32_e32 v66, s100, v40
	v_readlane_b32 s99, v9, 20
	v_fmac_f32_e32 v65, s0, v42
	v_readlane_b32 s100, v9, 21
	v_fmac_f32_e32 v66, s98, v43
	v_readlane_b32 s0, v9, 22
	v_fmac_f32_e32 v65, s99, v45
	v_readlane_b32 s98, v9, 23
	v_fmac_f32_e32 v66, s100, v46
	v_readlane_b32 s99, v9, 24
	v_fmac_f32_e32 v65, s0, v47
	v_readlane_b32 s100, v9, 25
	v_fmac_f32_e32 v66, s98, v49
	v_readlane_b32 s0, v9, 26
	v_fmac_f32_e32 v65, s99, v51
	v_readlane_b32 s98, v9, 27
	v_fmac_f32_e32 v66, s100, v52
	v_readlane_b32 s99, v9, 28
	v_fmac_f32_e32 v65, s0, v54
	v_readlane_b32 s100, v9, 29
	v_fmac_f32_e32 v66, s98, v56
	v_readlane_b32 s0, v9, 30
	v_fmac_f32_e32 v65, s99, v57
	v_readlane_b32 s98, v9, 31
	v_fmac_f32_e32 v66, s100, v59
	v_readlane_b32 s99, v9, 32
	v_fmac_f32_e32 v65, s0, v61
	v_readlane_b32 s100, v9, 33
	v_fmac_f32_e32 v66, s98, v63
	v_readlane_b32 s0, v9, 34
	v_fmac_f32_e32 v65, s99, v64
	v_readlane_b32 s98, v9, 35
	v_fmac_f32_e32 v66, s100, v62
; __device__ __forceinline__ void ph_gdn_prep(const Params& p, LAS unsigned char* lds) {
;     ...
;             for (int i = 1; i < 64; ++i) { const int mi = __float_as_int(mcol[i]); float a0 = mcol[i], a1 = 0.f;
; #pragma unroll
;                 for (int j = 0; j < i; ++j) { const float s = __int_as_float(__builtin_amdgcn_readlane(mi, j)); if (j & 1) a1 += s * mcol[j]; else a0 += s * mcol[j]; }
;                 mcol[i] = a0 + a1; }
	v_readlane_b32 s99, v9, 36
	v_fmac_f32_e32 v65, s0, v60
	v_readlane_b32 s100, v9, 37
	v_fmac_f32_e32 v66, s98, v58
	v_readlane_b32 s0, v9, 38
	v_fmac_f32_e32 v65, s99, v55
	v_readlane_b32 s98, v9, 39
	v_fmac_f32_e32 v66, s100, v53
	v_readlane_b32 s99, v9, 40
	v_fmac_f32_e32 v65, s0, v50
	v_readlane_b32 s100, v9, 41
	v_fmac_f32_e32 v66, s98, v48
	v_readlane_b32 s0, v9, 42
	v_fmac_f32_e32 v65, s99, v44
	v_readlane_b32 s98, v9, 43
	v_fmac_f32_e32 v66, s100, v41
	v_readlane_b32 s99, v9, 44
	v_fmac_f32_e32 v65, s0, v37
	v_readlane_b32 s100, v9, 45
	v_fmac_f32_e32 v66, s98, v30
	v_readlane_b32 s0, v9, 46
	v_fmac_f32_e32 v65, s99, v21
	v_readlane_b32 s98, v9, 47
	v_fmac_f32_e32 v66, s100, v20
	v_readlane_b32 s99, v9, 48
	v_fmac_f32_e32 v65, s0, v19
	v_readlane_b32 s100, v9, 49
	v_fmac_f32_e32 v66, s98, v18
	v_readlane_b32 s0, v9, 50
	v_fmac_f32_e32 v65, s99, v17
	v_readlane_b32 s98, v9, 51
	v_fmac_f32_e32 v66, s100, v16
	v_readlane_b32 s99, v9, 52
	v_fmac_f32_e32 v65, s0, v15
	v_readlane_b32 s100, v9, 53
	v_fmac_f32_e32 v66, s98, v14
	v_readlane_b32 s0, v9, 54
	v_fmac_f32_e32 v65, s99, v12
	v_readlane_b32 s98, v8, 0
	v_fmac_f32_e32 v66, s100, v11
	v_readlane_b32 s99, v8, 1
	v_fmac_f32_e32 v65, s0, v10
	v_add_f32_e32 v9, v66, v65
	v_readlane_b32 s100, v8, 2
	v_fma_f32 v65, 0, s98, v8
	v_readlane_b32 s0, v8, 3
	v_fma_f32 v66, v27, s99, 0
	v_readlane_b32 s98, v8, 4
	v_fmac_f32_e32 v65, s100, v25
	v_readlane_b32 s99, v8, 5
	v_fmac_f32_e32 v66, s0, v23
	v_readlane_b32 s100, v8, 6
	v_fmac_f32_e32 v65, s98, v5
	v_readlane_b32 s0, v8, 7
	v_fmac_f32_e32 v66, s99, v22
	v_readlane_b32 s98, v8, 8
	v_fmac_f32_e32 v65, s100, v24
	v_readlane_b32 s99, v8, 9
	v_fmac_f32_e32 v66, s0, v26
	v_readlane_b32 s100, v8, 10
	v_fmac_f32_e32 v65, s98, v28
	v_readlane_b32 s0, v8, 11
	v_fmac_f32_e32 v66, s99, v31
	v_readlane_b32 s98, v8, 12
	v_fmac_f32_e32 v65, s100, v32
	v_readlane_b32 s99, v8, 13
	v_fmac_f32_e32 v66, s0, v33
	v_readlane_b32 s100, v8, 14
	v_fmac_f32_e32 v65, s98, v34
	v_readlane_b32 s0, v8, 15
	v_fmac_f32_e32 v66, s99, v35
	v_readlane_b32 s98, v8, 16
	v_fmac_f32_e32 v65, s100, v36
	v_readlane_b32 s99, v8, 17
	v_fmac_f32_e32 v66, s0, v38
	v_readlane_b32 s100, v8, 18
	v_fmac_f32_e32 v65, s98, v39
	v_readlane_b32 s0, v8, 19
	v_fmac_f32_e32 v66, s99, v40
	v_readlane_b32 s98, v8, 20
	v_fmac_f32_e32 v65, s100, v42
	v_readlane_b32 s99, v8, 21
	v_fmac_f32_e32 v66, s0, v43
	v_readlane_b32 s100, v8, 22
	v_fmac_f32_e32 v65, s98, v45
	v_readlane_b32 s0, v8, 23
	v_fmac_f32_e32 v66, s99, v46
	v_readlane_b32 s98, v8, 24
	v_fmac_f32_e32 v65, s100, v47
	v_readlane_b32 s99, v8, 25
	v_fmac_f32_e32 v66, s0, v49
	v_readlane_b32 s100, v8, 26
	v_fmac_f32_e32 v65, s98, v51
	v_readlane_b32 s0, v8, 27
	v_fmac_f32_e32 v66, s99, v52
	v_readlane_b32 s98, v8, 28
	v_fmac_f32_e32 v65, s100, v54
	v_readlane_b32 s99, v8, 29
	v_fmac_f32_e32 v66, s0, v56
	v_readlane_b32 s100, v8, 30
	v_fmac_f32_e32 v65, s98, v57
	v_readlane_b32 s0, v8, 31
	v_fmac_f32_e32 v66, s99, v59
	v_readlane_b32 s98, v8, 32
	v_fmac_f32_e32 v65, s100, v61
	v_readlane_b32 s99, v8, 33
	v_fmac_f32_e32 v66, s0, v63
	v_readlane_b32 s100, v8, 34
	v_fmac_f32_e32 v65, s98, v64
	v_readlane_b32 s0, v8, 35
	v_fmac_f32_e32 v66, s99, v62
	v_readlane_b32 s98, v8, 36
	v_fmac_f32_e32 v65, s100, v60
	v_readlane_b32 s99, v8, 37
	v_fmac_f32_e32 v66, s0, v58
	v_readlane_b32 s100, v8, 38
	v_fmac_f32_e32 v65, s98, v55
	v_readlane_b32 s0, v8, 39
	v_fmac_f32_e32 v66, s99, v53
	v_readlane_b32 s98, v8, 40
	v_fmac_f32_e32 v65, s100, v50
	v_readlane_b32 s99, v8, 41
	v_fmac_f32_e32 v66, s0, v48
	v_readlane_b32 s100, v8, 42
	v_fmac_f32_e32 v65, s98, v44
	v_readlane_b32 s0, v8, 43
	v_fmac_f32_e32 v66, s99, v41
	v_readlane_b32 s98, v8, 44
	v_fmac_f32_e32 v65, s100, v37
	v_readlane_b32 s99, v8, 45
	v_fmac_f32_e32 v66, s0, v30
	v_readlane_b32 s100, v8, 46
	v_fmac_f32_e32 v65, s98, v21
	v_readlane_b32 s0, v8, 47
	v_fmac_f32_e32 v66, s99, v20
	v_readlane_b32 s98, v8, 48
	v_fmac_f32_e32 v65, s100, v19
	v_readlane_b32 s99, v8, 49
	v_fmac_f32_e32 v66, s0, v18
	v_readlane_b32 s100, v8, 50
	v_fmac_f32_e32 v65, s98, v17
	v_readlane_b32 s0, v8, 51
	v_fmac_f32_e32 v66, s99, v16
	v_readlane_b32 s98, v8, 52
	v_fmac_f32_e32 v65, s100, v15
	v_readlane_b32 s99, v8, 53
	v_fmac_f32_e32 v66, s0, v14
	v_readlane_b32 s100, v8, 54
	v_fmac_f32_e32 v65, s98, v12
	v_readlane_b32 s0, v8, 55
	v_fmac_f32_e32 v66, s99, v11
	v_readlane_b32 s98, v7, 0
	v_fmac_f32_e32 v65, s100, v10
	v_readlane_b32 s99, v7, 1
	v_fmac_f32_e32 v66, s0, v9
	v_add_f32_e32 v8, v65, v66
	v_readlane_b32 s100, v7, 2
	v_fma_f32 v65, 0, s98, v7
	v_readlane_b32 s0, v7, 3
	v_fma_f32 v66, v27, s99, 0
	v_readlane_b32 s98, v7, 4
	v_fmac_f32_e32 v65, s100, v25
	v_readlane_b32 s99, v7, 5
	v_fmac_f32_e32 v66, s0, v23
	v_readlane_b32 s100, v7, 6
	v_fmac_f32_e32 v65, s98, v5
	v_readlane_b32 s0, v7, 7
	v_fmac_f32_e32 v66, s99, v22
	v_readlane_b32 s98, v7, 8
	v_fmac_f32_e32 v65, s100, v24
	v_readlane_b32 s99, v7, 9
	v_fmac_f32_e32 v66, s0, v26
	v_readlane_b32 s100, v7, 10
	v_fmac_f32_e32 v65, s98, v28
	v_readlane_b32 s0, v7, 11
	v_fmac_f32_e32 v66, s99, v31
	v_readlane_b32 s98, v7, 12
	v_fmac_f32_e32 v65, s100, v32
	v_readlane_b32 s99, v7, 13
	v_fmac_f32_e32 v66, s0, v33
	v_readlane_b32 s100, v7, 14
	v_fmac_f32_e32 v65, s98, v34
	v_readlane_b32 s0, v7, 15
	v_fmac_f32_e32 v66, s99, v35
	v_readlane_b32 s98, v7, 16
	v_fmac_f32_e32 v65, s100, v36
	v_readlane_b32 s99, v7, 17
	v_fmac_f32_e32 v66, s0, v38
	v_readlane_b32 s100, v7, 18
	v_fmac_f32_e32 v65, s98, v39
	v_readlane_b32 s0, v7, 19
	v_fmac_f32_e32 v66, s99, v40
	v_readlane_b32 s98, v7, 20
	v_fmac_f32_e32 v65, s100, v42
	v_readlane_b32 s99, v7, 21
	v_fmac_f32_e32 v66, s0, v43
; __device__ __forceinline__ void ph_gdn_prep(const Params& p, LAS unsigned char* lds) {
;     ...
;             for (int i = 1; i < 64; ++i) { const int mi = __float_as_int(mcol[i]); float a0 = mcol[i], a1 = 0.f;
; #pragma unroll
;                 for (int j = 0; j < i; ++j) { const float s = __int_as_float(__builtin_amdgcn_readlane(mi, j)); if (j & 1) a1 += s * mcol[j]; else a0 += s * mcol[j]; }
;                 mcol[i] = a0 + a1; }
	v_readlane_b32 s100, v7, 22
	v_fmac_f32_e32 v65, s98, v45
	v_readlane_b32 s0, v7, 23
	v_fmac_f32_e32 v66, s99, v46
	v_readlane_b32 s98, v7, 24
	v_fmac_f32_e32 v65, s100, v47
	v_readlane_b32 s99, v7, 25
	v_fmac_f32_e32 v66, s0, v49
	v_readlane_b32 s100, v7, 26
	v_fmac_f32_e32 v65, s98, v51
	v_readlane_b32 s0, v7, 27
	v_fmac_f32_e32 v66, s99, v52
	v_readlane_b32 s98, v7, 28
	v_fmac_f32_e32 v65, s100, v54
	v_readlane_b32 s99, v7, 29
	v_fmac_f32_e32 v66, s0, v56
	v_readlane_b32 s100, v7, 30
	v_fmac_f32_e32 v65, s98, v57
	v_readlane_b32 s0, v7, 31
	v_fmac_f32_e32 v66, s99, v59
	v_readlane_b32 s98, v7, 32
	v_fmac_f32_e32 v65, s100, v61
	v_readlane_b32 s99, v7, 33
	v_fmac_f32_e32 v66, s0, v63
	v_readlane_b32 s100, v7, 34
	v_fmac_f32_e32 v65, s98, v64
	v_readlane_b32 s0, v7, 35
	v_fmac_f32_e32 v66, s99, v62
	v_readlane_b32 s98, v7, 36
	v_fmac_f32_e32 v65, s100, v60
	v_readlane_b32 s99, v7, 37
	v_fmac_f32_e32 v66, s0, v58
	v_readlane_b32 s100, v7, 38
	v_fmac_f32_e32 v65, s98, v55
	v_readlane_b32 s0, v7, 39
	v_fmac_f32_e32 v66, s99, v53
	v_readlane_b32 s98, v7, 40
	v_fmac_f32_e32 v65, s100, v50
	v_readlane_b32 s99, v7, 41
	v_fmac_f32_e32 v66, s0, v48
	v_readlane_b32 s100, v7, 42
	v_fmac_f32_e32 v65, s98, v44
	v_readlane_b32 s0, v7, 43
	v_fmac_f32_e32 v66, s99, v41
	v_readlane_b32 s98, v7, 44
	v_fmac_f32_e32 v65, s100, v37
	v_readlane_b32 s99, v7, 45
	v_fmac_f32_e32 v66, s0, v30
	v_readlane_b32 s100, v7, 46
	v_fmac_f32_e32 v65, s98, v21
	v_readlane_b32 s0, v7, 47
	v_fmac_f32_e32 v66, s99, v20
	v_readlane_b32 s98, v7, 48
	v_fmac_f32_e32 v65, s100, v19
	v_readlane_b32 s99, v7, 49
	v_fmac_f32_e32 v66, s0, v18
	v_readlane_b32 s100, v7, 50
	v_fmac_f32_e32 v65, s98, v17
	v_readlane_b32 s0, v7, 51
	v_fmac_f32_e32 v66, s99, v16
	v_readlane_b32 s98, v7, 52
	v_fmac_f32_e32 v65, s100, v15
	v_readlane_b32 s99, v7, 53
	v_fmac_f32_e32 v66, s0, v14
	v_readlane_b32 s100, v7, 54
	v_fmac_f32_e32 v65, s98, v12
	v_readlane_b32 s0, v7, 55
	v_fmac_f32_e32 v66, s99, v11
	v_readlane_b32 s98, v7, 56
	v_fmac_f32_e32 v65, s100, v10
	v_readlane_b32 s99, v6, 0
	v_fmac_f32_e32 v66, s0, v9
	v_readlane_b32 s100, v6, 1
	v_fmac_f32_e32 v65, s98, v8
	v_add_f32_e32 v7, v66, v65
	v_readlane_b32 s0, v6, 2
	v_fma_f32 v65, 0, s99, v6
	v_readlane_b32 s98, v6, 3
	v_fma_f32 v66, v27, s100, 0
	v_readlane_b32 s99, v6, 4
	v_fmac_f32_e32 v65, s0, v25
	v_readlane_b32 s100, v6, 5
	v_fmac_f32_e32 v66, s98, v23
	v_readlane_b32 s0, v6, 6
	v_fmac_f32_e32 v65, s99, v5
	v_readlane_b32 s98, v6, 7
	v_fmac_f32_e32 v66, s100, v22
	v_readlane_b32 s99, v6, 8
	v_fmac_f32_e32 v65, s0, v24
	v_readlane_b32 s100, v6, 9
	v_fmac_f32_e32 v66, s98, v26
	v_readlane_b32 s0, v6, 10
	v_fmac_f32_e32 v65, s99, v28
	v_readlane_b32 s98, v6, 11
	v_fmac_f32_e32 v66, s100, v31
	v_readlane_b32 s99, v6, 12
	v_fmac_f32_e32 v65, s0, v32
	v_readlane_b32 s100, v6, 13
	v_fmac_f32_e32 v66, s98, v33
	v_readlane_b32 s0, v6, 14
	v_fmac_f32_e32 v65, s99, v34
	v_readlane_b32 s98, v6, 15
	v_fmac_f32_e32 v66, s100, v35
	v_readlane_b32 s99, v6, 16
	v_fmac_f32_e32 v65, s0, v36
	v_readlane_b32 s100, v6, 17
	v_fmac_f32_e32 v66, s98, v38
	v_readlane_b32 s0, v6, 18
	v_fmac_f32_e32 v65, s99, v39
	v_readlane_b32 s98, v6, 19
	v_fmac_f32_e32 v66, s100, v40
	v_readlane_b32 s99, v6, 20
	v_fmac_f32_e32 v65, s0, v42
	v_readlane_b32 s100, v6, 21
	v_fmac_f32_e32 v66, s98, v43
	v_readlane_b32 s0, v6, 22
	v_fmac_f32_e32 v65, s99, v45
	v_readlane_b32 s98, v6, 23
	v_fmac_f32_e32 v66, s100, v46
	v_readlane_b32 s99, v6, 24
	v_fmac_f32_e32 v65, s0, v47
	v_readlane_b32 s100, v6, 25
	v_fmac_f32_e32 v66, s98, v49
	v_readlane_b32 s0, v6, 26
	v_fmac_f32_e32 v65, s99, v51
	v_readlane_b32 s98, v6, 27
	v_fmac_f32_e32 v66, s100, v52
	v_readlane_b32 s99, v6, 28
	v_fmac_f32_e32 v65, s0, v54
	v_readlane_b32 s100, v6, 29
	v_fmac_f32_e32 v66, s98, v56
	v_readlane_b32 s0, v6, 30
	v_fmac_f32_e32 v65, s99, v57
	v_readlane_b32 s98, v6, 31
	v_fmac_f32_e32 v66, s100, v59
	v_readlane_b32 s99, v6, 32
	v_fmac_f32_e32 v65, s0, v61
	v_readlane_b32 s100, v6, 33
	v_fmac_f32_e32 v66, s98, v63
	v_readlane_b32 s0, v6, 34
	v_fmac_f32_e32 v65, s99, v64
	v_readlane_b32 s98, v6, 35
	v_fmac_f32_e32 v66, s100, v62
	v_readlane_b32 s99, v6, 36
	v_fmac_f32_e32 v65, s0, v60
	v_readlane_b32 s100, v6, 37
	v_fmac_f32_e32 v66, s98, v58
	v_readlane_b32 s0, v6, 38
	v_fmac_f32_e32 v65, s99, v55
	v_readlane_b32 s98, v6, 39
	v_fmac_f32_e32 v66, s100, v53
	v_readlane_b32 s99, v6, 40
	v_fmac_f32_e32 v65, s0, v50
	v_readlane_b32 s100, v6, 41
	v_fmac_f32_e32 v66, s98, v48
	v_readlane_b32 s0, v6, 42
	v_fmac_f32_e32 v65, s99, v44
	v_readlane_b32 s98, v6, 43
	v_fmac_f32_e32 v66, s100, v41
	v_readlane_b32 s99, v6, 44
	v_fmac_f32_e32 v65, s0, v37
	v_readlane_b32 s100, v6, 45
	v_fmac_f32_e32 v66, s98, v30
	v_readlane_b32 s0, v6, 46
	v_fmac_f32_e32 v65, s99, v21
	v_readlane_b32 s98, v6, 47
	v_fmac_f32_e32 v66, s100, v20
	v_readlane_b32 s99, v6, 48
	v_fmac_f32_e32 v65, s0, v19
	v_readlane_b32 s100, v6, 49
	v_fmac_f32_e32 v66, s98, v18
	v_readlane_b32 s0, v6, 50
	v_fmac_f32_e32 v65, s99, v17
	v_readlane_b32 s98, v6, 51
	v_fmac_f32_e32 v66, s100, v16
	v_readlane_b32 s99, v6, 52
	v_fmac_f32_e32 v65, s0, v15
	v_readlane_b32 s100, v6, 53
	v_fmac_f32_e32 v66, s98, v14
	v_readlane_b32 s0, v6, 54
	v_fmac_f32_e32 v65, s99, v12
	v_readlane_b32 s98, v6, 55
	v_fmac_f32_e32 v66, s100, v11
	v_readlane_b32 s99, v6, 56
	v_fmac_f32_e32 v65, s0, v10
	v_readlane_b32 s100, v6, 57
	v_fmac_f32_e32 v66, s98, v9
	v_readlane_b32 s0, v13, 0
	v_fmac_f32_e32 v65, s99, v8
	v_readlane_b32 s98, v13, 1
	v_fmac_f32_e32 v66, s100, v7
	v_add_f32_e32 v6, v65, v66
	v_readlane_b32 s99, v13, 2
	v_fma_f32 v65, 0, s0, v13
	v_readlane_b32 s100, v13, 3
; __device__ __forceinline__ void ph_gdn_prep(const Params& p, LAS unsigned char* lds) {
;     ...
;             for (int i = 1; i < 64; ++i) { const int mi = __float_as_int(mcol[i]); float a0 = mcol[i], a1 = 0.f;
; #pragma unroll
;                 for (int j = 0; j < i; ++j) { const float s = __int_as_float(__builtin_amdgcn_readlane(mi, j)); if (j & 1) a1 += s * mcol[j]; else a0 += s * mcol[j]; }
;                 mcol[i] = a0 + a1; }
	v_fma_f32 v66, v27, s98, 0
	v_readlane_b32 s0, v13, 4
	v_fmac_f32_e32 v65, s99, v25
	v_readlane_b32 s98, v13, 5
	v_fmac_f32_e32 v66, s100, v23
	v_readlane_b32 s99, v13, 6
	v_fmac_f32_e32 v65, s0, v5
	v_readlane_b32 s100, v13, 7
	v_fmac_f32_e32 v66, s98, v22
	v_readlane_b32 s0, v13, 8
	v_fmac_f32_e32 v65, s99, v24
	v_readlane_b32 s98, v13, 9
	v_fmac_f32_e32 v66, s100, v26
	v_readlane_b32 s99, v13, 10
	v_fmac_f32_e32 v65, s0, v28
	v_readlane_b32 s100, v13, 11
	v_fmac_f32_e32 v66, s98, v31
	v_readlane_b32 s0, v13, 12
	v_fmac_f32_e32 v65, s99, v32
	v_readlane_b32 s98, v13, 13
	v_fmac_f32_e32 v66, s100, v33
	v_readlane_b32 s99, v13, 14
	v_fmac_f32_e32 v65, s0, v34
	v_readlane_b32 s100, v13, 15
	v_fmac_f32_e32 v66, s98, v35
	v_readlane_b32 s0, v13, 16
	v_fmac_f32_e32 v65, s99, v36
	v_readlane_b32 s98, v13, 17
	v_fmac_f32_e32 v66, s100, v38
	v_readlane_b32 s99, v13, 18
	v_fmac_f32_e32 v65, s0, v39
	v_readlane_b32 s100, v13, 19
	v_fmac_f32_e32 v66, s98, v40
	v_readlane_b32 s0, v13, 20
	v_fmac_f32_e32 v65, s99, v42
	v_readlane_b32 s98, v13, 21
	v_fmac_f32_e32 v66, s100, v43
	v_readlane_b32 s99, v13, 22
	v_fmac_f32_e32 v65, s0, v45
	v_readlane_b32 s100, v13, 23
	v_fmac_f32_e32 v66, s98, v46
	v_readlane_b32 s0, v13, 24
	v_fmac_f32_e32 v65, s99, v47
	v_readlane_b32 s98, v13, 25
	v_fmac_f32_e32 v66, s100, v49
	v_readlane_b32 s99, v13, 26
	v_fmac_f32_e32 v65, s0, v51
	v_readlane_b32 s100, v13, 27
	v_fmac_f32_e32 v66, s98, v52
	v_readlane_b32 s0, v13, 28
	v_fmac_f32_e32 v65, s99, v54
	v_readlane_b32 s98, v13, 29
	v_fmac_f32_e32 v66, s100, v56
	v_readlane_b32 s99, v13, 30
	v_fmac_f32_e32 v65, s0, v57
	v_readlane_b32 s100, v13, 31
	v_fmac_f32_e32 v66, s98, v59
	v_readlane_b32 s0, v13, 32
	v_fmac_f32_e32 v65, s99, v61
	v_readlane_b32 s98, v13, 33
	v_fmac_f32_e32 v66, s100, v63
	v_readlane_b32 s99, v13, 34
	v_fmac_f32_e32 v65, s0, v64
	v_readlane_b32 s100, v13, 35
	v_fmac_f32_e32 v66, s98, v62
	v_readlane_b32 s0, v13, 36
	v_fmac_f32_e32 v65, s99, v60
	v_readlane_b32 s98, v13, 37
	v_fmac_f32_e32 v66, s100, v58
	v_readlane_b32 s99, v13, 38
	v_fmac_f32_e32 v65, s0, v55
	v_readlane_b32 s100, v13, 39
	v_fmac_f32_e32 v66, s98, v53
	v_readlane_b32 s0, v13, 40
	v_fmac_f32_e32 v65, s99, v50
	v_readlane_b32 s98, v13, 41
	v_fmac_f32_e32 v66, s100, v48
	v_readlane_b32 s99, v13, 42
	v_fmac_f32_e32 v65, s0, v44
	v_readlane_b32 s100, v13, 43
	v_fmac_f32_e32 v66, s98, v41
	v_readlane_b32 s0, v13, 44
	v_fmac_f32_e32 v65, s99, v37
	v_readlane_b32 s98, v13, 45
	v_fmac_f32_e32 v66, s100, v30
	v_readlane_b32 s99, v13, 46
	v_fmac_f32_e32 v65, s0, v21
	v_readlane_b32 s100, v13, 47
	v_fmac_f32_e32 v66, s98, v20
	v_readlane_b32 s0, v13, 48
	v_fmac_f32_e32 v65, s99, v19
	v_readlane_b32 s98, v13, 49
	v_fmac_f32_e32 v66, s100, v18
	v_readlane_b32 s99, v13, 50
	v_fmac_f32_e32 v65, s0, v17
	v_readlane_b32 s100, v13, 51
	v_fmac_f32_e32 v66, s98, v16
	v_readlane_b32 s0, v13, 52
	v_fmac_f32_e32 v65, s99, v15
	v_readlane_b32 s98, v13, 53
	v_fmac_f32_e32 v66, s100, v14
	v_readlane_b32 s99, v13, 54
	v_fmac_f32_e32 v65, s0, v12
	v_readlane_b32 s100, v13, 55
	v_fmac_f32_e32 v66, s98, v11
	v_readlane_b32 s0, v13, 56
	v_fmac_f32_e32 v65, s99, v10
	v_readlane_b32 s98, v13, 57
	v_fmac_f32_e32 v66, s100, v9
	v_readlane_b32 s99, v13, 58
	v_fmac_f32_e32 v65, s0, v8
	v_readlane_b32 s100, v4, 0
	v_fmac_f32_e32 v66, s98, v7
	v_readlane_b32 s0, v4, 1
	v_fmac_f32_e32 v65, s99, v6
	v_add_f32_e32 v13, v66, v65
	v_readlane_b32 s98, v4, 2
	v_fma_f32 v65, 0, s100, v4
	v_readlane_b32 s99, v4, 3
	v_fma_f32 v66, v27, s0, 0
	v_readlane_b32 s100, v4, 4
	v_fmac_f32_e32 v65, s98, v25
	v_readlane_b32 s0, v4, 5
	v_fmac_f32_e32 v66, s99, v23
	v_readlane_b32 s98, v4, 6
	v_fmac_f32_e32 v65, s100, v5
	v_readlane_b32 s99, v4, 7
	v_fmac_f32_e32 v66, s0, v22
	v_readlane_b32 s100, v4, 8
	v_fmac_f32_e32 v65, s98, v24
	v_readlane_b32 s0, v4, 9
	v_fmac_f32_e32 v66, s99, v26
	v_readlane_b32 s98, v4, 10
	v_fmac_f32_e32 v65, s100, v28
	v_readlane_b32 s99, v4, 11
	v_fmac_f32_e32 v66, s0, v31
	v_readlane_b32 s100, v4, 12
	v_fmac_f32_e32 v65, s98, v32
	v_readlane_b32 s0, v4, 13
	v_fmac_f32_e32 v66, s99, v33
	v_readlane_b32 s98, v4, 14
	v_fmac_f32_e32 v65, s100, v34
	v_readlane_b32 s99, v4, 15
	v_fmac_f32_e32 v66, s0, v35
	v_readlane_b32 s100, v4, 16
	v_fmac_f32_e32 v65, s98, v36
	v_readlane_b32 s0, v4, 17
	v_fmac_f32_e32 v66, s99, v38
	v_readlane_b32 s98, v4, 18
	v_fmac_f32_e32 v65, s100, v39
	v_readlane_b32 s99, v4, 19
	v_fmac_f32_e32 v66, s0, v40
	v_readlane_b32 s100, v4, 20
	v_fmac_f32_e32 v65, s98, v42
	v_readlane_b32 s0, v4, 21
	v_fmac_f32_e32 v66, s99, v43
	v_readlane_b32 s98, v4, 22
	v_fmac_f32_e32 v65, s100, v45
	v_readlane_b32 s99, v4, 23
	v_fmac_f32_e32 v66, s0, v46
	v_readlane_b32 s100, v4, 24
	v_fmac_f32_e32 v65, s98, v47
	v_readlane_b32 s0, v4, 25
	v_fmac_f32_e32 v66, s99, v49
	v_readlane_b32 s98, v4, 26
	v_fmac_f32_e32 v65, s100, v51
	v_readlane_b32 s99, v4, 27
	v_fmac_f32_e32 v66, s0, v52
	v_readlane_b32 s100, v4, 28
	v_fmac_f32_e32 v65, s98, v54
	v_readlane_b32 s0, v4, 29
	v_fmac_f32_e32 v66, s99, v56
	v_readlane_b32 s98, v4, 30
	v_fmac_f32_e32 v65, s100, v57
	v_readlane_b32 s99, v4, 31
	v_fmac_f32_e32 v66, s0, v59
	v_readlane_b32 s100, v4, 32
	v_fmac_f32_e32 v65, s98, v61
	v_readlane_b32 s0, v4, 33
	v_fmac_f32_e32 v66, s99, v63
	v_readlane_b32 s98, v4, 34
	v_fmac_f32_e32 v65, s100, v64
	v_readlane_b32 s99, v4, 35
	v_fmac_f32_e32 v66, s0, v62
	v_readlane_b32 s100, v4, 36
	v_fmac_f32_e32 v65, s98, v60
	v_readlane_b32 s0, v4, 37
	v_fmac_f32_e32 v66, s99, v58
	v_readlane_b32 s98, v4, 38
	v_fmac_f32_e32 v65, s100, v55
	v_readlane_b32 s99, v4, 39
	v_fmac_f32_e32 v66, s0, v53
	v_readlane_b32 s100, v4, 40
	v_fmac_f32_e32 v65, s98, v50
; __device__ __forceinline__ void ph_gdn_prep(const Params& p, LAS unsigned char* lds) {
;     ...
;             for (int i = 1; i < 64; ++i) { const int mi = __float_as_int(mcol[i]); float a0 = mcol[i], a1 = 0.f;
; #pragma unroll
;                 for (int j = 0; j < i; ++j) { const float s = __int_as_float(__builtin_amdgcn_readlane(mi, j)); if (j & 1) a1 += s * mcol[j]; else a0 += s * mcol[j]; }
;                 mcol[i] = a0 + a1; }
	v_readlane_b32 s0, v4, 41
	v_fmac_f32_e32 v66, s99, v48
	v_readlane_b32 s98, v4, 42
	v_fmac_f32_e32 v65, s100, v44
	v_readlane_b32 s99, v4, 43
	v_fmac_f32_e32 v66, s0, v41
	v_readlane_b32 s100, v4, 44
	v_fmac_f32_e32 v65, s98, v37
	v_readlane_b32 s0, v4, 45
	v_fmac_f32_e32 v66, s99, v30
	v_readlane_b32 s98, v4, 46
	v_fmac_f32_e32 v65, s100, v21
	v_readlane_b32 s99, v4, 47
	v_fmac_f32_e32 v66, s0, v20
	v_readlane_b32 s100, v4, 48
	v_fmac_f32_e32 v65, s98, v19
	v_readlane_b32 s0, v4, 49
	v_fmac_f32_e32 v66, s99, v18
	v_readlane_b32 s98, v4, 50
	v_fmac_f32_e32 v65, s100, v17
	v_readlane_b32 s99, v4, 51
	v_fmac_f32_e32 v66, s0, v16
	v_readlane_b32 s100, v4, 52
	v_fmac_f32_e32 v65, s98, v15
	v_readlane_b32 s0, v4, 53
	v_fmac_f32_e32 v66, s99, v14
	v_readlane_b32 s98, v4, 54
	v_fmac_f32_e32 v65, s100, v12
	v_readlane_b32 s99, v4, 55
	v_fmac_f32_e32 v66, s0, v11
	v_readlane_b32 s100, v4, 56
	v_fmac_f32_e32 v65, s98, v10
	v_readlane_b32 s0, v4, 57
	v_fmac_f32_e32 v66, s99, v9
	v_readlane_b32 s98, v4, 58
	v_fmac_f32_e32 v65, s100, v8
	v_readlane_b32 s99, v4, 59
	v_fmac_f32_e32 v66, s0, v7
	v_readlane_b32 s100, v3, 0
	v_fmac_f32_e32 v65, s98, v6
	v_readlane_b32 s0, v3, 1
	v_fmac_f32_e32 v66, s99, v13
	v_add_f32_e32 v4, v65, v66
	v_readlane_b32 s98, v3, 2
	v_fma_f32 v65, 0, s100, v3
	v_readlane_b32 s99, v3, 3
	v_fma_f32 v66, v27, s0, 0
	v_readlane_b32 s100, v3, 4
	v_fmac_f32_e32 v65, s98, v25
	v_readlane_b32 s0, v3, 5
	v_fmac_f32_e32 v66, s99, v23
	v_readlane_b32 s98, v3, 6
	v_fmac_f32_e32 v65, s100, v5
	v_readlane_b32 s99, v3, 7
	v_fmac_f32_e32 v66, s0, v22
	v_readlane_b32 s100, v3, 8
	v_fmac_f32_e32 v65, s98, v24
	v_readlane_b32 s0, v3, 9
	v_fmac_f32_e32 v66, s99, v26
	v_readlane_b32 s98, v3, 10
	v_fmac_f32_e32 v65, s100, v28
	v_readlane_b32 s99, v3, 11
	v_fmac_f32_e32 v66, s0, v31
	v_readlane_b32 s100, v3, 12
	v_fmac_f32_e32 v65, s98, v32
	v_readlane_b32 s0, v3, 13
	v_fmac_f32_e32 v66, s99, v33
	v_readlane_b32 s98, v3, 14
	v_fmac_f32_e32 v65, s100, v34
	v_readlane_b32 s99, v3, 15
	v_fmac_f32_e32 v66, s0, v35
	v_readlane_b32 s100, v3, 16
	v_fmac_f32_e32 v65, s98, v36
	v_readlane_b32 s0, v3, 17
	v_fmac_f32_e32 v66, s99, v38
	v_readlane_b32 s98, v3, 18
	v_fmac_f32_e32 v65, s100, v39
	v_readlane_b32 s99, v3, 19
	v_fmac_f32_e32 v66, s0, v40
	v_readlane_b32 s100, v3, 20
	v_fmac_f32_e32 v65, s98, v42
	v_readlane_b32 s0, v3, 21
	v_fmac_f32_e32 v66, s99, v43
	v_readlane_b32 s98, v3, 22
	v_fmac_f32_e32 v65, s100, v45
	v_readlane_b32 s99, v3, 23
	v_fmac_f32_e32 v66, s0, v46
	v_readlane_b32 s100, v3, 24
	v_fmac_f32_e32 v65, s98, v47
	v_readlane_b32 s0, v3, 25
	v_fmac_f32_e32 v66, s99, v49
	v_readlane_b32 s98, v3, 26
	v_fmac_f32_e32 v65, s100, v51
	v_readlane_b32 s99, v3, 27
	v_fmac_f32_e32 v66, s0, v52
	v_readlane_b32 s100, v3, 28
	v_fmac_f32_e32 v65, s98, v54
	v_readlane_b32 s0, v3, 29
	v_fmac_f32_e32 v66, s99, v56
	v_readlane_b32 s98, v3, 30
	v_fmac_f32_e32 v65, s100, v57
	v_readlane_b32 s99, v3, 31
	v_fmac_f32_e32 v66, s0, v59
	v_readlane_b32 s100, v3, 32
	v_fmac_f32_e32 v65, s98, v61
	v_readlane_b32 s0, v3, 33
	v_fmac_f32_e32 v66, s99, v63
	v_readlane_b32 s98, v3, 34
	v_fmac_f32_e32 v65, s100, v64
	v_readlane_b32 s99, v3, 35
	v_fmac_f32_e32 v66, s0, v62
	v_readlane_b32 s100, v3, 36
	v_fmac_f32_e32 v65, s98, v60
	v_readlane_b32 s0, v3, 37
	v_fmac_f32_e32 v66, s99, v58
	v_readlane_b32 s98, v3, 38
	v_fmac_f32_e32 v65, s100, v55
	v_readlane_b32 s99, v3, 39
	v_fmac_f32_e32 v66, s0, v53
	v_readlane_b32 s100, v3, 40
	v_fmac_f32_e32 v65, s98, v50
	v_readlane_b32 s0, v3, 41
	v_fmac_f32_e32 v66, s99, v48
	v_readlane_b32 s98, v3, 42
	v_fmac_f32_e32 v65, s100, v44
	v_readlane_b32 s99, v3, 43
	v_fmac_f32_e32 v66, s0, v41
	v_readlane_b32 s100, v3, 44
	v_fmac_f32_e32 v65, s98, v37
	v_readlane_b32 s0, v3, 45
	v_fmac_f32_e32 v66, s99, v30
	v_readlane_b32 s98, v3, 46
	v_fmac_f32_e32 v65, s100, v21
	v_readlane_b32 s99, v3, 47
	v_fmac_f32_e32 v66, s0, v20
	v_readlane_b32 s100, v3, 48
	v_fmac_f32_e32 v65, s98, v19
	v_readlane_b32 s0, v3, 49
	v_fmac_f32_e32 v66, s99, v18
	v_readlane_b32 s98, v3, 50
	v_fmac_f32_e32 v65, s100, v17
	v_readlane_b32 s99, v3, 51
	v_fmac_f32_e32 v66, s0, v16
	v_readlane_b32 s100, v3, 52
	v_fmac_f32_e32 v65, s98, v15
	v_readlane_b32 s0, v3, 53
	v_fmac_f32_e32 v66, s99, v14
	v_readlane_b32 s98, v3, 54
	v_fmac_f32_e32 v65, s100, v12
	v_readlane_b32 s99, v3, 55
	v_fmac_f32_e32 v66, s0, v11
	v_readlane_b32 s100, v3, 56
	v_fmac_f32_e32 v65, s98, v10
	v_readlane_b32 s0, v3, 57
	v_fmac_f32_e32 v66, s99, v9
	v_readlane_b32 s98, v3, 58
	v_fmac_f32_e32 v65, s100, v8
	v_readlane_b32 s99, v3, 59
	v_fmac_f32_e32 v66, s0, v7
	v_readlane_b32 s100, v3, 60
	v_fmac_f32_e32 v65, s98, v6
	v_readlane_b32 s0, v2, 0
	v_fmac_f32_e32 v66, s99, v13
	v_readlane_b32 s98, v2, 1
	v_fmac_f32_e32 v65, s100, v4
	v_add_f32_e32 v3, v66, v65
	v_readlane_b32 s99, v2, 2
	v_fma_f32 v65, 0, s0, v2
	v_readlane_b32 s100, v2, 3
	v_fma_f32 v66, v27, s98, 0
	v_readlane_b32 s0, v2, 4
	v_fmac_f32_e32 v65, s99, v25
	v_readlane_b32 s98, v2, 5
	v_fmac_f32_e32 v66, s100, v23
	v_readlane_b32 s99, v2, 6
	v_fmac_f32_e32 v65, s0, v5
	v_readlane_b32 s100, v2, 7
	v_fmac_f32_e32 v66, s98, v22
	v_readlane_b32 s0, v2, 8
	v_fmac_f32_e32 v65, s99, v24
	v_readlane_b32 s98, v2, 9
	v_fmac_f32_e32 v66, s100, v26
	v_readlane_b32 s99, v2, 10
	v_fmac_f32_e32 v65, s0, v28
	v_readlane_b32 s100, v2, 11
	v_fmac_f32_e32 v66, s98, v31
	v_readlane_b32 s0, v2, 12
	v_fmac_f32_e32 v65, s99, v32
	v_readlane_b32 s98, v2, 13
	v_fmac_f32_e32 v66, s100, v33
	v_readlane_b32 s99, v2, 14
	v_fmac_f32_e32 v65, s0, v34
	v_readlane_b32 s100, v2, 15
	v_fmac_f32_e32 v66, s98, v35
	v_readlane_b32 s0, v2, 16
	v_fmac_f32_e32 v65, s99, v36
; __device__ __forceinline__ void ph_gdn_prep(const Params& p, LAS unsigned char* lds) {
;     ...
;             for (int i = 1; i < 64; ++i) { const int mi = __float_as_int(mcol[i]); float a0 = mcol[i], a1 = 0.f;
; #pragma unroll
;                 for (int j = 0; j < i; ++j) { const float s = __int_as_float(__builtin_amdgcn_readlane(mi, j)); if (j & 1) a1 += s * mcol[j]; else a0 += s * mcol[j]; }
;                 mcol[i] = a0 + a1; }
	v_readlane_b32 s98, v2, 17
	v_fmac_f32_e32 v66, s100, v38
	v_readlane_b32 s99, v2, 18
	v_fmac_f32_e32 v65, s0, v39
	v_readlane_b32 s100, v2, 19
	v_fmac_f32_e32 v66, s98, v40
	v_readlane_b32 s0, v2, 20
	v_fmac_f32_e32 v65, s99, v42
	v_readlane_b32 s98, v2, 21
	v_fmac_f32_e32 v66, s100, v43
	v_readlane_b32 s99, v2, 22
	v_fmac_f32_e32 v65, s0, v45
	v_readlane_b32 s100, v2, 23
	v_fmac_f32_e32 v66, s98, v46
	v_readlane_b32 s0, v2, 24
	v_fmac_f32_e32 v65, s99, v47
	v_readlane_b32 s98, v2, 25
	v_fmac_f32_e32 v66, s100, v49
	v_readlane_b32 s99, v2, 26
	v_fmac_f32_e32 v65, s0, v51
	v_readlane_b32 s100, v2, 27
	v_fmac_f32_e32 v66, s98, v52
	v_readlane_b32 s0, v2, 28
	v_fmac_f32_e32 v65, s99, v54
	v_readlane_b32 s98, v2, 29
	v_fmac_f32_e32 v66, s100, v56
	v_readlane_b32 s99, v2, 30
	v_fmac_f32_e32 v65, s0, v57
	v_readlane_b32 s100, v2, 31
	v_fmac_f32_e32 v66, s98, v59
	v_readlane_b32 s0, v2, 32
	v_fmac_f32_e32 v65, s99, v61
	v_readlane_b32 s98, v2, 33
	v_fmac_f32_e32 v66, s100, v63
	v_readlane_b32 s99, v2, 34
	v_fmac_f32_e32 v65, s0, v64
	v_readlane_b32 s100, v2, 35
	v_fmac_f32_e32 v66, s98, v62
	v_readlane_b32 s0, v2, 36
	v_fmac_f32_e32 v65, s99, v60
	v_readlane_b32 s98, v2, 37
	v_fmac_f32_e32 v66, s100, v58
	v_readlane_b32 s99, v2, 38
	v_fmac_f32_e32 v65, s0, v55
	v_readlane_b32 s100, v2, 39
	v_fmac_f32_e32 v66, s98, v53
	v_readlane_b32 s0, v2, 40
	v_fmac_f32_e32 v65, s99, v50
	v_readlane_b32 s98, v2, 41
	v_fmac_f32_e32 v66, s100, v48
	v_readlane_b32 s99, v2, 42
	v_fmac_f32_e32 v65, s0, v44
	v_readlane_b32 s100, v2, 43
	v_fmac_f32_e32 v66, s98, v41
	v_readlane_b32 s0, v2, 44
	v_fmac_f32_e32 v65, s99, v37
	v_readlane_b32 s98, v2, 45
	v_fmac_f32_e32 v66, s100, v30
	v_readlane_b32 s99, v2, 46
	v_fmac_f32_e32 v65, s0, v21
	v_readlane_b32 s100, v2, 47
	v_fmac_f32_e32 v66, s98, v20
	v_readlane_b32 s0, v2, 48
	v_fmac_f32_e32 v65, s99, v19
	v_readlane_b32 s98, v2, 49
	v_fmac_f32_e32 v66, s100, v18
	v_readlane_b32 s99, v2, 50
	v_fmac_f32_e32 v65, s0, v17
	v_readlane_b32 s100, v2, 51
	v_fmac_f32_e32 v66, s98, v16
	v_readlane_b32 s0, v2, 52
	v_fmac_f32_e32 v65, s99, v15
	v_readlane_b32 s98, v2, 53
	v_fmac_f32_e32 v66, s100, v14
	v_readlane_b32 s99, v2, 54
	v_fmac_f32_e32 v65, s0, v12
	v_readlane_b32 s100, v2, 55
	v_fmac_f32_e32 v66, s98, v11
	v_readlane_b32 s0, v2, 56
	v_fmac_f32_e32 v65, s99, v10
	v_readlane_b32 s98, v2, 57
	v_fmac_f32_e32 v66, s100, v9
	v_readlane_b32 s99, v2, 58
	v_fmac_f32_e32 v65, s0, v8
	v_readlane_b32 s100, v2, 59
	v_fmac_f32_e32 v66, s98, v7
	v_readlane_b32 s0, v2, 60
	v_fmac_f32_e32 v65, s99, v6
	v_readlane_b32 s98, v2, 61
	v_fmac_f32_e32 v66, s100, v13
	v_readlane_b32 s99, v29, 0
	v_fmac_f32_e32 v65, s0, v4
	v_readlane_b32 s100, v29, 1
	v_fmac_f32_e32 v66, s98, v3
	v_add_f32_e32 v2, v65, v66
	v_readlane_b32 s0, v29, 2
	v_fma_f32 v65, 0, s99, v29
	v_readlane_b32 s98, v29, 3
	v_fma_f32 v66, v27, s100, 0
	v_readlane_b32 s99, v29, 4
	v_fmac_f32_e32 v65, s0, v25
	v_readlane_b32 s100, v29, 5
	v_fmac_f32_e32 v66, s98, v23
	v_readlane_b32 s0, v29, 6
	v_fmac_f32_e32 v65, s99, v5
	v_readlane_b32 s98, v29, 7
	v_fmac_f32_e32 v66, s100, v22
	v_readlane_b32 s99, v29, 8
	v_fmac_f32_e32 v65, s0, v24
	v_readlane_b32 s100, v29, 9
	v_fmac_f32_e32 v66, s98, v26
	v_readlane_b32 s0, v29, 10
	v_fmac_f32_e32 v65, s99, v28
	v_readlane_b32 s98, v29, 11
	v_fmac_f32_e32 v66, s100, v31
	v_readlane_b32 s99, v29, 12
	v_fmac_f32_e32 v65, s0, v32
	v_readlane_b32 s100, v29, 13
	v_fmac_f32_e32 v66, s98, v33
	v_readlane_b32 s0, v29, 14
	v_fmac_f32_e32 v65, s99, v34
	v_readlane_b32 s98, v29, 15
	v_fmac_f32_e32 v66, s100, v35
	v_readlane_b32 s99, v29, 16
	v_fmac_f32_e32 v65, s0, v36
	v_readlane_b32 s100, v29, 17
	v_fmac_f32_e32 v66, s98, v38
	v_readlane_b32 s0, v29, 18
	v_fmac_f32_e32 v65, s99, v39
	v_readlane_b32 s98, v29, 19
	v_fmac_f32_e32 v66, s100, v40
	v_readlane_b32 s99, v29, 20
	v_fmac_f32_e32 v65, s0, v42
	v_readlane_b32 s100, v29, 21
	v_fmac_f32_e32 v66, s98, v43
	v_readlane_b32 s0, v29, 22
	v_fmac_f32_e32 v65, s99, v45
	v_readlane_b32 s98, v29, 23
	v_fmac_f32_e32 v66, s100, v46
	v_readlane_b32 s99, v29, 24
	v_fmac_f32_e32 v65, s0, v47
	v_readlane_b32 s100, v29, 25
	v_fmac_f32_e32 v66, s98, v49
	v_readlane_b32 s0, v29, 26
	v_fmac_f32_e32 v65, s99, v51
	v_readlane_b32 s98, v29, 27
	v_fmac_f32_e32 v66, s100, v52
	v_readlane_b32 s99, v29, 28
	v_fmac_f32_e32 v65, s0, v54
	v_readlane_b32 s100, v29, 29
	v_fmac_f32_e32 v66, s98, v56
	v_readlane_b32 s0, v29, 30
	v_fmac_f32_e32 v65, s99, v57
	v_readlane_b32 s98, v29, 31
	v_fmac_f32_e32 v66, s100, v59
	v_readlane_b32 s99, v29, 32
	v_fmac_f32_e32 v65, s0, v61
	v_readlane_b32 s100, v29, 33
	v_fmac_f32_e32 v66, s98, v63
	v_readlane_b32 s0, v29, 34
	v_fmac_f32_e32 v65, s99, v64
	v_readlane_b32 s98, v29, 35
	v_fmac_f32_e32 v66, s100, v62
	v_readlane_b32 s99, v29, 36
	v_fmac_f32_e32 v65, s0, v60
	v_readlane_b32 s100, v29, 37
	v_fmac_f32_e32 v66, s98, v58
	v_readlane_b32 s0, v29, 38
	v_fmac_f32_e32 v65, s99, v55
	v_readlane_b32 s98, v29, 39
	v_fmac_f32_e32 v66, s100, v53
	v_readlane_b32 s99, v29, 40
	v_fmac_f32_e32 v65, s0, v50
	v_readlane_b32 s100, v29, 41
	v_fmac_f32_e32 v66, s98, v48
	v_readlane_b32 s0, v29, 42
	v_fmac_f32_e32 v65, s99, v44
	v_readlane_b32 s98, v29, 43
	v_fmac_f32_e32 v66, s100, v41
	v_readlane_b32 s99, v29, 44
	v_fmac_f32_e32 v65, s0, v37
	v_readlane_b32 s100, v29, 45
	v_fmac_f32_e32 v66, s98, v30
	v_readlane_b32 s0, v29, 46
	v_fmac_f32_e32 v65, s99, v21
	v_readlane_b32 s98, v29, 47
	v_fmac_f32_e32 v66, s100, v20
	v_readlane_b32 s99, v29, 48
	v_fmac_f32_e32 v65, s0, v19
	v_readlane_b32 s100, v29, 49
	v_fmac_f32_e32 v66, s98, v18
	v_readlane_b32 s0, v29, 50
	v_fmac_f32_e32 v65, s99, v17
; #define LAS __attribute__((address_space(3)))
; __device__ __forceinline__ unsigned cvt_pk_bf16(float lo, float hi) { const f32x2 v = {lo, hi}; return __builtin_bit_cast(unsigned, __builtin_convertvector(v, bf16x2_t)); }
; __device__ __forceinline__ int otid() { int t = threadIdx.x; asm volatile("" : "+v"(t)); return t; }
; __device__ __forceinline__ void ph_gdn_prep(const Params& p, LAS unsigned char* lds) {
;     ...
;             for (int i = 1; i < 64; ++i) { const int mi = __float_as_int(mcol[i]); float a0 = mcol[i], a1 = 0.f;
; #pragma unroll
;                 for (int j = 0; j < i; ++j) { const float s = __int_as_float(__builtin_amdgcn_readlane(mi, j)); if (j & 1) a1 += s * mcol[j]; else a0 += s * mcol[j]; }
;                 mcol[i] = a0 + a1; }
;             LAS unsigned char* TMh = TM + wid * 8192; const int lane = otid() & 63;
; #pragma unroll
;             for (int i = 0; i < 64; ++i) { const float v = (i > lane) ? mcol[i] : (i == lane ? 1.0f : 0.f); *(LAS bf16_t*)(TMh + img128(i, lane)) = (bf16_t)(cvt_pk_bf16(v, 0.f) & 0xffffu); }
	v_readlane_b32 s98, v29, 51
	v_fmac_f32_e32 v66, s100, v16
	v_readlane_b32 s99, v29, 52
	v_fmac_f32_e32 v65, s0, v15
	v_readlane_b32 s100, v29, 53
	v_fmac_f32_e32 v66, s98, v14
	v_readlane_b32 s0, v29, 54
	v_fmac_f32_e32 v65, s99, v12
	v_readlane_b32 s98, v29, 55
	v_fmac_f32_e32 v66, s100, v11
	v_readlane_b32 s99, v29, 56
	v_fmac_f32_e32 v65, s0, v10
	v_readlane_b32 s100, v29, 57
	v_fmac_f32_e32 v66, s98, v9
	v_readlane_b32 s0, v29, 58
	v_fmac_f32_e32 v65, s99, v8
	v_readlane_b32 s98, v29, 59
	v_fmac_f32_e32 v66, s100, v7
	v_readlane_b32 s99, v29, 60
	v_fmac_f32_e32 v65, s0, v6
	v_readlane_b32 s100, v29, 61
	v_fmac_f32_e32 v66, s98, v13
	v_readlane_b32 s0, v29, 62
	v_fmac_f32_e32 v65, s99, v4
	v_fmac_f32_e32 v66, s100, v3
	v_fmac_f32_e32 v65, s0, v2
	v_add_f32_e32 v29, v66, v65
	v_mov_b32_e32 v65, v0
	s_nop 0
	v_and_b32_e32 v65, 63, v65
	v_lshlrev_b32_e32 v67, 1, v65
	v_and_b32_e32 v68, 14, v67
	v_cmp_eq_u32_e32 vcc, 0, v65
	v_and_b32_e32 v66, 0x70, v67
	v_add3_u32 v66, s77, v66, v68
	v_cndmask_b32_e32 v69, 0, v142, vcc
	v_cmp_eq_u32_e64 s[8:9], 1, v65
	ds_write_b16 v66, v69 offset:4096
	s_nop 0
	v_cndmask_b32_e64 v69, 0, 1.0, s[8:9]
	v_cndmask_b32_e32 v27, v69, v27, vcc
	v_cvt_pk_bf16_f32 v27, v27, s0
	v_cmp_eq_u32_e64 s[8:9], 2, v65
	ds_write_b16 v66, v27 offset:4224
	v_cmp_gt_u32_e32 vcc, 2, v65
	v_cndmask_b32_e64 v27, 0, 1.0, s[8:9]
	v_cmp_eq_u32_e64 s[8:9], 3, v65
	v_cndmask_b32_e32 v25, v27, v25, vcc
	v_cvt_pk_bf16_f32 v27, v25, s0
	v_bitop3_b32 v25, v67, 16, v143 bitop3:0x6c
	v_add3_u32 v25, s77, v25, v68
	ds_write_b16 v25, v27 offset:4352
	v_cmp_gt_u32_e32 vcc, 3, v65
	v_cndmask_b32_e64 v27, 0, 1.0, s[8:9]
	v_cmp_eq_u32_e64 s[8:9], 4, v65
	v_cndmask_b32_e32 v23, v27, v23, vcc
	v_cvt_pk_bf16_f32 v23, v23, s0
	ds_write_b16 v25, v23 offset:4480
	v_cmp_gt_u32_e32 vcc, 4, v65
	v_cndmask_b32_e64 v23, 0, 1.0, s[8:9]
	v_cmp_eq_u32_e64 s[8:9], 5, v65
	v_cndmask_b32_e32 v5, v23, v5, vcc
	v_cvt_pk_bf16_f32 v23, v5, s0
	v_bitop3_b32 v5, v67, 32, v143 bitop3:0x6c
	v_add3_u32 v5, s77, v5, v68
	ds_write_b16 v5, v23 offset:4608
	v_cmp_gt_u32_e32 vcc, 5, v65
	v_cndmask_b32_e64 v23, 0, 1.0, s[8:9]
	v_cmp_eq_u32_e64 s[8:9], 6, v65
	v_cndmask_b32_e32 v22, v23, v22, vcc
	v_cvt_pk_bf16_f32 v22, v22, s0
	ds_write_b16 v5, v22 offset:4736
	v_cmp_gt_u32_e32 vcc, 6, v65
	v_cndmask_b32_e64 v22, 0, 1.0, s[8:9]
	v_cmp_eq_u32_e64 s[8:9], 7, v65
	v_cndmask_b32_e32 v22, v22, v24, vcc
	v_cvt_pk_bf16_f32 v23, v22, s0
	v_bitop3_b32 v22, v67, 48, v143 bitop3:0x6c
	v_add3_u32 v22, s77, v22, v68
	ds_write_b16 v22, v23 offset:4864
	v_cmp_gt_u32_e32 vcc, 7, v65
	v_cndmask_b32_e64 v23, 0, 1.0, s[8:9]
	v_cmp_eq_u32_e64 s[8:9], 8, v65
	v_cndmask_b32_e32 v23, v23, v26, vcc
	v_cvt_pk_bf16_f32 v23, v23, s0
	ds_write_b16 v22, v23 offset:4992
	v_cmp_gt_u32_e32 vcc, 8, v65
	v_cndmask_b32_e64 v23, 0, 1.0, s[8:9]
	v_cmp_eq_u32_e64 s[8:9], 9, v65
	v_cndmask_b32_e32 v23, v23, v28, vcc
	v_cvt_pk_bf16_f32 v24, v23, s0
	v_bitop3_b32 v23, v67, 64, v143 bitop3:0x6c
	v_add3_u32 v23, s77, v23, v68
	ds_write_b16 v23, v24 offset:5120
	v_cmp_gt_u32_e32 vcc, 9, v65
	v_cndmask_b32_e64 v24, 0, 1.0, s[8:9]
	v_cmp_eq_u32_e64 s[8:9], 10, v65
	v_cndmask_b32_e32 v24, v24, v31, vcc
	v_cvt_pk_bf16_f32 v24, v24, s0
	ds_write_b16 v23, v24 offset:5248
	v_cmp_gt_u32_e32 vcc, 10, v65
	v_cndmask_b32_e64 v24, 0, 1.0, s[8:9]
	v_cmp_eq_u32_e64 s[8:9], 11, v65
	v_cndmask_b32_e32 v24, v24, v32, vcc
	v_cvt_pk_bf16_f32 v26, v24, s0
	v_bitop3_b32 v24, v67, s91, v143 bitop3:0x6c
	v_add3_u32 v24, s77, v24, v68
	ds_write_b16 v24, v26 offset:5376
	v_cmp_gt_u32_e32 vcc, 11, v65
	v_cndmask_b32_e64 v26, 0, 1.0, s[8:9]
	v_cmp_eq_u32_e64 s[8:9], 12, v65
	v_cndmask_b32_e32 v26, v26, v33, vcc
	v_cvt_pk_bf16_f32 v26, v26, s0
	ds_write_b16 v24, v26 offset:5504
	v_cmp_gt_u32_e32 vcc, 12, v65
	v_cndmask_b32_e64 v26, 0, 1.0, s[8:9]
	v_cmp_eq_u32_e64 s[8:9], 13, v65
	v_cndmask_b32_e32 v26, v26, v34, vcc
	v_cvt_pk_bf16_f32 v27, v26, s0
	v_bitop3_b32 v26, v67, s96, v143 bitop3:0x6c
	v_add3_u32 v26, s77, v26, v68
	ds_write_b16 v26, v27 offset:5632
	v_cmp_gt_u32_e32 vcc, 13, v65
	v_cndmask_b32_e64 v27, 0, 1.0, s[8:9]
	v_cmp_eq_u32_e64 s[8:9], 14, v65
	v_cndmask_b32_e32 v27, v27, v35, vcc
	v_cvt_pk_bf16_f32 v27, v27, s0
	ds_write_b16 v26, v27 offset:5760
	v_cmp_gt_u32_e32 vcc, 14, v65
	v_cndmask_b32_e64 v27, 0, 1.0, s[8:9]
	v_cmp_eq_u32_e64 s[8:9], 15, v65
	v_cndmask_b32_e32 v27, v27, v36, vcc
	v_cvt_pk_bf16_f32 v28, v27, s0
	v_bitop3_b32 v27, v67, s81, v67 bitop3:0xc
	v_add3_u32 v27, s77, v27, v68
	ds_write_b16 v27, v28 offset:5888
	v_cmp_gt_u32_e32 vcc, 15, v65
	v_cndmask_b32_e64 v28, 0, 1.0, s[8:9]
	v_cmp_eq_u32_e64 s[8:9], 16, v65
	v_cndmask_b32_e32 v28, v28, v38, vcc
	v_cvt_pk_bf16_f32 v28, v28, s0
	ds_write_b16 v27, v28 offset:6016
	v_cmp_gt_u32_e32 vcc, 16, v65
	v_cndmask_b32_e64 v28, 0, 1.0, s[8:9]
	v_cmp_eq_u32_e64 s[8:9], 17, v65
	v_cndmask_b32_e32 v28, v28, v39, vcc
	v_cvt_pk_bf16_f32 v28, v28, s0
	ds_write_b16 v66, v28 offset:6144
	v_cmp_gt_u32_e32 vcc, 17, v65
	v_cndmask_b32_e64 v28, 0, 1.0, s[8:9]
	v_cmp_eq_u32_e64 s[8:9], 18, v65
	v_cndmask_b32_e32 v28, v28, v40, vcc
	v_cvt_pk_bf16_f32 v28, v28, s0
	ds_write_b16 v66, v28 offset:6272
	v_cmp_gt_u32_e32 vcc, 18, v65
	v_cndmask_b32_e64 v28, 0, 1.0, s[8:9]
	v_cmp_eq_u32_e64 s[8:9], 19, v65
	v_cndmask_b32_e32 v28, v28, v42, vcc
	v_cvt_pk_bf16_f32 v28, v28, s0
	ds_write_b16 v25, v28 offset:6400
	v_cmp_gt_u32_e32 vcc, 19, v65
	v_cndmask_b32_e64 v28, 0, 1.0, s[8:9]
	v_cmp_eq_u32_e64 s[8:9], 20, v65
	v_cndmask_b32_e32 v28, v28, v43, vcc
	v_cvt_pk_bf16_f32 v28, v28, s0
	ds_write_b16 v25, v28 offset:6528
	v_cmp_gt_u32_e32 vcc, 20, v65
	v_cndmask_b32_e64 v28, 0, 1.0, s[8:9]
; #define LAS __attribute__((address_space(3)))
; __device__ __forceinline__ unsigned cvt_pk_bf16(float lo, float hi) { const f32x2 v = {lo, hi}; return __builtin_bit_cast(unsigned, __builtin_convertvector(v, bf16x2_t)); }
; __device__ __forceinline__ int otid() { int t = threadIdx.x; asm volatile("" : "+v"(t)); return t; }
; __device__ __forceinline__ void ph_gdn_prep(const Params& p, LAS unsigned char* lds) {
;     ...
;             LAS unsigned char* TMh = TM + wid * 8192; const int lane = otid() & 63;
; #pragma unroll
;             for (int i = 0; i < 64; ++i) { const float v = (i > lane) ? mcol[i] : (i == lane ? 1.0f : 0.f); *(LAS bf16_t*)(TMh + img128(i, lane)) = (bf16_t)(cvt_pk_bf16(v, 0.f) & 0xffffu); }
	v_cmp_eq_u32_e64 s[8:9], 21, v65
	v_cndmask_b32_e32 v28, v28, v45, vcc
	v_cvt_pk_bf16_f32 v28, v28, s0
	ds_write_b16 v5, v28 offset:6656
	v_cmp_gt_u32_e32 vcc, 21, v65
	v_cndmask_b32_e64 v28, 0, 1.0, s[8:9]
	v_cmp_eq_u32_e64 s[8:9], 22, v65
	v_cndmask_b32_e32 v28, v28, v46, vcc
	v_cvt_pk_bf16_f32 v28, v28, s0
	ds_write_b16 v5, v28 offset:6784
	v_cmp_gt_u32_e32 vcc, 22, v65
	v_cndmask_b32_e64 v28, 0, 1.0, s[8:9]
	v_cmp_eq_u32_e64 s[8:9], 23, v65
	v_cndmask_b32_e32 v28, v28, v47, vcc
	v_cvt_pk_bf16_f32 v28, v28, s0
	ds_write_b16 v22, v28 offset:6912
	v_cmp_gt_u32_e32 vcc, 23, v65
	v_cndmask_b32_e64 v28, 0, 1.0, s[8:9]
	v_cmp_eq_u32_e64 s[8:9], 24, v65
	v_cndmask_b32_e32 v28, v28, v49, vcc
	v_cvt_pk_bf16_f32 v28, v28, s0
	ds_write_b16 v22, v28 offset:7040
	v_cmp_gt_u32_e32 vcc, 24, v65
	v_cndmask_b32_e64 v28, 0, 1.0, s[8:9]
	v_cmp_eq_u32_e64 s[8:9], 25, v65
	v_cndmask_b32_e32 v28, v28, v51, vcc
	v_cvt_pk_bf16_f32 v28, v28, s0
	ds_write_b16 v23, v28 offset:7168
	v_cmp_gt_u32_e32 vcc, 25, v65
	v_cndmask_b32_e64 v28, 0, 1.0, s[8:9]
	v_cmp_eq_u32_e64 s[8:9], 26, v65
	v_cndmask_b32_e32 v28, v28, v52, vcc
	v_cvt_pk_bf16_f32 v28, v28, s0
	ds_write_b16 v23, v28 offset:7296
	v_cmp_gt_u32_e32 vcc, 26, v65
	v_cndmask_b32_e64 v28, 0, 1.0, s[8:9]
	v_cmp_eq_u32_e64 s[8:9], 27, v65
	v_cndmask_b32_e32 v28, v28, v54, vcc
	v_cvt_pk_bf16_f32 v28, v28, s0
	ds_write_b16 v24, v28 offset:7424
	v_cmp_gt_u32_e32 vcc, 27, v65
	v_cndmask_b32_e64 v28, 0, 1.0, s[8:9]
	v_cmp_eq_u32_e64 s[8:9], 28, v65
	v_cndmask_b32_e32 v28, v28, v56, vcc
	v_cvt_pk_bf16_f32 v28, v28, s0
	ds_write_b16 v24, v28 offset:7552
	v_cmp_gt_u32_e32 vcc, 28, v65
	v_cndmask_b32_e64 v28, 0, 1.0, s[8:9]
	v_cmp_eq_u32_e64 s[8:9], 29, v65
	v_cndmask_b32_e32 v28, v28, v57, vcc
	v_cvt_pk_bf16_f32 v28, v28, s0
	ds_write_b16 v26, v28 offset:7680
	v_cmp_gt_u32_e32 vcc, 29, v65
	v_cndmask_b32_e64 v28, 0, 1.0, s[8:9]
	v_cmp_eq_u32_e64 s[8:9], 30, v65
	v_cndmask_b32_e32 v28, v28, v59, vcc
	v_cvt_pk_bf16_f32 v28, v28, s0
	ds_write_b16 v26, v28 offset:7808
	v_cmp_gt_u32_e32 vcc, 30, v65
	v_cndmask_b32_e64 v28, 0, 1.0, s[8:9]
	v_cmp_eq_u32_e64 s[8:9], 31, v65
	v_cndmask_b32_e32 v28, v28, v61, vcc
	v_cvt_pk_bf16_f32 v28, v28, s0
	ds_write_b16 v27, v28 offset:7936
	v_cmp_gt_u32_e32 vcc, 31, v65
	v_cndmask_b32_e64 v28, 0, 1.0, s[8:9]
	v_cmp_eq_u32_e64 s[8:9], 32, v65
	v_cndmask_b32_e32 v28, v28, v63, vcc
	v_cvt_pk_bf16_f32 v28, v28, s0
	ds_write_b16 v27, v28 offset:8064
	v_cmp_gt_u32_e32 vcc, 32, v65
	v_cndmask_b32_e64 v28, 0, 1.0, s[8:9]
	v_cmp_eq_u32_e64 s[8:9], 33, v65
	v_cndmask_b32_e32 v28, v28, v64, vcc
	v_cvt_pk_bf16_f32 v28, v28, s0
	ds_write_b16 v66, v28 offset:8192
	v_cmp_gt_u32_e32 vcc, 33, v65
	v_cndmask_b32_e64 v28, 0, 1.0, s[8:9]
	v_cmp_eq_u32_e64 s[8:9], 34, v65
	v_cndmask_b32_e32 v28, v28, v62, vcc
	v_cvt_pk_bf16_f32 v28, v28, s0
	ds_write_b16 v66, v28 offset:8320
	v_cmp_gt_u32_e32 vcc, 34, v65
	v_cndmask_b32_e64 v28, 0, 1.0, s[8:9]
	v_cmp_eq_u32_e64 s[8:9], 35, v65
	v_cndmask_b32_e32 v28, v28, v60, vcc
	v_cvt_pk_bf16_f32 v28, v28, s0
	ds_write_b16 v25, v28 offset:8448
	v_cmp_gt_u32_e32 vcc, 35, v65
	v_cndmask_b32_e64 v28, 0, 1.0, s[8:9]
	v_cmp_eq_u32_e64 s[8:9], 36, v65
	v_cndmask_b32_e32 v28, v28, v58, vcc
	v_cvt_pk_bf16_f32 v28, v28, s0
	ds_write_b16 v25, v28 offset:8576
	v_cmp_gt_u32_e32 vcc, 36, v65
	v_cndmask_b32_e64 v28, 0, 1.0, s[8:9]
	v_cmp_eq_u32_e64 s[8:9], 37, v65
	v_cndmask_b32_e32 v28, v28, v55, vcc
	v_cvt_pk_bf16_f32 v28, v28, s0
	ds_write_b16 v5, v28 offset:8704
	v_cmp_gt_u32_e32 vcc, 37, v65
	v_cndmask_b32_e64 v28, 0, 1.0, s[8:9]
	v_cmp_eq_u32_e64 s[8:9], 38, v65
	v_cndmask_b32_e32 v28, v28, v53, vcc
	v_cvt_pk_bf16_f32 v28, v28, s0
	ds_write_b16 v5, v28 offset:8832
	v_cmp_gt_u32_e32 vcc, 38, v65
	v_cndmask_b32_e64 v28, 0, 1.0, s[8:9]
	v_cmp_eq_u32_e64 s[8:9], 39, v65
	v_cndmask_b32_e32 v28, v28, v50, vcc
	v_cvt_pk_bf16_f32 v28, v28, s0
	ds_write_b16 v22, v28 offset:8960
	v_cmp_gt_u32_e32 vcc, 39, v65
	v_cndmask_b32_e64 v28, 0, 1.0, s[8:9]
	v_cmp_eq_u32_e64 s[8:9], 40, v65
	v_cndmask_b32_e32 v28, v28, v48, vcc
	v_cvt_pk_bf16_f32 v28, v28, s0
	ds_write_b16 v22, v28 offset:9088
	v_cmp_gt_u32_e32 vcc, 40, v65
	v_cndmask_b32_e64 v28, 0, 1.0, s[8:9]
	v_cmp_eq_u32_e64 s[8:9], 41, v65
	v_cndmask_b32_e32 v28, v28, v44, vcc
	v_cvt_pk_bf16_f32 v28, v28, s0
	ds_write_b16 v23, v28 offset:9216
	v_cmp_gt_u32_e32 vcc, 41, v65
	v_cndmask_b32_e64 v28, 0, 1.0, s[8:9]
	v_cmp_eq_u32_e64 s[8:9], 42, v65
	v_cndmask_b32_e32 v28, v28, v41, vcc
	v_cvt_pk_bf16_f32 v28, v28, s0
	ds_write_b16 v23, v28 offset:9344
	v_cmp_gt_u32_e32 vcc, 42, v65
	v_cndmask_b32_e64 v28, 0, 1.0, s[8:9]
	v_cmp_eq_u32_e64 s[8:9], 43, v65
	v_cndmask_b32_e32 v28, v28, v37, vcc
	v_cvt_pk_bf16_f32 v28, v28, s0
	ds_write_b16 v24, v28 offset:9472
	v_cmp_gt_u32_e32 vcc, 43, v65
	v_cndmask_b32_e64 v28, 0, 1.0, s[8:9]
	v_cmp_eq_u32_e64 s[8:9], 44, v65
	v_cndmask_b32_e32 v28, v28, v30, vcc
	v_cvt_pk_bf16_f32 v28, v28, s0
	ds_write_b16 v24, v28 offset:9600
	v_cmp_gt_u32_e32 vcc, 44, v65
	v_cndmask_b32_e64 v28, 0, 1.0, s[8:9]
; #define LAS __attribute__((address_space(3)))
; __device__ __forceinline__ unsigned cvt_pk_bf16(float lo, float hi) { const f32x2 v = {lo, hi}; return __builtin_bit_cast(unsigned, __builtin_convertvector(v, bf16x2_t)); }
; __device__ __forceinline__ int otid() { int t = threadIdx.x; asm volatile("" : "+v"(t)); return t; }
; __device__ __forceinline__ void ph_gdn_prep(const Params& p, LAS unsigned char* lds) {
;     ...
;             LAS unsigned char* TMh = TM + wid * 8192; const int lane = otid() & 63;
; #pragma unroll
;             for (int i = 0; i < 64; ++i) { const float v = (i > lane) ? mcol[i] : (i == lane ? 1.0f : 0.f); *(LAS bf16_t*)(TMh + img128(i, lane)) = (bf16_t)(cvt_pk_bf16(v, 0.f) & 0xffffu); }
;         }
;         __syncthreads();
;         u32x4 va, vb, ka, kb, qa, qb;
;         { const int tidC = otid(), jrow = tidC >> 3, part = tidC & 7; const bf16_t* rowp = qkvc + (t0 + jrow) * DM;
;             va = *(const u32x4*)(rowp + 1024 + part * 16); vb = *(const u32x4*)(rowp + 1024 + part * 16 + 8);
;             ka = *(const u32x4*)(rowp + 512 + part * 16); kb = *(const u32x4*)(rowp + 512 + part * 16 + 8);
;             qa = *(const u32x4*)(rowp + part * 16); qb = *(const u32x4*)(rowp + part * 16 + 8); }
	v_cmp_eq_u32_e64 s[8:9], 45, v65
	v_cndmask_b32_e32 v21, v28, v21, vcc
	v_cvt_pk_bf16_f32 v21, v21, s0
	ds_write_b16 v26, v21 offset:9728
	v_cmp_gt_u32_e32 vcc, 45, v65
	v_cndmask_b32_e64 v21, 0, 1.0, s[8:9]
	v_cmp_eq_u32_e64 s[8:9], 46, v65
	v_cndmask_b32_e32 v20, v21, v20, vcc
	v_cvt_pk_bf16_f32 v20, v20, s0
	ds_write_b16 v26, v20 offset:9856
	v_cmp_gt_u32_e32 vcc, 46, v65
	v_cndmask_b32_e64 v20, 0, 1.0, s[8:9]
	v_cmp_eq_u32_e64 s[8:9], 47, v65
	v_cndmask_b32_e32 v19, v20, v19, vcc
	v_cvt_pk_bf16_f32 v19, v19, s0
	ds_write_b16 v27, v19 offset:9984
	v_cmp_gt_u32_e32 vcc, 47, v65
	v_cndmask_b32_e64 v19, 0, 1.0, s[8:9]
	v_cmp_eq_u32_e64 s[8:9], 48, v65
	v_cndmask_b32_e32 v18, v19, v18, vcc
	v_cvt_pk_bf16_f32 v18, v18, s0
	ds_write_b16 v27, v18 offset:10112
	v_cmp_gt_u32_e32 vcc, 48, v65
	v_cndmask_b32_e64 v18, 0, 1.0, s[8:9]
	v_cmp_eq_u32_e64 s[8:9], 49, v65
	v_cndmask_b32_e32 v17, v18, v17, vcc
	v_cvt_pk_bf16_f32 v17, v17, s0
	ds_write_b16 v66, v17 offset:10240
	v_cmp_gt_u32_e32 vcc, 49, v65
	v_cndmask_b32_e64 v17, 0, 1.0, s[8:9]
	v_cmp_eq_u32_e64 s[8:9], 50, v65
	v_cndmask_b32_e32 v16, v17, v16, vcc
	v_cvt_pk_bf16_f32 v16, v16, s0
	ds_write_b16 v66, v16 offset:10368
	v_cmp_gt_u32_e32 vcc, 50, v65
	v_cndmask_b32_e64 v16, 0, 1.0, s[8:9]
	v_cmp_eq_u32_e64 s[8:9], 51, v65
	v_cndmask_b32_e32 v15, v16, v15, vcc
	v_cvt_pk_bf16_f32 v15, v15, s0
	ds_write_b16 v25, v15 offset:10496
	v_cmp_gt_u32_e32 vcc, 51, v65
	v_cndmask_b32_e64 v15, 0, 1.0, s[8:9]
	v_cmp_eq_u32_e64 s[8:9], 52, v65
	v_cndmask_b32_e32 v14, v15, v14, vcc
	v_cvt_pk_bf16_f32 v14, v14, s0
	ds_write_b16 v25, v14 offset:10624
	v_cmp_gt_u32_e32 vcc, 52, v65
	v_cndmask_b32_e64 v14, 0, 1.0, s[8:9]
	v_cmp_eq_u32_e64 s[8:9], 53, v65
	v_cndmask_b32_e32 v12, v14, v12, vcc
	v_cvt_pk_bf16_f32 v12, v12, s0
	ds_write_b16 v5, v12 offset:10752
	v_cmp_gt_u32_e32 vcc, 53, v65
	v_cndmask_b32_e64 v12, 0, 1.0, s[8:9]
	v_cmp_eq_u32_e64 s[8:9], 54, v65
	v_cndmask_b32_e32 v11, v12, v11, vcc
	v_cvt_pk_bf16_f32 v11, v11, s0
	ds_write_b16 v5, v11 offset:10880
	v_cmp_gt_u32_e32 vcc, 54, v65
	v_cndmask_b32_e64 v5, 0, 1.0, s[8:9]
	v_cmp_eq_u32_e64 s[8:9], 55, v65
	v_cndmask_b32_e32 v5, v5, v10, vcc
	v_cvt_pk_bf16_f32 v5, v5, s0
	ds_write_b16 v22, v5 offset:11008
	v_cmp_gt_u32_e32 vcc, 55, v65
	v_cndmask_b32_e64 v5, 0, 1.0, s[8:9]
	v_cmp_eq_u32_e64 s[8:9], 56, v65
	v_cndmask_b32_e32 v5, v5, v9, vcc
	v_cvt_pk_bf16_f32 v5, v5, s0
	ds_write_b16 v22, v5 offset:11136
	v_cmp_gt_u32_e32 vcc, 56, v65
	v_cndmask_b32_e64 v5, 0, 1.0, s[8:9]
	v_cmp_eq_u32_e64 s[8:9], 57, v65
	v_cndmask_b32_e32 v5, v5, v8, vcc
	v_cvt_pk_bf16_f32 v5, v5, s0
	ds_write_b16 v23, v5 offset:11264
	v_cmp_gt_u32_e32 vcc, 57, v65
	v_cndmask_b32_e64 v5, 0, 1.0, s[8:9]
	v_cmp_eq_u32_e64 s[8:9], 58, v65
	v_cndmask_b32_e32 v5, v5, v7, vcc
	v_cvt_pk_bf16_f32 v5, v5, s0
	ds_write_b16 v23, v5 offset:11392
	v_cmp_gt_u32_e32 vcc, 58, v65
	v_cndmask_b32_e64 v5, 0, 1.0, s[8:9]
	v_cmp_eq_u32_e64 s[8:9], 59, v65
	v_cndmask_b32_e32 v5, v5, v6, vcc
	v_cvt_pk_bf16_f32 v5, v5, s0
	ds_write_b16 v24, v5 offset:11520
	v_cmp_gt_u32_e32 vcc, 59, v65
	v_cndmask_b32_e64 v5, 0, 1.0, s[8:9]
	v_cmp_eq_u32_e64 s[8:9], 60, v65
	v_cndmask_b32_e32 v5, v5, v13, vcc
	v_cvt_pk_bf16_f32 v5, v5, s0
	ds_write_b16 v24, v5 offset:11648
	v_cmp_gt_u32_e32 vcc, 60, v65
	v_cndmask_b32_e64 v5, 0, 1.0, s[8:9]
	v_cmp_eq_u32_e64 s[8:9], 61, v65
	v_cndmask_b32_e32 v4, v5, v4, vcc
	v_cvt_pk_bf16_f32 v4, v4, s0
	ds_write_b16 v26, v4 offset:11776
	v_cmp_gt_u32_e32 vcc, 61, v65
	v_cndmask_b32_e64 v4, 0, 1.0, s[8:9]
	v_cmp_eq_u32_e64 s[8:9], 62, v65
	v_cndmask_b32_e32 v3, v4, v3, vcc
	v_cvt_pk_bf16_f32 v3, v3, s0
	ds_write_b16 v26, v3 offset:11904
	v_cmp_gt_u32_e32 vcc, 62, v65
	v_cndmask_b32_e64 v3, 0, 1.0, s[8:9]
	v_mov_b32_e32 v4, v0
	v_cndmask_b32_e32 v2, v3, v2, vcc
	v_cvt_pk_bf16_f32 v2, v2, s0
	ds_write_b16 v27, v2 offset:12032
	v_cvt_pk_bf16_f32 v2, v29, s0
	v_cmp_ne_u32_e32 vcc, 63, v65
	s_lshl_b32 s0, s56, 2
	s_add_u32 s1, s2, s1
	v_cndmask_b32_e32 v2, v142, v2, vcc
	ds_write_b16 v27, v2 offset:12160
	s_waitcnt lgkmcnt(0)
	s_barrier
	v_readlane_b32 s2, v240, 13
	v_ashrrev_i32_e32 v2, 3, v4
	v_ashrrev_i32_e32 v3, 31, v2
	v_lshl_add_u64 v[2:3], s[58:59], 0, v[2:3]
	v_lshlrev_b64 v[2:3], 12, v[2:3]
	v_lshlrev_b32_e32 v4, 5, v4
	v_lshl_add_u64 v[2:3], s[60:61], 0, v[2:3]
	v_and_b32_e32 v122, 0xe0, v4
	v_lshl_add_u64 v[14:15], v[2:3], 0, v[122:123]
	global_load_dwordx4 v[10:13], v[14:15], off offset:2064
	global_load_dwordx4 v[22:25], v[14:15], off offset:2048
	global_load_dwordx4 v[2:5], v[14:15], off offset:1040
	global_load_dwordx4 v[6:9], v[14:15], off offset:1024
	global_load_dwordx4 v[18:21], v[14:15], off offset:16
	s_nop 0
	global_load_dwordx4 v[14:17], v[14:15], off
	s_mul_i32 s9, s56, 0x5000000
	s_addc_u32 s2, s2, 0
	s_or_b32 s9, s9, s10
	s_mul_hi_i32 s8, s71, 0xa00000
	s_add_u32 s33, s20, s9
	s_addc_u32 s68, s21, s8
	s_add_i32 s10, s3, s62
	s_lshl_b64 s[56:57], s[10:11], 18
	s_mov_b32 s10, 0
	s_mov_b64 s[58:59], s[22:23]
	s_mov_b64 s[60:61], s[22:23]
	s_branch .LBB0_224
